# baseline (speedup 1.0000x reference)
.LBB1_12:
	s_endpgm
	.p2alignl 8, 3212836864

_Z11gemm_kernelILi256ELi192ELi4ELi2ELi0EEvPKDF16_S1_PKfS3_PDF16_S4_S4_Pfi:
	s_lshl_b32 s3, s2, 1
	s_and_b32 s3, s3, 12
	s_bfe_u32 s12, s2, 0x20003
	s_load_dwordx8 s[4:11], s[0:1], 0x0
	s_or_b32 s17, s3, s12
	s_lshl_b32 s3, s2, 3
	s_and_b32 s3, s3, 8
	s_lshr_b32 s2, s2, 5
	s_add_i32 s2, s3, s2
	s_mulk_i32 s2, 0xc0
	s_mov_b32 s3, 0
	s_lshl_b64 s[12:13], s[2:3], 11
	s_lshl_b32 s14, s17, 19
	v_readfirstlane_b32 s16, v0
	s_waitcnt lgkmcnt(0)
	s_add_u32 s4, s4, s14
	v_lshlrev_b32_e32 v2, 4, v0
	s_addc_u32 s5, s5, 0
	s_bfe_i32 s18, s16, 0x10006
	v_and_b32_e32 v164, 0x70, v2
	v_lshlrev_b32_e32 v2, 8, v0
	s_and_b32 s19, s18, 0x60
	s_and_b32 s15, s18, 32
	v_lshlrev_b32_e32 v1, 7, v0
	v_mov_b32_e32 v165, 0
	v_and_b32_e32 v46, 0x1f800, v2
	s_mov_b32 s14, 0x1fc00
	v_mov_b32_e32 v2, 0x10000
	v_lshl_add_u64 v[10:11], s[4:5], 0, v[164:165]
	v_mov_b32_e32 v47, v165
	v_bitop3_b32 v2, v1, s14, v2 bitop3:0xc8
	s_mov_b32 s14, 0x3fc00
	v_mov_b32_e32 v12, 0x30000
	s_add_u32 s6, s6, s12
	v_lshl_add_u64 v[96:97], v[10:11], 0, v[46:47]
	v_lshlrev_b32_e32 v48, 1, v2
	v_mov_b32_e32 v49, v165
	v_or_b32_e32 v50, 0x40000, v46
	v_mov_b32_e32 v51, v165
	v_bitop3_b32 v1, v1, s14, v12 bitop3:0xc8
	s_addc_u32 s7, s7, s13
	v_lshl_add_u64 v[98:99], v[10:11], 0, v[48:49]
	global_load_dwordx4 v[2:5], v[96:97], off
	global_load_dwordx4 v[6:9], v[98:99], off
	v_lshl_add_u64 v[100:101], v[10:11], 0, v[50:51]
	v_lshlrev_b32_e32 v30, 1, v1
	v_mov_b32_e32 v31, v165
	v_lshl_add_u64 v[26:27], s[6:7], 0, v[164:165]
	v_lshl_add_u64 v[102:103], v[10:11], 0, v[30:31]
	global_load_dwordx4 v[10:13], v[100:101], off
	global_load_dwordx4 v[14:17], v[102:103], off
	v_lshl_add_u64 v[106:107], v[26:27], 0, v[46:47]
	v_lshl_add_u64 v[108:109], v[26:27], 0, v[48:49]
	global_load_dwordx4 v[18:21], v[106:107], off
	global_load_dwordx4 v[22:25], v[108:109], off
	v_lshl_add_u64 v[110:111], v[26:27], 0, v[50:51]
	global_load_dwordx4 v[26:29], v[110:111], off
	v_or_b32_e32 v32, 0x200, v0
	v_lshrrev_b32_e32 v65, 3, v32
	v_lshl_add_u64 v[32:33], s[4:5], 0, v[46:47]
	v_lshl_add_u64 v[30:31], s[4:5], 0, v[30:31]
	s_movk_i32 s20, 0x90
	v_lshrrev_b32_e32 v1, 3, v0
	v_add_u32_e32 v66, 0, v164
	v_lshl_add_u64 v[34:35], s[4:5], 0, v[48:49]
	v_lshl_add_u64 v[36:37], s[4:5], 0, v[50:51]
	v_lshl_add_u64 v[52:53], v[32:33], 0, v[164:165]
	v_lshl_add_u64 v[58:59], v[30:31], 0, v[164:165]
	v_lshl_add_u64 v[46:47], s[6:7], 0, v[46:47]
	v_or_b32_e32 v64, 0x600, v0
	v_mad_u32_u24 v114, v1, s20, v66
	v_lshl_add_u64 v[54:55], v[34:35], 0, v[164:165]
	v_lshl_add_u64 v[56:57], v[36:37], 0, v[164:165]
	global_load_dwordx4 v[30:33], v[52:53], off offset:128
	global_load_dwordx4 v[34:37], v[54:55], off offset:128
	global_load_dwordx4 v[38:41], v[56:57], off offset:128
	global_load_dwordx4 v[42:45], v[58:59], off offset:128
	v_lshl_add_u64 v[48:49], s[6:7], 0, v[48:49]
	v_lshl_add_u64 v[50:51], s[6:7], 0, v[50:51]
	v_lshl_add_u64 v[58:59], v[46:47], 0, v[164:165]
	v_mad_u32_u24 v115, v65, s20, v66
	v_lshl_add_u64 v[60:61], v[48:49], 0, v[164:165]
	v_lshl_add_u64 v[62:63], v[50:51], 0, v[164:165]
	global_load_dwordx4 v[46:49], v[58:59], off offset:128
	global_load_dwordx4 v[50:53], v[60:61], off offset:128
	global_load_dwordx4 v[54:57], v[62:63], off offset:128
	s_add_i32 s14, s19, s2
	s_lshr_b32 s2, s16, 1
	v_and_b32_e32 v166, 31, v0
	s_and_b32 s2, s2, 0x7fffffc0
	v_or_b32_e32 v168, s15, v166
	v_add_u32_e32 v118, 0x4800, v114
	v_or_b32_e32 v162, s19, v166
	v_lshrrev_b32_e32 v113, 1, v168
	s_waitcnt vmcnt(13)
	ds_write_b128 v114, v[2:5]
	s_waitcnt vmcnt(12)
	ds_write_b128 v115, v[6:9]
	s_waitcnt vmcnt(11)
	ds_write_b128 v114, v[10:13] offset:18432
	v_lshrrev_b32_e32 v2, 3, v64
	v_mad_u32_u24 v117, v2, s20, v66
	s_waitcnt vmcnt(10)
	ds_write_b128 v117, v[14:17]
	s_waitcnt vmcnt(9)
	ds_write_b128 v114, v[18:21] offset:36864
	s_waitcnt vmcnt(8)
	ds_write_b128 v115, v[22:25] offset:36864
	s_waitcnt vmcnt(7)
	ds_write_b128 v114, v[26:29] offset:55296
	s_waitcnt lgkmcnt(0)
	s_barrier
	global_load_dwordx4 v[122:125], v[96:97], off offset:256
	global_load_dwordx4 v[126:129], v[98:99], off offset:256
	global_load_dwordx4 v[130:133], v[100:101], off offset:256
	global_load_dwordx4 v[134:137], v[102:103], off offset:256
	global_load_dwordx4 v[138:141], v[106:107], off offset:256
	global_load_dwordx4 v[142:145], v[108:109], off offset:256
	global_load_dwordx4 v[146:149], v[110:111], off offset:256
	s_load_dwordx4 s[4:7], s[0:1], 0x20
	s_load_dwordx2 s[12:13], s[0:1], 0x30
	v_bfe_u32 v2, v0, 5, 1
	s_lshl_b32 s0, s17, 8
	s_add_i32 s1, 0, 0x18c00
	v_bitop3_b32 v3, s18, 32, v166 bitop3:0x26
	v_add_u32_e32 v5, s1, v164
	v_lshlrev_b32_e32 v121, 4, v2
	s_add_i32 s0, s2, s0
	v_lshlrev_b32_e32 v2, 2, v2
	v_and_b32_e32 v164, 1, v0
	v_or_b32_e32 v6, s2, v166
	v_add_u32_e32 v4, 0, v121
	v_or3_b32 v167, s0, v2, v164
	v_lshrrev_b32_e32 v112, 1, v3
	v_mad_u32_u24 v119, v1, s20, v5
	v_mad_u32_u24 v120, v65, s20, v5
	s_waitcnt vmcnt(13)
	ds_write_b128 v114, v[30:33] offset:64512
	s_waitcnt vmcnt(12)
	ds_write_b128 v115, v[34:37] offset:64512
	s_waitcnt vmcnt(11)
	ds_write_b128 v118, v[38:41] offset:64512
	s_waitcnt vmcnt(10)
	ds_write_b128 v117, v[42:45] offset:64512
	s_waitcnt vmcnt(9)
	ds_write_b128 v119, v[46:49]
	s_waitcnt vmcnt(8)
	ds_write_b128 v120, v[50:53]
	s_waitcnt vmcnt(7)
	ds_write_b128 v119, v[54:57] offset:18432
	v_mad_u64_u32 v[104:105], s[16:17], v6, s20, v[4:5]
	ds_read_b128 v[0:3], v104
	v_mad_u32_u24 v116, v162, s20, v4
	ds_read_b128 v[4:7], v116 offset:36864
	ds_read_b128 v[150:153], v104 offset:32
	ds_read_b128 v[154:157], v116 offset:36896
	ds_read_b128 v[8:11], v116 offset:41472
	ds_read_b128 v[158:161], v116 offset:41504
	ds_read_b128 v[12:15], v116 offset:46080
	ds_read_b128 v[170:173], v116 offset:46112
	s_waitcnt lgkmcnt(0)
	v_mfma_f32_32x32x16_f16 v[80:95], v[0:3], v[4:7], 0
	v_add_u32_e32 v169, 0x1200, v104
	v_mul_u32_u24_e32 v105, 0x90, v162
	v_mfma_f32_32x32x16_f16 v[48:63], v[0:3], v[8:11], 0
	v_mfma_f32_32x32x16_f16 v[16:31], v[0:3], v[12:15], 0
	ds_read_b128 v[0:3], v104 offset:4608
	ds_read_b128 v[174:177], v104 offset:4640
	s_waitcnt lgkmcnt(1)
	v_mfma_f32_32x32x16_f16 v[64:79], v[0:3], v[4:7], 0
	v_mfma_f32_32x32x16_f16 v[32:47], v[0:3], v[8:11], 0
	v_mfma_f32_32x32x16_f16 v[0:15], v[0:3], v[12:15], 0
	v_mfma_f32_32x32x16_f16 v[80:95], v[150:153], v[154:157], v[80:95]
	v_mfma_f32_32x32x16_f16 v[48:63], v[150:153], v[158:161], v[48:63]
	v_mfma_f32_32x32x16_f16 v[16:31], v[150:153], v[170:173], v[16:31]
	s_waitcnt lgkmcnt(0)
	v_mfma_f32_32x32x16_f16 v[64:79], v[174:177], v[154:157], v[64:79]
	v_mfma_f32_32x32x16_f16 v[32:47], v[174:177], v[158:161], v[32:47]
	v_mfma_f32_32x32x16_f16 v[0:15], v[174:177], v[170:173], v[0:15]
	ds_read_b128 v[150:153], v104 offset:64
	ds_read_b128 v[154:157], v116 offset:36928
	ds_read_b128 v[158:161], v104 offset:96
	ds_read_b128 v[170:173], v116 offset:36960
	ds_read_b128 v[174:177], v116 offset:41536
	ds_read_b128 v[178:181], v116 offset:41568
	ds_read_b128 v[182:185], v116 offset:46144
	ds_read_b128 v[186:189], v116 offset:46176
	s_waitcnt lgkmcnt(6)
	v_mfma_f32_32x32x16_f16 v[80:95], v[150:153], v[154:157], v[80:95]
	s_waitcnt lgkmcnt(3)
	v_mfma_f32_32x32x16_f16 v[48:63], v[150:153], v[174:177], v[48:63]
	s_waitcnt lgkmcnt(1)
	v_mfma_f32_32x32x16_f16 v[16:31], v[150:153], v[182:185], v[16:31]
	ds_read_b128 v[150:153], v104 offset:4672
	ds_read_b128 v[190:193], v104 offset:4704
	s_waitcnt lgkmcnt(0)
	s_barrier
	v_mfma_f32_32x32x16_f16 v[64:79], v[150:153], v[154:157], v[64:79]
	v_mfma_f32_32x32x16_f16 v[32:47], v[150:153], v[174:177], v[32:47]
	v_mfma_f32_32x32x16_f16 v[0:15], v[150:153], v[182:185], v[0:15]
	v_mfma_f32_32x32x16_f16 v[80:95], v[158:161], v[170:173], v[80:95]
	v_mfma_f32_32x32x16_f16 v[48:63], v[158:161], v[178:181], v[48:63]
	v_mfma_f32_32x32x16_f16 v[16:31], v[158:161], v[186:189], v[16:31]
	v_mfma_f32_32x32x16_f16 v[64:79], v[190:193], v[170:173], v[64:79]
	v_mfma_f32_32x32x16_f16 v[32:47], v[190:193], v[178:181], v[32:47]
	global_load_dwordx4 v[150:153], v[96:97], off offset:384
	global_load_dwordx4 v[154:157], v[98:99], off offset:384
	global_load_dwordx4 v[158:161], v[100:101], off offset:384
	global_load_dwordx4 v[170:173], v[102:103], off offset:384
	global_load_dwordx4 v[174:177], v[106:107], off offset:384
	global_load_dwordx4 v[178:181], v[108:109], off offset:384
	global_load_dwordx4 v[182:185], v[110:111], off offset:384
	v_mfma_f32_32x32x16_f16 v[0:15], v[190:193], v[186:189], v[0:15]
	s_waitcnt vmcnt(13)
	ds_write_b128 v114, v[122:125]
	s_waitcnt vmcnt(12)
	ds_write_b128 v115, v[126:129]
	s_waitcnt vmcnt(11)
	ds_write_b128 v114, v[130:133] offset:18432
	s_waitcnt vmcnt(10)
	ds_write_b128 v117, v[134:137]
	s_waitcnt vmcnt(9)
	ds_write_b128 v114, v[138:141] offset:36864
	s_waitcnt vmcnt(8)
	ds_write_b128 v115, v[142:145] offset:36864
	s_waitcnt vmcnt(7)
	ds_write_b128 v114, v[146:149] offset:55296
	ds_read_b128 v[122:125], v104 offset:64512
	v_add3_u32 v105, s1, v121, v105
	ds_read_b128 v[126:129], v105
	ds_read_b128 v[130:133], v104 offset:64544
	ds_read_b128 v[134:137], v105 offset:32
	ds_read_b128 v[138:141], v105 offset:4608
	ds_read_b128 v[142:145], v105 offset:4640
	ds_read_b128 v[146:149], v105 offset:9216
	ds_read_b128 v[186:189], v105 offset:9248
	s_waitcnt lgkmcnt(6)
	v_mfma_f32_32x32x16_f16 v[80:95], v[122:125], v[126:129], v[80:95]
	s_waitcnt lgkmcnt(3)
	v_mfma_f32_32x32x16_f16 v[48:63], v[122:125], v[138:141], v[48:63]
	s_waitcnt lgkmcnt(1)
	v_mfma_f32_32x32x16_f16 v[16:31], v[122:125], v[146:149], v[16:31]
	ds_read_b128 v[122:125], v169 offset:64512
	ds_read_b128 v[190:193], v169 offset:64544
	s_waitcnt lgkmcnt(1)
	v_mfma_f32_32x32x16_f16 v[64:79], v[122:125], v[126:129], v[64:79]
	v_mfma_f32_32x32x16_f16 v[32:47], v[122:125], v[138:141], v[32:47]
	v_mfma_f32_32x32x16_f16 v[0:15], v[122:125], v[146:149], v[0:15]
	v_mfma_f32_32x32x16_f16 v[80:95], v[130:133], v[134:137], v[80:95]
	v_mfma_f32_32x32x16_f16 v[48:63], v[130:133], v[142:145], v[48:63]
	v_mfma_f32_32x32x16_f16 v[16:31], v[130:133], v[186:189], v[16:31]
	s_waitcnt lgkmcnt(0)
	v_mfma_f32_32x32x16_f16 v[64:79], v[190:193], v[134:137], v[64:79]
	ds_read_b128 v[122:125], v104 offset:64576
	ds_read_b128 v[126:129], v105 offset:64
	ds_read_b128 v[130:133], v104 offset:64608
	ds_read_b128 v[134:137], v105 offset:96
	v_mfma_f32_32x32x16_f16 v[32:47], v[190:193], v[142:145], v[32:47]
	ds_read_b128 v[138:141], v105 offset:4672
	ds_read_b128 v[142:145], v105 offset:4704
	v_mfma_f32_32x32x16_f16 v[0:15], v[190:193], v[186:189], v[0:15]
	ds_read_b128 v[146:149], v105 offset:9280
	ds_read_b128 v[186:189], v105 offset:9312
	s_waitcnt lgkmcnt(6)
	v_mfma_f32_32x32x16_f16 v[80:95], v[122:125], v[126:129], v[80:95]
	s_waitcnt lgkmcnt(3)
	v_mfma_f32_32x32x16_f16 v[48:63], v[122:125], v[138:141], v[48:63]
	s_waitcnt lgkmcnt(1)
	v_mfma_f32_32x32x16_f16 v[16:31], v[122:125], v[146:149], v[16:31]
	ds_read_b128 v[122:125], v169 offset:64576
	ds_read_b128 v[190:193], v169 offset:64608
	s_waitcnt lgkmcnt(0)
	s_barrier
	v_mfma_f32_32x32x16_f16 v[64:79], v[122:125], v[126:129], v[64:79]
	v_mfma_f32_32x32x16_f16 v[32:47], v[122:125], v[138:141], v[32:47]
	v_mfma_f32_32x32x16_f16 v[0:15], v[122:125], v[146:149], v[0:15]
	v_mfma_f32_32x32x16_f16 v[80:95], v[130:133], v[134:137], v[80:95]
	v_mfma_f32_32x32x16_f16 v[48:63], v[130:133], v[142:145], v[48:63]
	v_mfma_f32_32x32x16_f16 v[16:31], v[130:133], v[186:189], v[16:31]
	v_mfma_f32_32x32x16_f16 v[64:79], v[190:193], v[134:137], v[64:79]
	v_mfma_f32_32x32x16_f16 v[32:47], v[190:193], v[142:145], v[32:47]
	global_load_dwordx4 v[122:125], v[96:97], off offset:512
	global_load_dwordx4 v[126:129], v[98:99], off offset:512
	global_load_dwordx4 v[130:133], v[100:101], off offset:512
	global_load_dwordx4 v[134:137], v[102:103], off offset:512
	global_load_dwordx4 v[138:141], v[106:107], off offset:512
	global_load_dwordx4 v[142:145], v[108:109], off offset:512
	global_load_dwordx4 v[146:149], v[110:111], off offset:512
	v_mfma_f32_32x32x16_f16 v[0:15], v[190:193], v[186:189], v[0:15]
	s_waitcnt vmcnt(13)
	ds_write_b128 v114, v[150:153] offset:64512
	s_waitcnt vmcnt(12)
	ds_write_b128 v115, v[154:157] offset:64512
	s_waitcnt vmcnt(11)
	ds_write_b128 v118, v[158:161] offset:64512
	s_waitcnt vmcnt(10)
	ds_write_b128 v117, v[170:173] offset:64512
	s_waitcnt vmcnt(9)
	ds_write_b128 v119, v[174:177]
	s_waitcnt vmcnt(8)
	ds_write_b128 v120, v[178:181]
	s_waitcnt vmcnt(7)
	ds_write_b128 v119, v[182:185] offset:18432
	ds_read_b128 v[150:153], v104
	ds_read_b128 v[154:157], v116 offset:36864
	ds_read_b128 v[158:161], v104 offset:32
	ds_read_b128 v[170:173], v116 offset:36896
	ds_read_b128 v[174:177], v116 offset:41472
	ds_read_b128 v[178:181], v116 offset:41504
	ds_read_b128 v[182:185], v116 offset:46080
	ds_read_b128 v[186:189], v116 offset:46112
	s_waitcnt lgkmcnt(6)
	v_mfma_f32_32x32x16_f16 v[80:95], v[150:153], v[154:157], v[80:95]
	s_waitcnt lgkmcnt(3)
	v_mfma_f32_32x32x16_f16 v[48:63], v[150:153], v[174:177], v[48:63]
	s_waitcnt lgkmcnt(1)
	v_mfma_f32_32x32x16_f16 v[16:31], v[150:153], v[182:185], v[16:31]
	ds_read_b128 v[150:153], v104 offset:4608
	ds_read_b128 v[190:193], v104 offset:4640
	s_waitcnt lgkmcnt(1)
	v_mfma_f32_32x32x16_f16 v[64:79], v[150:153], v[154:157], v[64:79]
	v_mfma_f32_32x32x16_f16 v[32:47], v[150:153], v[174:177], v[32:47]
	v_mfma_f32_32x32x16_f16 v[0:15], v[150:153], v[182:185], v[0:15]
	v_mfma_f32_32x32x16_f16 v[80:95], v[158:161], v[170:173], v[80:95]
	v_mfma_f32_32x32x16_f16 v[48:63], v[158:161], v[178:181], v[48:63]
	v_mfma_f32_32x32x16_f16 v[16:31], v[158:161], v[186:189], v[16:31]
	s_waitcnt lgkmcnt(0)
	v_mfma_f32_32x32x16_f16 v[64:79], v[190:193], v[170:173], v[64:79]
	ds_read_b128 v[150:153], v104 offset:64
	ds_read_b128 v[154:157], v116 offset:36928
	ds_read_b128 v[158:161], v104 offset:96
	ds_read_b128 v[170:173], v116 offset:36960
	v_mfma_f32_32x32x16_f16 v[32:47], v[190:193], v[178:181], v[32:47]
	ds_read_b128 v[174:177], v116 offset:41536
	ds_read_b128 v[178:181], v116 offset:41568
	v_mfma_f32_32x32x16_f16 v[0:15], v[190:193], v[186:189], v[0:15]
	ds_read_b128 v[182:185], v116 offset:46144
	ds_read_b128 v[186:189], v116 offset:46176
	s_waitcnt lgkmcnt(6)
	v_mfma_f32_32x32x16_f16 v[80:95], v[150:153], v[154:157], v[80:95]
	s_waitcnt lgkmcnt(3)
	v_mfma_f32_32x32x16_f16 v[48:63], v[150:153], v[174:177], v[48:63]
	s_waitcnt lgkmcnt(1)
	v_mfma_f32_32x32x16_f16 v[16:31], v[150:153], v[182:185], v[16:31]
	ds_read_b128 v[150:153], v104 offset:4672
	ds_read_b128 v[190:193], v104 offset:4704
	s_waitcnt lgkmcnt(0)
	s_barrier
	v_mfma_f32_32x32x16_f16 v[64:79], v[150:153], v[154:157], v[64:79]
	v_mfma_f32_32x32x16_f16 v[32:47], v[150:153], v[174:177], v[32:47]
	v_mfma_f32_32x32x16_f16 v[0:15], v[150:153], v[182:185], v[0:15]
	v_mfma_f32_32x32x16_f16 v[80:95], v[158:161], v[170:173], v[80:95]
	v_mfma_f32_32x32x16_f16 v[48:63], v[158:161], v[178:181], v[48:63]
	v_mfma_f32_32x32x16_f16 v[16:31], v[158:161], v[186:189], v[16:31]
	v_mfma_f32_32x32x16_f16 v[64:79], v[190:193], v[170:173], v[64:79]
	v_mfma_f32_32x32x16_f16 v[32:47], v[190:193], v[178:181], v[32:47]
	global_load_dwordx4 v[150:153], v[96:97], off offset:640
	global_load_dwordx4 v[154:157], v[98:99], off offset:640
	global_load_dwordx4 v[158:161], v[100:101], off offset:640
	global_load_dwordx4 v[170:173], v[102:103], off offset:640
	global_load_dwordx4 v[174:177], v[106:107], off offset:640
	global_load_dwordx4 v[178:181], v[108:109], off offset:640
	global_load_dwordx4 v[182:185], v[110:111], off offset:640
	v_mfma_f32_32x32x16_f16 v[0:15], v[190:193], v[186:189], v[0:15]
	s_waitcnt vmcnt(13)
	ds_write_b128 v114, v[122:125]
	s_waitcnt vmcnt(12)
	ds_write_b128 v115, v[126:129]
	s_waitcnt vmcnt(11)
	ds_write_b128 v114, v[130:133] offset:18432
	s_waitcnt vmcnt(10)
	ds_write_b128 v117, v[134:137]
	s_waitcnt vmcnt(9)
	ds_write_b128 v114, v[138:141] offset:36864
	s_waitcnt vmcnt(8)
	ds_write_b128 v115, v[142:145] offset:36864
	s_waitcnt vmcnt(7)
	ds_write_b128 v114, v[146:149] offset:55296
	ds_read_b128 v[122:125], v104 offset:64512
	ds_read_b128 v[126:129], v105
	ds_read_b128 v[130:133], v104 offset:64544
	ds_read_b128 v[134:137], v105 offset:32
	ds_read_b128 v[138:141], v105 offset:4608
	ds_read_b128 v[142:145], v105 offset:4640
	ds_read_b128 v[146:149], v105 offset:9216
	ds_read_b128 v[186:189], v105 offset:9248
	s_waitcnt lgkmcnt(6)
	v_mfma_f32_32x32x16_f16 v[80:95], v[122:125], v[126:129], v[80:95]
	s_waitcnt lgkmcnt(3)
	v_mfma_f32_32x32x16_f16 v[48:63], v[122:125], v[138:141], v[48:63]
	s_waitcnt lgkmcnt(1)
	v_mfma_f32_32x32x16_f16 v[16:31], v[122:125], v[146:149], v[16:31]
	ds_read_b128 v[122:125], v169 offset:64512
	ds_read_b128 v[190:193], v169 offset:64544
	s_waitcnt lgkmcnt(1)
	v_mfma_f32_32x32x16_f16 v[64:79], v[122:125], v[126:129], v[64:79]
	v_mfma_f32_32x32x16_f16 v[32:47], v[122:125], v[138:141], v[32:47]
	v_mfma_f32_32x32x16_f16 v[0:15], v[122:125], v[146:149], v[0:15]
	v_mfma_f32_32x32x16_f16 v[80:95], v[130:133], v[134:137], v[80:95]
	v_mfma_f32_32x32x16_f16 v[48:63], v[130:133], v[142:145], v[48:63]
	v_mfma_f32_32x32x16_f16 v[16:31], v[130:133], v[186:189], v[16:31]
	s_waitcnt lgkmcnt(0)
	v_mfma_f32_32x32x16_f16 v[64:79], v[190:193], v[134:137], v[64:79]
	ds_read_b128 v[122:125], v104 offset:64576
	ds_read_b128 v[126:129], v105 offset:64
	ds_read_b128 v[130:133], v104 offset:64608
	ds_read_b128 v[134:137], v105 offset:96
	v_mfma_f32_32x32x16_f16 v[32:47], v[190:193], v[142:145], v[32:47]
	ds_read_b128 v[138:141], v105 offset:4672
	ds_read_b128 v[142:145], v105 offset:4704
	v_mfma_f32_32x32x16_f16 v[0:15], v[190:193], v[186:189], v[0:15]
	ds_read_b128 v[146:149], v105 offset:9280
	ds_read_b128 v[186:189], v105 offset:9312
	s_waitcnt lgkmcnt(6)
	v_mfma_f32_32x32x16_f16 v[80:95], v[122:125], v[126:129], v[80:95]
	s_waitcnt lgkmcnt(3)
	v_mfma_f32_32x32x16_f16 v[48:63], v[122:125], v[138:141], v[48:63]
	s_waitcnt lgkmcnt(1)
	v_mfma_f32_32x32x16_f16 v[16:31], v[122:125], v[146:149], v[16:31]
	ds_read_b128 v[122:125], v169 offset:64576
	ds_read_b128 v[190:193], v169 offset:64608
	s_waitcnt lgkmcnt(0)
	s_barrier
	v_mfma_f32_32x32x16_f16 v[64:79], v[122:125], v[126:129], v[64:79]
	v_mfma_f32_32x32x16_f16 v[32:47], v[122:125], v[138:141], v[32:47]
	v_mfma_f32_32x32x16_f16 v[0:15], v[122:125], v[146:149], v[0:15]
	v_mfma_f32_32x32x16_f16 v[80:95], v[130:133], v[134:137], v[80:95]
	v_mfma_f32_32x32x16_f16 v[48:63], v[130:133], v[142:145], v[48:63]
	v_mfma_f32_32x32x16_f16 v[16:31], v[130:133], v[186:189], v[16:31]
	v_mfma_f32_32x32x16_f16 v[64:79], v[190:193], v[134:137], v[64:79]
	v_mfma_f32_32x32x16_f16 v[32:47], v[190:193], v[142:145], v[32:47]
	global_load_dwordx4 v[122:125], v[96:97], off offset:768
	global_load_dwordx4 v[126:129], v[98:99], off offset:768
	global_load_dwordx4 v[130:133], v[100:101], off offset:768
	global_load_dwordx4 v[134:137], v[102:103], off offset:768
	global_load_dwordx4 v[138:141], v[106:107], off offset:768
	global_load_dwordx4 v[142:145], v[108:109], off offset:768
	global_load_dwordx4 v[146:149], v[110:111], off offset:768
	v_mfma_f32_32x32x16_f16 v[0:15], v[190:193], v[186:189], v[0:15]
	s_waitcnt vmcnt(13)
	ds_write_b128 v114, v[150:153] offset:64512
	s_waitcnt vmcnt(12)
	ds_write_b128 v115, v[154:157] offset:64512
	s_waitcnt vmcnt(11)
	ds_write_b128 v118, v[158:161] offset:64512
	s_waitcnt vmcnt(10)
	ds_write_b128 v117, v[170:173] offset:64512
	s_waitcnt vmcnt(9)
	ds_write_b128 v119, v[174:177]
	s_waitcnt vmcnt(8)
	ds_write_b128 v120, v[178:181]
	s_waitcnt vmcnt(7)
	ds_write_b128 v119, v[182:185] offset:18432
	ds_read_b128 v[150:153], v104
	ds_read_b128 v[154:157], v116 offset:36864
	ds_read_b128 v[158:161], v104 offset:32
	ds_read_b128 v[170:173], v116 offset:36896
	ds_read_b128 v[174:177], v116 offset:41472
	ds_read_b128 v[178:181], v116 offset:41504
	ds_read_b128 v[182:185], v116 offset:46080
	ds_read_b128 v[186:189], v116 offset:46112
	s_waitcnt lgkmcnt(6)
	v_mfma_f32_32x32x16_f16 v[80:95], v[150:153], v[154:157], v[80:95]
	s_waitcnt lgkmcnt(3)
	v_mfma_f32_32x32x16_f16 v[48:63], v[150:153], v[174:177], v[48:63]
	s_waitcnt lgkmcnt(1)
	v_mfma_f32_32x32x16_f16 v[16:31], v[150:153], v[182:185], v[16:31]
	ds_read_b128 v[150:153], v104 offset:4608
	ds_read_b128 v[190:193], v104 offset:4640
	s_waitcnt lgkmcnt(1)
	v_mfma_f32_32x32x16_f16 v[64:79], v[150:153], v[154:157], v[64:79]
	v_mfma_f32_32x32x16_f16 v[32:47], v[150:153], v[174:177], v[32:47]
	v_mfma_f32_32x32x16_f16 v[0:15], v[150:153], v[182:185], v[0:15]
	v_mfma_f32_32x32x16_f16 v[80:95], v[158:161], v[170:173], v[80:95]
	v_mfma_f32_32x32x16_f16 v[48:63], v[158:161], v[178:181], v[48:63]
	v_mfma_f32_32x32x16_f16 v[16:31], v[158:161], v[186:189], v[16:31]
	s_waitcnt lgkmcnt(0)
	v_mfma_f32_32x32x16_f16 v[64:79], v[190:193], v[170:173], v[64:79]
	ds_read_b128 v[150:153], v104 offset:64
	ds_read_b128 v[154:157], v116 offset:36928
	ds_read_b128 v[158:161], v104 offset:96
	ds_read_b128 v[170:173], v116 offset:36960
	v_mfma_f32_32x32x16_f16 v[32:47], v[190:193], v[178:181], v[32:47]
	ds_read_b128 v[174:177], v116 offset:41536
	ds_read_b128 v[178:181], v116 offset:41568
	v_mfma_f32_32x32x16_f16 v[0:15], v[190:193], v[186:189], v[0:15]
	ds_read_b128 v[182:185], v116 offset:46144
	ds_read_b128 v[186:189], v116 offset:46176
	s_waitcnt lgkmcnt(6)
	v_mfma_f32_32x32x16_f16 v[80:95], v[150:153], v[154:157], v[80:95]
	s_waitcnt lgkmcnt(3)
	v_mfma_f32_32x32x16_f16 v[48:63], v[150:153], v[174:177], v[48:63]
	s_waitcnt lgkmcnt(1)
	v_mfma_f32_32x32x16_f16 v[16:31], v[150:153], v[182:185], v[16:31]
	ds_read_b128 v[150:153], v104 offset:4672
	ds_read_b128 v[190:193], v104 offset:4704
	s_waitcnt lgkmcnt(0)
	s_barrier
	v_mfma_f32_32x32x16_f16 v[64:79], v[150:153], v[154:157], v[64:79]
	v_mfma_f32_32x32x16_f16 v[32:47], v[150:153], v[174:177], v[32:47]
	v_mfma_f32_32x32x16_f16 v[0:15], v[150:153], v[182:185], v[0:15]
	v_mfma_f32_32x32x16_f16 v[80:95], v[158:161], v[170:173], v[80:95]
	v_mfma_f32_32x32x16_f16 v[48:63], v[158:161], v[178:181], v[48:63]
	v_mfma_f32_32x32x16_f16 v[16:31], v[158:161], v[186:189], v[16:31]
	v_mfma_f32_32x32x16_f16 v[64:79], v[190:193], v[170:173], v[64:79]
	v_mfma_f32_32x32x16_f16 v[32:47], v[190:193], v[178:181], v[32:47]
	global_load_dwordx4 v[150:153], v[96:97], off offset:896
	global_load_dwordx4 v[154:157], v[98:99], off offset:896
	global_load_dwordx4 v[158:161], v[100:101], off offset:896
	global_load_dwordx4 v[170:173], v[102:103], off offset:896
	global_load_dwordx4 v[174:177], v[106:107], off offset:896
	global_load_dwordx4 v[178:181], v[108:109], off offset:896
	global_load_dwordx4 v[182:185], v[110:111], off offset:896
	v_mfma_f32_32x32x16_f16 v[0:15], v[190:193], v[186:189], v[0:15]
	s_waitcnt vmcnt(13)
	ds_write_b128 v114, v[122:125]
	s_waitcnt vmcnt(12)
	ds_write_b128 v115, v[126:129]
	s_waitcnt vmcnt(11)
	ds_write_b128 v114, v[130:133] offset:18432
	s_waitcnt vmcnt(10)
	ds_write_b128 v117, v[134:137]
	s_waitcnt vmcnt(9)
	ds_write_b128 v114, v[138:141] offset:36864
	s_waitcnt vmcnt(8)
	ds_write_b128 v115, v[142:145] offset:36864
	s_waitcnt vmcnt(7)
	ds_write_b128 v114, v[146:149] offset:55296
	ds_read_b128 v[122:125], v104 offset:64512
	ds_read_b128 v[126:129], v105
	ds_read_b128 v[130:133], v104 offset:64544
	ds_read_b128 v[134:137], v105 offset:32
	ds_read_b128 v[138:141], v105 offset:4608
	ds_read_b128 v[142:145], v105 offset:4640
	ds_read_b128 v[146:149], v105 offset:9216
	ds_read_b128 v[186:189], v105 offset:9248
	s_waitcnt lgkmcnt(6)
	v_mfma_f32_32x32x16_f16 v[80:95], v[122:125], v[126:129], v[80:95]
	s_waitcnt lgkmcnt(3)
	v_mfma_f32_32x32x16_f16 v[48:63], v[122:125], v[138:141], v[48:63]
	s_waitcnt lgkmcnt(1)
	v_mfma_f32_32x32x16_f16 v[16:31], v[122:125], v[146:149], v[16:31]
	ds_read_b128 v[122:125], v169 offset:64512
	ds_read_b128 v[190:193], v169 offset:64544
	s_waitcnt lgkmcnt(1)
	v_mfma_f32_32x32x16_f16 v[64:79], v[122:125], v[126:129], v[64:79]
	v_mfma_f32_32x32x16_f16 v[32:47], v[122:125], v[138:141], v[32:47]
	v_mfma_f32_32x32x16_f16 v[0:15], v[122:125], v[146:149], v[0:15]
	v_mfma_f32_32x32x16_f16 v[80:95], v[130:133], v[134:137], v[80:95]
	v_mfma_f32_32x32x16_f16 v[48:63], v[130:133], v[142:145], v[48:63]
	v_mfma_f32_32x32x16_f16 v[16:31], v[130:133], v[186:189], v[16:31]
	s_waitcnt lgkmcnt(0)
	v_mfma_f32_32x32x16_f16 v[64:79], v[190:193], v[134:137], v[64:79]
	ds_read_b128 v[122:125], v104 offset:64576
	ds_read_b128 v[126:129], v105 offset:64
	ds_read_b128 v[130:133], v104 offset:64608
	ds_read_b128 v[134:137], v105 offset:96
	v_mfma_f32_32x32x16_f16 v[32:47], v[190:193], v[142:145], v[32:47]
	ds_read_b128 v[138:141], v105 offset:4672
	ds_read_b128 v[142:145], v105 offset:4704
	v_mfma_f32_32x32x16_f16 v[0:15], v[190:193], v[186:189], v[0:15]
	ds_read_b128 v[146:149], v105 offset:9280
	ds_read_b128 v[186:189], v105 offset:9312
	s_waitcnt lgkmcnt(6)
	v_mfma_f32_32x32x16_f16 v[80:95], v[122:125], v[126:129], v[80:95]
	s_waitcnt lgkmcnt(3)
	v_mfma_f32_32x32x16_f16 v[48:63], v[122:125], v[138:141], v[48:63]
	s_waitcnt lgkmcnt(1)
	v_mfma_f32_32x32x16_f16 v[16:31], v[122:125], v[146:149], v[16:31]
	ds_read_b128 v[122:125], v169 offset:64576
	ds_read_b128 v[190:193], v169 offset:64608
	s_waitcnt lgkmcnt(0)
	s_barrier
	v_mfma_f32_32x32x16_f16 v[64:79], v[122:125], v[126:129], v[64:79]
	v_mfma_f32_32x32x16_f16 v[32:47], v[122:125], v[138:141], v[32:47]
	v_mfma_f32_32x32x16_f16 v[0:15], v[122:125], v[146:149], v[0:15]
	v_mfma_f32_32x32x16_f16 v[80:95], v[130:133], v[134:137], v[80:95]
	v_mfma_f32_32x32x16_f16 v[48:63], v[130:133], v[142:145], v[48:63]
	v_mfma_f32_32x32x16_f16 v[16:31], v[130:133], v[186:189], v[16:31]
	v_mfma_f32_32x32x16_f16 v[64:79], v[190:193], v[134:137], v[64:79]
	v_mfma_f32_32x32x16_f16 v[32:47], v[190:193], v[142:145], v[32:47]
	global_load_dwordx4 v[122:125], v[96:97], off offset:1024
	global_load_dwordx4 v[126:129], v[98:99], off offset:1024
	global_load_dwordx4 v[130:133], v[100:101], off offset:1024
	global_load_dwordx4 v[134:137], v[102:103], off offset:1024
	global_load_dwordx4 v[138:141], v[106:107], off offset:1024
	global_load_dwordx4 v[142:145], v[108:109], off offset:1024
	global_load_dwordx4 v[146:149], v[110:111], off offset:1024
	v_mfma_f32_32x32x16_f16 v[0:15], v[190:193], v[186:189], v[0:15]
	s_waitcnt vmcnt(13)
	ds_write_b128 v114, v[150:153] offset:64512
	s_waitcnt vmcnt(12)
	ds_write_b128 v115, v[154:157] offset:64512
	s_waitcnt vmcnt(11)
	ds_write_b128 v118, v[158:161] offset:64512
	s_waitcnt vmcnt(10)
	ds_write_b128 v117, v[170:173] offset:64512
	s_waitcnt vmcnt(9)
	ds_write_b128 v119, v[174:177]
	s_waitcnt vmcnt(8)
	ds_write_b128 v120, v[178:181]
	s_waitcnt vmcnt(7)
	ds_write_b128 v119, v[182:185] offset:18432
	ds_read_b128 v[150:153], v104
	ds_read_b128 v[154:157], v116 offset:36864
	ds_read_b128 v[158:161], v104 offset:32
	ds_read_b128 v[170:173], v116 offset:36896
	ds_read_b128 v[174:177], v116 offset:41472
	ds_read_b128 v[178:181], v116 offset:41504
	ds_read_b128 v[182:185], v116 offset:46080
	ds_read_b128 v[186:189], v116 offset:46112
	s_waitcnt lgkmcnt(6)
	v_mfma_f32_32x32x16_f16 v[80:95], v[150:153], v[154:157], v[80:95]
	s_waitcnt lgkmcnt(3)
	v_mfma_f32_32x32x16_f16 v[48:63], v[150:153], v[174:177], v[48:63]
	s_waitcnt lgkmcnt(1)
	v_mfma_f32_32x32x16_f16 v[16:31], v[150:153], v[182:185], v[16:31]
	ds_read_b128 v[150:153], v104 offset:4608
	ds_read_b128 v[190:193], v104 offset:4640
	s_waitcnt lgkmcnt(1)
	v_mfma_f32_32x32x16_f16 v[64:79], v[150:153], v[154:157], v[64:79]
	v_mfma_f32_32x32x16_f16 v[32:47], v[150:153], v[174:177], v[32:47]
	v_mfma_f32_32x32x16_f16 v[0:15], v[150:153], v[182:185], v[0:15]
	v_mfma_f32_32x32x16_f16 v[80:95], v[158:161], v[170:173], v[80:95]
	v_mfma_f32_32x32x16_f16 v[48:63], v[158:161], v[178:181], v[48:63]
	v_mfma_f32_32x32x16_f16 v[16:31], v[158:161], v[186:189], v[16:31]
	s_waitcnt lgkmcnt(0)
	v_mfma_f32_32x32x16_f16 v[64:79], v[190:193], v[170:173], v[64:79]
	ds_read_b128 v[150:153], v104 offset:64
	ds_read_b128 v[154:157], v116 offset:36928
	ds_read_b128 v[158:161], v104 offset:96
	ds_read_b128 v[170:173], v116 offset:36960
	v_mfma_f32_32x32x16_f16 v[32:47], v[190:193], v[178:181], v[32:47]
	ds_read_b128 v[174:177], v116 offset:41536
	ds_read_b128 v[178:181], v116 offset:41568
	v_mfma_f32_32x32x16_f16 v[0:15], v[190:193], v[186:189], v[0:15]
	ds_read_b128 v[182:185], v116 offset:46144
	ds_read_b128 v[186:189], v116 offset:46176
	s_waitcnt lgkmcnt(6)
	v_mfma_f32_32x32x16_f16 v[80:95], v[150:153], v[154:157], v[80:95]
	s_waitcnt lgkmcnt(3)
	v_mfma_f32_32x32x16_f16 v[48:63], v[150:153], v[174:177], v[48:63]
	s_waitcnt lgkmcnt(1)
	v_mfma_f32_32x32x16_f16 v[16:31], v[150:153], v[182:185], v[16:31]
	ds_read_b128 v[150:153], v104 offset:4672
	ds_read_b128 v[190:193], v104 offset:4704
	s_waitcnt lgkmcnt(0)
	s_barrier
	v_mfma_f32_32x32x16_f16 v[64:79], v[150:153], v[154:157], v[64:79]
	v_mfma_f32_32x32x16_f16 v[32:47], v[150:153], v[174:177], v[32:47]
	v_mfma_f32_32x32x16_f16 v[0:15], v[150:153], v[182:185], v[0:15]
	v_mfma_f32_32x32x16_f16 v[80:95], v[158:161], v[170:173], v[80:95]
	v_mfma_f32_32x32x16_f16 v[48:63], v[158:161], v[178:181], v[48:63]
	v_mfma_f32_32x32x16_f16 v[16:31], v[158:161], v[186:189], v[16:31]
	v_mfma_f32_32x32x16_f16 v[64:79], v[190:193], v[170:173], v[64:79]
	v_mfma_f32_32x32x16_f16 v[32:47], v[190:193], v[178:181], v[32:47]
	global_load_dwordx4 v[150:153], v[96:97], off offset:1152
	global_load_dwordx4 v[154:157], v[98:99], off offset:1152
	global_load_dwordx4 v[158:161], v[100:101], off offset:1152
	global_load_dwordx4 v[170:173], v[102:103], off offset:1152
	global_load_dwordx4 v[174:177], v[106:107], off offset:1152
	global_load_dwordx4 v[178:181], v[108:109], off offset:1152
	global_load_dwordx4 v[182:185], v[110:111], off offset:1152
	v_mfma_f32_32x32x16_f16 v[0:15], v[190:193], v[186:189], v[0:15]
	s_waitcnt vmcnt(13)
	ds_write_b128 v114, v[122:125]
	s_waitcnt vmcnt(12)
	ds_write_b128 v115, v[126:129]
	s_waitcnt vmcnt(11)
	ds_write_b128 v114, v[130:133] offset:18432
	s_waitcnt vmcnt(10)
	ds_write_b128 v117, v[134:137]
	s_waitcnt vmcnt(9)
	ds_write_b128 v114, v[138:141] offset:36864
	s_waitcnt vmcnt(8)
	ds_write_b128 v115, v[142:145] offset:36864
	s_waitcnt vmcnt(7)
	ds_write_b128 v114, v[146:149] offset:55296
	ds_read_b128 v[122:125], v104 offset:64512
	ds_read_b128 v[126:129], v105
	ds_read_b128 v[130:133], v104 offset:64544
	ds_read_b128 v[134:137], v105 offset:32
	ds_read_b128 v[138:141], v105 offset:4608
	ds_read_b128 v[142:145], v105 offset:4640
	ds_read_b128 v[146:149], v105 offset:9216
	ds_read_b128 v[186:189], v105 offset:9248
	s_waitcnt lgkmcnt(6)
	v_mfma_f32_32x32x16_f16 v[80:95], v[122:125], v[126:129], v[80:95]
	s_waitcnt lgkmcnt(3)
	v_mfma_f32_32x32x16_f16 v[48:63], v[122:125], v[138:141], v[48:63]
	s_waitcnt lgkmcnt(1)
	v_mfma_f32_32x32x16_f16 v[16:31], v[122:125], v[146:149], v[16:31]
	ds_read_b128 v[122:125], v169 offset:64512
	ds_read_b128 v[190:193], v169 offset:64544
	s_waitcnt lgkmcnt(1)
	v_mfma_f32_32x32x16_f16 v[64:79], v[122:125], v[126:129], v[64:79]
	v_mfma_f32_32x32x16_f16 v[32:47], v[122:125], v[138:141], v[32:47]
	v_mfma_f32_32x32x16_f16 v[0:15], v[122:125], v[146:149], v[0:15]
	v_mfma_f32_32x32x16_f16 v[80:95], v[130:133], v[134:137], v[80:95]
	v_mfma_f32_32x32x16_f16 v[48:63], v[130:133], v[142:145], v[48:63]
	v_mfma_f32_32x32x16_f16 v[16:31], v[130:133], v[186:189], v[16:31]
	s_waitcnt lgkmcnt(0)
	v_mfma_f32_32x32x16_f16 v[64:79], v[190:193], v[134:137], v[64:79]
	ds_read_b128 v[122:125], v104 offset:64576
	ds_read_b128 v[126:129], v105 offset:64
	ds_read_b128 v[130:133], v104 offset:64608
	ds_read_b128 v[134:137], v105 offset:96
	v_mfma_f32_32x32x16_f16 v[32:47], v[190:193], v[142:145], v[32:47]
	ds_read_b128 v[138:141], v105 offset:4672
	ds_read_b128 v[142:145], v105 offset:4704
	v_mfma_f32_32x32x16_f16 v[0:15], v[190:193], v[186:189], v[0:15]
	ds_read_b128 v[146:149], v105 offset:9280
	ds_read_b128 v[186:189], v105 offset:9312
	s_waitcnt lgkmcnt(6)
	v_mfma_f32_32x32x16_f16 v[80:95], v[122:125], v[126:129], v[80:95]
	s_waitcnt lgkmcnt(3)
	v_mfma_f32_32x32x16_f16 v[48:63], v[122:125], v[138:141], v[48:63]
	s_waitcnt lgkmcnt(1)
	v_mfma_f32_32x32x16_f16 v[16:31], v[122:125], v[146:149], v[16:31]
	ds_read_b128 v[122:125], v169 offset:64576
	ds_read_b128 v[190:193], v169 offset:64608
	s_waitcnt lgkmcnt(0)
	s_barrier
	v_mfma_f32_32x32x16_f16 v[64:79], v[122:125], v[126:129], v[64:79]
	v_mfma_f32_32x32x16_f16 v[32:47], v[122:125], v[138:141], v[32:47]
	v_mfma_f32_32x32x16_f16 v[0:15], v[122:125], v[146:149], v[0:15]
	v_mfma_f32_32x32x16_f16 v[80:95], v[130:133], v[134:137], v[80:95]
	v_mfma_f32_32x32x16_f16 v[48:63], v[130:133], v[142:145], v[48:63]
	v_mfma_f32_32x32x16_f16 v[16:31], v[130:133], v[186:189], v[16:31]
	v_mfma_f32_32x32x16_f16 v[64:79], v[190:193], v[134:137], v[64:79]
	v_mfma_f32_32x32x16_f16 v[32:47], v[190:193], v[142:145], v[32:47]
	global_load_dwordx4 v[122:125], v[96:97], off offset:1280
	global_load_dwordx4 v[126:129], v[98:99], off offset:1280
	global_load_dwordx4 v[130:133], v[100:101], off offset:1280
	global_load_dwordx4 v[134:137], v[102:103], off offset:1280
	global_load_dwordx4 v[138:141], v[106:107], off offset:1280
	global_load_dwordx4 v[142:145], v[108:109], off offset:1280
	global_load_dwordx4 v[146:149], v[110:111], off offset:1280
	v_mfma_f32_32x32x16_f16 v[0:15], v[190:193], v[186:189], v[0:15]
	s_waitcnt vmcnt(13)
	ds_write_b128 v114, v[150:153] offset:64512
	s_waitcnt vmcnt(12)
	ds_write_b128 v115, v[154:157] offset:64512
	s_waitcnt vmcnt(11)
	ds_write_b128 v118, v[158:161] offset:64512
	s_waitcnt vmcnt(10)
	ds_write_b128 v117, v[170:173] offset:64512
	s_waitcnt vmcnt(9)
	ds_write_b128 v119, v[174:177]
	s_waitcnt vmcnt(8)
	ds_write_b128 v120, v[178:181]
	s_waitcnt vmcnt(7)
	ds_write_b128 v119, v[182:185] offset:18432
	ds_read_b128 v[150:153], v104
	ds_read_b128 v[154:157], v116 offset:36864
	ds_read_b128 v[158:161], v104 offset:32
	ds_read_b128 v[170:173], v116 offset:36896
	ds_read_b128 v[174:177], v116 offset:41472
	ds_read_b128 v[178:181], v116 offset:41504
	ds_read_b128 v[182:185], v116 offset:46080
	ds_read_b128 v[186:189], v116 offset:46112
	s_waitcnt lgkmcnt(6)
	v_mfma_f32_32x32x16_f16 v[80:95], v[150:153], v[154:157], v[80:95]
	s_waitcnt lgkmcnt(3)
	v_mfma_f32_32x32x16_f16 v[48:63], v[150:153], v[174:177], v[48:63]
	s_waitcnt lgkmcnt(1)
	v_mfma_f32_32x32x16_f16 v[16:31], v[150:153], v[182:185], v[16:31]
	ds_read_b128 v[150:153], v104 offset:4608
	ds_read_b128 v[190:193], v104 offset:4640
	s_waitcnt lgkmcnt(1)
	v_mfma_f32_32x32x16_f16 v[64:79], v[150:153], v[154:157], v[64:79]
	v_mfma_f32_32x32x16_f16 v[32:47], v[150:153], v[174:177], v[32:47]
	v_mfma_f32_32x32x16_f16 v[0:15], v[150:153], v[182:185], v[0:15]
	v_mfma_f32_32x32x16_f16 v[80:95], v[158:161], v[170:173], v[80:95]
	v_mfma_f32_32x32x16_f16 v[48:63], v[158:161], v[178:181], v[48:63]
	v_mfma_f32_32x32x16_f16 v[16:31], v[158:161], v[186:189], v[16:31]
	s_waitcnt lgkmcnt(0)
	v_mfma_f32_32x32x16_f16 v[64:79], v[190:193], v[170:173], v[64:79]
	ds_read_b128 v[150:153], v104 offset:64
	ds_read_b128 v[154:157], v116 offset:36928
	ds_read_b128 v[158:161], v104 offset:96
	ds_read_b128 v[170:173], v116 offset:36960
	v_mfma_f32_32x32x16_f16 v[32:47], v[190:193], v[178:181], v[32:47]
	ds_read_b128 v[174:177], v116 offset:41536
	ds_read_b128 v[178:181], v116 offset:41568
	v_mfma_f32_32x32x16_f16 v[0:15], v[190:193], v[186:189], v[0:15]
	ds_read_b128 v[182:185], v116 offset:46144
	ds_read_b128 v[186:189], v116 offset:46176
	s_waitcnt lgkmcnt(6)
	v_mfma_f32_32x32x16_f16 v[80:95], v[150:153], v[154:157], v[80:95]
	s_waitcnt lgkmcnt(3)
	v_mfma_f32_32x32x16_f16 v[48:63], v[150:153], v[174:177], v[48:63]
	s_waitcnt lgkmcnt(1)
	v_mfma_f32_32x32x16_f16 v[16:31], v[150:153], v[182:185], v[16:31]
	ds_read_b128 v[150:153], v104 offset:4672
	ds_read_b128 v[190:193], v104 offset:4704
	s_waitcnt lgkmcnt(0)
	s_barrier
	v_mfma_f32_32x32x16_f16 v[64:79], v[150:153], v[154:157], v[64:79]
	v_mfma_f32_32x32x16_f16 v[32:47], v[150:153], v[174:177], v[32:47]
	v_mfma_f32_32x32x16_f16 v[0:15], v[150:153], v[182:185], v[0:15]
	v_mfma_f32_32x32x16_f16 v[80:95], v[158:161], v[170:173], v[80:95]
	v_mfma_f32_32x32x16_f16 v[48:63], v[158:161], v[178:181], v[48:63]
	v_mfma_f32_32x32x16_f16 v[16:31], v[158:161], v[186:189], v[16:31]
	v_mfma_f32_32x32x16_f16 v[64:79], v[190:193], v[170:173], v[64:79]
	v_mfma_f32_32x32x16_f16 v[32:47], v[190:193], v[178:181], v[32:47]
	global_load_dwordx4 v[150:153], v[96:97], off offset:1408
	global_load_dwordx4 v[154:157], v[98:99], off offset:1408
	global_load_dwordx4 v[158:161], v[100:101], off offset:1408
	global_load_dwordx4 v[170:173], v[102:103], off offset:1408
	global_load_dwordx4 v[174:177], v[106:107], off offset:1408
	global_load_dwordx4 v[178:181], v[108:109], off offset:1408
	global_load_dwordx4 v[182:185], v[110:111], off offset:1408
	v_mfma_f32_32x32x16_f16 v[0:15], v[190:193], v[186:189], v[0:15]
	s_waitcnt vmcnt(13)
	ds_write_b128 v114, v[122:125]
	s_waitcnt vmcnt(12)
	ds_write_b128 v115, v[126:129]
	s_waitcnt vmcnt(11)
	ds_write_b128 v114, v[130:133] offset:18432
	s_waitcnt vmcnt(10)
	ds_write_b128 v117, v[134:137]
	s_waitcnt vmcnt(9)
	ds_write_b128 v114, v[138:141] offset:36864
	s_waitcnt vmcnt(8)
	ds_write_b128 v115, v[142:145] offset:36864
	s_waitcnt vmcnt(7)
	ds_write_b128 v114, v[146:149] offset:55296
	ds_read_b128 v[122:125], v104 offset:64512
	ds_read_b128 v[126:129], v105
	ds_read_b128 v[130:133], v104 offset:64544
	ds_read_b128 v[134:137], v105 offset:32
	ds_read_b128 v[138:141], v105 offset:4608
	ds_read_b128 v[142:145], v105 offset:4640
	ds_read_b128 v[146:149], v105 offset:9216
	ds_read_b128 v[186:189], v105 offset:9248
	s_waitcnt lgkmcnt(6)
	v_mfma_f32_32x32x16_f16 v[80:95], v[122:125], v[126:129], v[80:95]
	s_waitcnt lgkmcnt(3)
	v_mfma_f32_32x32x16_f16 v[48:63], v[122:125], v[138:141], v[48:63]
	s_waitcnt lgkmcnt(1)
	v_mfma_f32_32x32x16_f16 v[16:31], v[122:125], v[146:149], v[16:31]
	ds_read_b128 v[122:125], v169 offset:64512
	ds_read_b128 v[190:193], v169 offset:64544
	s_waitcnt lgkmcnt(1)
	v_mfma_f32_32x32x16_f16 v[64:79], v[122:125], v[126:129], v[64:79]
	v_mfma_f32_32x32x16_f16 v[32:47], v[122:125], v[138:141], v[32:47]
	v_mfma_f32_32x32x16_f16 v[0:15], v[122:125], v[146:149], v[0:15]
	v_mfma_f32_32x32x16_f16 v[80:95], v[130:133], v[134:137], v[80:95]
	v_mfma_f32_32x32x16_f16 v[48:63], v[130:133], v[142:145], v[48:63]
	v_mfma_f32_32x32x16_f16 v[16:31], v[130:133], v[186:189], v[16:31]
	s_waitcnt lgkmcnt(0)
	v_mfma_f32_32x32x16_f16 v[64:79], v[190:193], v[134:137], v[64:79]
	ds_read_b128 v[122:125], v104 offset:64576
	ds_read_b128 v[126:129], v105 offset:64
	ds_read_b128 v[130:133], v104 offset:64608
	ds_read_b128 v[134:137], v105 offset:96
	v_mfma_f32_32x32x16_f16 v[32:47], v[190:193], v[142:145], v[32:47]
	ds_read_b128 v[138:141], v105 offset:4672
	ds_read_b128 v[142:145], v105 offset:4704
	v_mfma_f32_32x32x16_f16 v[0:15], v[190:193], v[186:189], v[0:15]
	ds_read_b128 v[146:149], v105 offset:9280
	ds_read_b128 v[186:189], v105 offset:9312
	s_waitcnt lgkmcnt(6)
	v_mfma_f32_32x32x16_f16 v[80:95], v[122:125], v[126:129], v[80:95]
	s_waitcnt lgkmcnt(3)
	v_mfma_f32_32x32x16_f16 v[48:63], v[122:125], v[138:141], v[48:63]
	s_waitcnt lgkmcnt(1)
	v_mfma_f32_32x32x16_f16 v[16:31], v[122:125], v[146:149], v[16:31]
	ds_read_b128 v[122:125], v169 offset:64576
	ds_read_b128 v[190:193], v169 offset:64608
	s_waitcnt lgkmcnt(0)
	s_barrier
	v_mfma_f32_32x32x16_f16 v[64:79], v[122:125], v[126:129], v[64:79]
	v_mfma_f32_32x32x16_f16 v[32:47], v[122:125], v[138:141], v[32:47]
	v_mfma_f32_32x32x16_f16 v[0:15], v[122:125], v[146:149], v[0:15]
	v_mfma_f32_32x32x16_f16 v[80:95], v[130:133], v[134:137], v[80:95]
	v_mfma_f32_32x32x16_f16 v[48:63], v[130:133], v[142:145], v[48:63]
	v_mfma_f32_32x32x16_f16 v[16:31], v[130:133], v[186:189], v[16:31]
	v_mfma_f32_32x32x16_f16 v[64:79], v[190:193], v[134:137], v[64:79]
	v_mfma_f32_32x32x16_f16 v[32:47], v[190:193], v[142:145], v[32:47]
	global_load_dwordx4 v[122:125], v[96:97], off offset:1536
	global_load_dwordx4 v[126:129], v[98:99], off offset:1536
	global_load_dwordx4 v[130:133], v[100:101], off offset:1536
	global_load_dwordx4 v[134:137], v[102:103], off offset:1536
	global_load_dwordx4 v[138:141], v[106:107], off offset:1536
	global_load_dwordx4 v[142:145], v[108:109], off offset:1536
	global_load_dwordx4 v[146:149], v[110:111], off offset:1536
	v_mfma_f32_32x32x16_f16 v[0:15], v[190:193], v[186:189], v[0:15]
	s_waitcnt vmcnt(13)
	ds_write_b128 v114, v[150:153] offset:64512
	s_waitcnt vmcnt(12)
	ds_write_b128 v115, v[154:157] offset:64512
	s_waitcnt vmcnt(11)
	ds_write_b128 v118, v[158:161] offset:64512
	s_waitcnt vmcnt(10)
	ds_write_b128 v117, v[170:173] offset:64512
	s_waitcnt vmcnt(9)
	ds_write_b128 v119, v[174:177]
	s_waitcnt vmcnt(8)
	ds_write_b128 v120, v[178:181]
	s_waitcnt vmcnt(7)
	ds_write_b128 v119, v[182:185] offset:18432
	ds_read_b128 v[150:153], v104
	ds_read_b128 v[154:157], v116 offset:36864
	ds_read_b128 v[158:161], v104 offset:32
	ds_read_b128 v[170:173], v116 offset:36896
	ds_read_b128 v[174:177], v116 offset:41472
	ds_read_b128 v[178:181], v116 offset:41504
	ds_read_b128 v[182:185], v116 offset:46080
	ds_read_b128 v[186:189], v116 offset:46112
	s_waitcnt lgkmcnt(6)
	v_mfma_f32_32x32x16_f16 v[80:95], v[150:153], v[154:157], v[80:95]
	s_waitcnt lgkmcnt(3)
	v_mfma_f32_32x32x16_f16 v[48:63], v[150:153], v[174:177], v[48:63]
	s_waitcnt lgkmcnt(1)
	v_mfma_f32_32x32x16_f16 v[16:31], v[150:153], v[182:185], v[16:31]
	ds_read_b128 v[150:153], v104 offset:4608
	ds_read_b128 v[190:193], v104 offset:4640
	s_waitcnt lgkmcnt(1)
	v_mfma_f32_32x32x16_f16 v[64:79], v[150:153], v[154:157], v[64:79]
	v_mfma_f32_32x32x16_f16 v[32:47], v[150:153], v[174:177], v[32:47]
	v_mfma_f32_32x32x16_f16 v[0:15], v[150:153], v[182:185], v[0:15]
	v_mfma_f32_32x32x16_f16 v[80:95], v[158:161], v[170:173], v[80:95]
	v_mfma_f32_32x32x16_f16 v[48:63], v[158:161], v[178:181], v[48:63]
	v_mfma_f32_32x32x16_f16 v[16:31], v[158:161], v[186:189], v[16:31]
	s_waitcnt lgkmcnt(0)
	v_mfma_f32_32x32x16_f16 v[64:79], v[190:193], v[170:173], v[64:79]
	ds_read_b128 v[150:153], v104 offset:64
	ds_read_b128 v[154:157], v116 offset:36928
	ds_read_b128 v[158:161], v104 offset:96
	ds_read_b128 v[170:173], v116 offset:36960
	v_mfma_f32_32x32x16_f16 v[32:47], v[190:193], v[178:181], v[32:47]
	ds_read_b128 v[174:177], v116 offset:41536
	ds_read_b128 v[178:181], v116 offset:41568
	v_mfma_f32_32x32x16_f16 v[0:15], v[190:193], v[186:189], v[0:15]
	ds_read_b128 v[182:185], v116 offset:46144
	ds_read_b128 v[186:189], v116 offset:46176
	s_waitcnt lgkmcnt(6)
	v_mfma_f32_32x32x16_f16 v[80:95], v[150:153], v[154:157], v[80:95]
	s_waitcnt lgkmcnt(3)
	v_mfma_f32_32x32x16_f16 v[48:63], v[150:153], v[174:177], v[48:63]
	s_waitcnt lgkmcnt(1)
	v_mfma_f32_32x32x16_f16 v[16:31], v[150:153], v[182:185], v[16:31]
	ds_read_b128 v[150:153], v104 offset:4672
	ds_read_b128 v[190:193], v104 offset:4704
	s_waitcnt lgkmcnt(0)
	s_barrier
	v_mfma_f32_32x32x16_f16 v[64:79], v[150:153], v[154:157], v[64:79]
	v_mfma_f32_32x32x16_f16 v[32:47], v[150:153], v[174:177], v[32:47]
	v_mfma_f32_32x32x16_f16 v[0:15], v[150:153], v[182:185], v[0:15]
	v_mfma_f32_32x32x16_f16 v[80:95], v[158:161], v[170:173], v[80:95]
	v_mfma_f32_32x32x16_f16 v[48:63], v[158:161], v[178:181], v[48:63]
	v_mfma_f32_32x32x16_f16 v[16:31], v[158:161], v[186:189], v[16:31]
	v_mfma_f32_32x32x16_f16 v[64:79], v[190:193], v[170:173], v[64:79]
	v_mfma_f32_32x32x16_f16 v[32:47], v[190:193], v[178:181], v[32:47]
	global_load_dwordx4 v[150:153], v[96:97], off offset:1664
	global_load_dwordx4 v[154:157], v[98:99], off offset:1664
	global_load_dwordx4 v[158:161], v[100:101], off offset:1664
	global_load_dwordx4 v[170:173], v[102:103], off offset:1664
	global_load_dwordx4 v[174:177], v[106:107], off offset:1664
	global_load_dwordx4 v[178:181], v[108:109], off offset:1664
	global_load_dwordx4 v[182:185], v[110:111], off offset:1664
	v_mfma_f32_32x32x16_f16 v[0:15], v[190:193], v[186:189], v[0:15]
	s_waitcnt vmcnt(13)
	ds_write_b128 v114, v[122:125]
	s_waitcnt vmcnt(12)
	ds_write_b128 v115, v[126:129]
	s_waitcnt vmcnt(11)
	ds_write_b128 v114, v[130:133] offset:18432
	s_waitcnt vmcnt(10)
	ds_write_b128 v117, v[134:137]
	s_waitcnt vmcnt(9)
	ds_write_b128 v114, v[138:141] offset:36864
	s_waitcnt vmcnt(8)
	ds_write_b128 v115, v[142:145] offset:36864
	s_waitcnt vmcnt(7)
	ds_write_b128 v114, v[146:149] offset:55296
	ds_read_b128 v[122:125], v104 offset:64512
	ds_read_b128 v[126:129], v105
	ds_read_b128 v[130:133], v104 offset:64544
	ds_read_b128 v[134:137], v105 offset:32
	ds_read_b128 v[138:141], v105 offset:4608
	ds_read_b128 v[142:145], v105 offset:4640
	ds_read_b128 v[146:149], v105 offset:9216
	ds_read_b128 v[186:189], v105 offset:9248
	s_waitcnt lgkmcnt(6)
	v_mfma_f32_32x32x16_f16 v[80:95], v[122:125], v[126:129], v[80:95]
	s_waitcnt lgkmcnt(3)
	v_mfma_f32_32x32x16_f16 v[48:63], v[122:125], v[138:141], v[48:63]
	s_waitcnt lgkmcnt(1)
	v_mfma_f32_32x32x16_f16 v[16:31], v[122:125], v[146:149], v[16:31]
	ds_read_b128 v[122:125], v169 offset:64512
	ds_read_b128 v[190:193], v169 offset:64544
	s_waitcnt lgkmcnt(1)
	v_mfma_f32_32x32x16_f16 v[64:79], v[122:125], v[126:129], v[64:79]
	v_mfma_f32_32x32x16_f16 v[32:47], v[122:125], v[138:141], v[32:47]
	v_mfma_f32_32x32x16_f16 v[0:15], v[122:125], v[146:149], v[0:15]
	v_mfma_f32_32x32x16_f16 v[80:95], v[130:133], v[134:137], v[80:95]
	v_mfma_f32_32x32x16_f16 v[48:63], v[130:133], v[142:145], v[48:63]
	v_mfma_f32_32x32x16_f16 v[16:31], v[130:133], v[186:189], v[16:31]
	s_waitcnt lgkmcnt(0)
	v_mfma_f32_32x32x16_f16 v[64:79], v[190:193], v[134:137], v[64:79]
	ds_read_b128 v[122:125], v104 offset:64576
	ds_read_b128 v[126:129], v105 offset:64
	ds_read_b128 v[130:133], v104 offset:64608
	ds_read_b128 v[134:137], v105 offset:96
	v_mfma_f32_32x32x16_f16 v[32:47], v[190:193], v[142:145], v[32:47]
	ds_read_b128 v[138:141], v105 offset:4672
	ds_read_b128 v[142:145], v105 offset:4704
	v_mfma_f32_32x32x16_f16 v[0:15], v[190:193], v[186:189], v[0:15]
	ds_read_b128 v[146:149], v105 offset:9280
	ds_read_b128 v[186:189], v105 offset:9312
	s_waitcnt lgkmcnt(6)
	v_mfma_f32_32x32x16_f16 v[80:95], v[122:125], v[126:129], v[80:95]
	s_waitcnt lgkmcnt(3)
	v_mfma_f32_32x32x16_f16 v[48:63], v[122:125], v[138:141], v[48:63]
	s_waitcnt lgkmcnt(1)
	v_mfma_f32_32x32x16_f16 v[16:31], v[122:125], v[146:149], v[16:31]
	ds_read_b128 v[122:125], v169 offset:64576
	ds_read_b128 v[190:193], v169 offset:64608
	s_waitcnt lgkmcnt(0)
	s_barrier
	v_mfma_f32_32x32x16_f16 v[64:79], v[122:125], v[126:129], v[64:79]
	v_mfma_f32_32x32x16_f16 v[32:47], v[122:125], v[138:141], v[32:47]
	v_mfma_f32_32x32x16_f16 v[0:15], v[122:125], v[146:149], v[0:15]
	v_mfma_f32_32x32x16_f16 v[80:95], v[130:133], v[134:137], v[80:95]
	v_mfma_f32_32x32x16_f16 v[48:63], v[130:133], v[142:145], v[48:63]
	v_mfma_f32_32x32x16_f16 v[16:31], v[130:133], v[186:189], v[16:31]
	v_mfma_f32_32x32x16_f16 v[64:79], v[190:193], v[134:137], v[64:79]
	v_mfma_f32_32x32x16_f16 v[32:47], v[190:193], v[142:145], v[32:47]
	global_load_dwordx4 v[122:125], v[96:97], off offset:1792
	global_load_dwordx4 v[126:129], v[98:99], off offset:1792
	global_load_dwordx4 v[130:133], v[100:101], off offset:1792
	global_load_dwordx4 v[134:137], v[102:103], off offset:1792
	global_load_dwordx4 v[138:141], v[106:107], off offset:1792
	global_load_dwordx4 v[142:145], v[108:109], off offset:1792
	global_load_dwordx4 v[146:149], v[110:111], off offset:1792
	v_mfma_f32_32x32x16_f16 v[0:15], v[190:193], v[186:189], v[0:15]
	s_waitcnt vmcnt(13)
	ds_write_b128 v114, v[150:153] offset:64512
	s_waitcnt vmcnt(12)
	ds_write_b128 v115, v[154:157] offset:64512
	s_waitcnt vmcnt(11)
	ds_write_b128 v118, v[158:161] offset:64512
	s_waitcnt vmcnt(10)
	ds_write_b128 v117, v[170:173] offset:64512
	s_waitcnt vmcnt(9)
	ds_write_b128 v119, v[174:177]
	s_waitcnt vmcnt(8)
	ds_write_b128 v120, v[178:181]
	s_waitcnt vmcnt(7)
	ds_write_b128 v119, v[182:185] offset:18432
	ds_read_b128 v[150:153], v104
	ds_read_b128 v[154:157], v116 offset:36864
	ds_read_b128 v[158:161], v104 offset:32
	ds_read_b128 v[170:173], v116 offset:36896
	ds_read_b128 v[174:177], v116 offset:41472
	ds_read_b128 v[178:181], v116 offset:41504
	ds_read_b128 v[182:185], v116 offset:46080
	ds_read_b128 v[186:189], v116 offset:46112
	s_waitcnt lgkmcnt(6)
	v_mfma_f32_32x32x16_f16 v[80:95], v[150:153], v[154:157], v[80:95]
	s_waitcnt lgkmcnt(3)
	v_mfma_f32_32x32x16_f16 v[48:63], v[150:153], v[174:177], v[48:63]
	s_waitcnt lgkmcnt(1)
	v_mfma_f32_32x32x16_f16 v[16:31], v[150:153], v[182:185], v[16:31]
	ds_read_b128 v[150:153], v104 offset:4608
	ds_read_b128 v[190:193], v104 offset:4640
	s_waitcnt lgkmcnt(1)
	v_mfma_f32_32x32x16_f16 v[64:79], v[150:153], v[154:157], v[64:79]
	v_mfma_f32_32x32x16_f16 v[32:47], v[150:153], v[174:177], v[32:47]
	v_mfma_f32_32x32x16_f16 v[0:15], v[150:153], v[182:185], v[0:15]
	v_mfma_f32_32x32x16_f16 v[80:95], v[158:161], v[170:173], v[80:95]
	v_mfma_f32_32x32x16_f16 v[48:63], v[158:161], v[178:181], v[48:63]
	v_mfma_f32_32x32x16_f16 v[16:31], v[158:161], v[186:189], v[16:31]
	s_waitcnt lgkmcnt(0)
	v_mfma_f32_32x32x16_f16 v[64:79], v[190:193], v[170:173], v[64:79]
	ds_read_b128 v[150:153], v104 offset:64
	ds_read_b128 v[154:157], v116 offset:36928
	ds_read_b128 v[158:161], v104 offset:96
	ds_read_b128 v[170:173], v116 offset:36960
	v_mfma_f32_32x32x16_f16 v[32:47], v[190:193], v[178:181], v[32:47]
	ds_read_b128 v[174:177], v116 offset:41536
	ds_read_b128 v[178:181], v116 offset:41568
	v_mfma_f32_32x32x16_f16 v[0:15], v[190:193], v[186:189], v[0:15]
	ds_read_b128 v[182:185], v116 offset:46144
	ds_read_b128 v[186:189], v116 offset:46176
	s_waitcnt lgkmcnt(6)
	v_mfma_f32_32x32x16_f16 v[80:95], v[150:153], v[154:157], v[80:95]
	s_waitcnt lgkmcnt(3)
	v_mfma_f32_32x32x16_f16 v[48:63], v[150:153], v[174:177], v[48:63]
	s_waitcnt lgkmcnt(1)
	v_mfma_f32_32x32x16_f16 v[16:31], v[150:153], v[182:185], v[16:31]
	ds_read_b128 v[150:153], v104 offset:4672
	ds_read_b128 v[190:193], v104 offset:4704
	s_waitcnt lgkmcnt(0)
	s_barrier
	v_mfma_f32_32x32x16_f16 v[64:79], v[150:153], v[154:157], v[64:79]
	v_mfma_f32_32x32x16_f16 v[32:47], v[150:153], v[174:177], v[32:47]
	v_mfma_f32_32x32x16_f16 v[0:15], v[150:153], v[182:185], v[0:15]
	v_mfma_f32_32x32x16_f16 v[80:95], v[158:161], v[170:173], v[80:95]
	v_mfma_f32_32x32x16_f16 v[48:63], v[158:161], v[178:181], v[48:63]
	v_mfma_f32_32x32x16_f16 v[16:31], v[158:161], v[186:189], v[16:31]
	v_mfma_f32_32x32x16_f16 v[64:79], v[190:193], v[170:173], v[64:79]
	global_load_dwordx4 v[150:153], v[96:97], off offset:1920
	s_nop 0
	global_load_dwordx4 v[96:99], v[98:99], off offset:1920
	s_nop 0
	global_load_dwordx4 v[154:157], v[100:101], off offset:1920
	s_nop 0
	global_load_dwordx4 v[100:103], v[102:103], off offset:1920
	s_nop 0
	global_load_dwordx4 v[158:161], v[106:107], off offset:1920
	s_nop 0
	global_load_dwordx4 v[106:109], v[108:109], off offset:1920
	s_nop 0
	global_load_dwordx4 v[170:173], v[110:111], off offset:1920
	v_mfma_f32_32x32x16_f16 v[32:47], v[190:193], v[178:181], v[32:47]
	v_mfma_f32_32x32x16_f16 v[0:15], v[190:193], v[186:189], v[0:15]
	s_waitcnt vmcnt(13)
	ds_write_b128 v114, v[122:125]
	s_waitcnt vmcnt(12)
	ds_write_b128 v115, v[126:129]
	s_waitcnt vmcnt(11)
	ds_write_b128 v114, v[130:133] offset:18432
	s_waitcnt vmcnt(10)
	ds_write_b128 v117, v[134:137]
	s_waitcnt vmcnt(9)
	ds_write_b128 v114, v[138:141] offset:36864
	s_waitcnt vmcnt(8)
	ds_write_b128 v115, v[142:145] offset:36864
	s_waitcnt vmcnt(7)
	ds_write_b128 v114, v[146:149] offset:55296
	ds_read_b128 v[122:125], v104 offset:64512
	ds_read_b128 v[126:129], v105
	ds_read_b128 v[130:133], v104 offset:64544
	ds_read_b128 v[134:137], v105 offset:32
	ds_read_b128 v[138:141], v105 offset:4608
	ds_read_b128 v[142:145], v105 offset:4640
	ds_read_b128 v[146:149], v105 offset:9216
	ds_read_b128 v[174:177], v105 offset:9248
	s_waitcnt lgkmcnt(6)
	v_mfma_f32_32x32x16_f16 v[80:95], v[122:125], v[126:129], v[80:95]
	s_waitcnt lgkmcnt(3)
	v_mfma_f32_32x32x16_f16 v[48:63], v[122:125], v[138:141], v[48:63]
	s_waitcnt lgkmcnt(1)
	v_mfma_f32_32x32x16_f16 v[16:31], v[122:125], v[146:149], v[16:31]
	ds_read_b128 v[122:125], v169 offset:64512
	ds_read_b128 v[178:181], v169 offset:64544
	s_waitcnt lgkmcnt(1)
	v_mfma_f32_32x32x16_f16 v[64:79], v[122:125], v[126:129], v[64:79]
	v_mfma_f32_32x32x16_f16 v[32:47], v[122:125], v[138:141], v[32:47]
	v_mfma_f32_32x32x16_f16 v[0:15], v[122:125], v[146:149], v[0:15]
	v_mfma_f32_32x32x16_f16 v[80:95], v[130:133], v[134:137], v[80:95]
	v_mfma_f32_32x32x16_f16 v[48:63], v[130:133], v[142:145], v[48:63]
	v_mfma_f32_32x32x16_f16 v[16:31], v[130:133], v[174:177], v[16:31]
	s_waitcnt lgkmcnt(0)
	v_mfma_f32_32x32x16_f16 v[64:79], v[178:181], v[134:137], v[64:79]
	ds_read_b128 v[122:125], v104 offset:64576
	ds_read_b128 v[126:129], v105 offset:64
	ds_read_b128 v[130:133], v104 offset:64608
	ds_read_b128 v[134:137], v105 offset:96
	v_mfma_f32_32x32x16_f16 v[32:47], v[178:181], v[142:145], v[32:47]
	ds_read_b128 v[138:141], v105 offset:4672
	ds_read_b128 v[142:145], v105 offset:4704
	v_mfma_f32_32x32x16_f16 v[0:15], v[178:181], v[174:177], v[0:15]
	ds_read_b128 v[146:149], v105 offset:9280
	ds_read_b128 v[174:177], v105 offset:9312
	s_waitcnt lgkmcnt(6)
	v_mfma_f32_32x32x16_f16 v[80:95], v[122:125], v[126:129], v[80:95]
	s_waitcnt lgkmcnt(3)
	v_mfma_f32_32x32x16_f16 v[48:63], v[122:125], v[138:141], v[48:63]
	s_waitcnt lgkmcnt(1)
	v_mfma_f32_32x32x16_f16 v[16:31], v[122:125], v[146:149], v[16:31]
	ds_read_b128 v[122:125], v169 offset:64576
	ds_read_b128 v[178:181], v169 offset:64608
	s_waitcnt lgkmcnt(0)
	s_barrier
	v_mfma_f32_32x32x16_f16 v[64:79], v[122:125], v[126:129], v[64:79]
	v_mfma_f32_32x32x16_f16 v[32:47], v[122:125], v[138:141], v[32:47]
	v_mfma_f32_32x32x16_f16 v[0:15], v[122:125], v[146:149], v[0:15]
	v_mfma_f32_32x32x16_f16 v[80:95], v[130:133], v[134:137], v[80:95]
	v_mfma_f32_32x32x16_f16 v[48:63], v[130:133], v[142:145], v[48:63]
	v_mfma_f32_32x32x16_f16 v[16:31], v[130:133], v[174:177], v[16:31]
	v_mfma_f32_32x32x16_f16 v[64:79], v[178:181], v[134:137], v[64:79]
	v_mfma_f32_32x32x16_f16 v[32:47], v[178:181], v[142:145], v[32:47]
	v_mfma_f32_32x32x16_f16 v[0:15], v[178:181], v[174:177], v[0:15]
	s_waitcnt vmcnt(6)
	ds_write_b128 v114, v[150:153] offset:64512
	s_waitcnt vmcnt(5)
	ds_write_b128 v115, v[96:99] offset:64512
	s_waitcnt vmcnt(4)
	ds_write_b128 v118, v[154:157] offset:64512
	s_waitcnt vmcnt(3)
	ds_write_b128 v117, v[100:103] offset:64512
	s_waitcnt vmcnt(2)
	ds_write_b128 v119, v[158:161]
	s_waitcnt vmcnt(1)
	ds_write_b128 v120, v[106:109]
	s_waitcnt vmcnt(0)
	ds_write_b128 v119, v[170:173] offset:18432
	ds_read_b128 v[96:99], v104
	ds_read_b128 v[100:103], v116 offset:36864
	ds_read_b128 v[106:109], v104 offset:32
	ds_read_b128 v[118:121], v116 offset:36896
	ds_read_b128 v[122:125], v116 offset:41472
	ds_read_b128 v[126:129], v116 offset:41504
	ds_read_b128 v[130:133], v116 offset:46080
	ds_read_b128 v[134:137], v116 offset:46112
	s_waitcnt lgkmcnt(6)
	v_mfma_f32_32x32x16_f16 v[80:95], v[96:99], v[100:103], v[80:95]
	s_waitcnt lgkmcnt(3)
	v_mfma_f32_32x32x16_f16 v[48:63], v[96:99], v[122:125], v[48:63]
	s_waitcnt lgkmcnt(1)
	v_mfma_f32_32x32x16_f16 v[16:31], v[96:99], v[130:133], v[16:31]
	ds_read_b128 v[96:99], v104 offset:4608
	ds_read_b128 v[138:141], v104 offset:4640
	v_mfma_f32_32x32x16_f16 v[80:95], v[106:109], v[118:121], v[80:95]
	v_mfma_f32_32x32x16_f16 v[48:63], v[106:109], v[126:129], v[48:63]
	s_waitcnt lgkmcnt(2)
	v_mfma_f32_32x32x16_f16 v[16:31], v[106:109], v[134:137], v[16:31]
	v_lshlrev_b32_e32 v106, 5, v167
	v_and_b32_e32 v106, 0xf8a0, v106
	v_or_b32_e32 v107, v106, v113
	v_or_b32_e32 v108, v106, v112
	v_lshlrev_b32_e32 v107, 2, v107
	v_lshlrev_b32_e32 v108, 2, v108
	s_waitcnt lgkmcnt(1)
	v_mfma_f32_32x32x16_f16 v[64:79], v[96:99], v[100:103], v[64:79]
	v_mfma_f32_32x32x16_f16 v[32:47], v[96:99], v[122:125], v[32:47]
	v_mfma_f32_32x32x16_f16 v[0:15], v[96:99], v[130:133], v[0:15]
	ds_read_b128 v[96:99], v104 offset:64
	ds_read_b128 v[100:103], v104 offset:96
	ds_read_b128 v[122:125], v104 offset:4672
	ds_read_b128 v[130:133], v104 offset:4704
	ds_read_b128 v[142:145], v116 offset:36928
	ds_read_b128 v[146:149], v116 offset:36960
	ds_read_b128 v[150:153], v116 offset:41536
	ds_read_b128 v[154:157], v116 offset:41568
	ds_read_b128 v[158:161], v116 offset:46144
	ds_read_b128 v[114:117], v116 offset:46176
	s_waitcnt lgkmcnt(0)
	s_barrier
	global_load_dword v200, v107, s[8:9]
	global_load_dword v201, v107, s[10:11]
	global_load_dword v198, v107, s[8:9] offset:256
	global_load_dword v199, v107, s[10:11] offset:256
	global_load_dword v196, v107, s[8:9] offset:1024
	global_load_dword v197, v107, s[10:11] offset:1024
	global_load_dword v194, v107, s[8:9] offset:1280
	global_load_dword v195, v107, s[10:11] offset:1280
	global_load_dword v233, v108, s[8:9]
	global_load_dword v234, v108, s[10:11]
	global_load_dword v231, v108, s[8:9] offset:256
	global_load_dword v232, v108, s[10:11] offset:256
	global_load_dword v229, v108, s[8:9] offset:1024
	global_load_dword v230, v108, s[10:11] offset:1024
	global_load_dword v226, v108, s[8:9] offset:1280
	global_load_dword v227, v108, s[10:11] offset:1280
	global_load_dword v192, v107, s[8:9] offset:2048
	global_load_dword v193, v107, s[10:11] offset:2048
	global_load_dword v190, v107, s[8:9] offset:2304
	global_load_dword v191, v107, s[10:11] offset:2304
	global_load_dword v188, v107, s[8:9] offset:3072
	global_load_dword v189, v107, s[10:11] offset:3072
	global_load_dword v186, v107, s[8:9] offset:3328
	global_load_dword v187, v107, s[10:11] offset:3328
	v_mfma_f32_32x32x16_f16 v[80:95], v[96:99], v[142:145], v[80:95]
	v_or_b32_e32 v107, 0x400, v106
	global_load_dword v224, v108, s[8:9] offset:2048
	global_load_dword v225, v108, s[10:11] offset:2048
	global_load_dword v222, v108, s[8:9] offset:2304
	global_load_dword v223, v108, s[10:11] offset:2304
	global_load_dword v220, v108, s[8:9] offset:3072
	global_load_dword v221, v108, s[10:11] offset:3072
	global_load_dword v218, v108, s[8:9] offset:3328
	global_load_dword v219, v108, s[10:11] offset:3328
	v_or_b32_e32 v108, v107, v113
	v_or_b32_e32 v107, v107, v112
	v_lshlrev_b32_e32 v108, 2, v108
	v_lshlrev_b32_e32 v107, 2, v107
	global_load_dword v184, v108, s[8:9]
	global_load_dword v185, v108, s[10:11]
	v_mfma_f32_32x32x16_f16 v[48:63], v[96:99], v[150:153], v[48:63]
	global_load_dword v216, v107, s[8:9]
	global_load_dword v217, v107, s[10:11]
	v_mfma_f32_32x32x16_f16 v[16:31], v[96:99], v[158:161], v[16:31]
	v_or_b32_e32 v96, 0x440, v106
	v_or_b32_e32 v97, v96, v113
	v_or_b32_e32 v96, v96, v112
	v_lshlrev_b32_e32 v97, 2, v97
	v_lshlrev_b32_e32 v96, 2, v96
	global_load_dword v182, v97, s[8:9]
	global_load_dword v183, v97, s[10:11]
	global_load_dword v214, v96, s[8:9]
	global_load_dword v215, v96, s[10:11]
	v_or_b32_e32 v96, 0x500, v106
	v_or_b32_e32 v97, v96, v113
	v_or_b32_e32 v96, v96, v112
	v_lshlrev_b32_e32 v97, 2, v97
	v_lshlrev_b32_e32 v96, 2, v96
	global_load_dword v180, v97, s[8:9]
	global_load_dword v181, v97, s[10:11]
	global_load_dword v212, v96, s[8:9]
	global_load_dword v213, v96, s[10:11]
	v_or_b32_e32 v96, 0x540, v106
	v_or_b32_e32 v97, v96, v113
	v_or_b32_e32 v96, v96, v112
	v_lshlrev_b32_e32 v97, 2, v97
	v_lshlrev_b32_e32 v96, 2, v96
	global_load_dword v178, v97, s[8:9]
	global_load_dword v179, v97, s[10:11]
	global_load_dword v210, v96, s[8:9]
	global_load_dword v211, v96, s[10:11]
	v_or_b32_e32 v96, 0x600, v106
	v_or_b32_e32 v97, v96, v113
	v_or_b32_e32 v96, v96, v112
	v_lshlrev_b32_e32 v97, 2, v97
	v_lshlrev_b32_e32 v96, 2, v96
	global_load_dword v176, v97, s[8:9]
	global_load_dword v177, v97, s[10:11]
	global_load_dword v208, v96, s[8:9]
	global_load_dword v209, v96, s[10:11]
	v_or_b32_e32 v96, 0x640, v106
	v_or_b32_e32 v97, v96, v113
	v_or_b32_e32 v96, v96, v112
	v_lshlrev_b32_e32 v97, 2, v97
	v_lshlrev_b32_e32 v96, 2, v96
	global_load_dword v174, v97, s[8:9]
	global_load_dword v175, v97, s[10:11]
	global_load_dword v206, v96, s[8:9]
	global_load_dword v207, v96, s[10:11]
	v_or_b32_e32 v96, 0x700, v106
	v_or_b32_e32 v97, v96, v113
	v_or_b32_e32 v96, v96, v112
	v_lshlrev_b32_e32 v97, 2, v97
	v_lshlrev_b32_e32 v96, 2, v96
	global_load_dword v172, v97, s[8:9]
	global_load_dword v173, v97, s[10:11]
	global_load_dword v204, v96, s[8:9]
	global_load_dword v205, v96, s[10:11]
	v_or_b32_e32 v96, 0x740, v106
	v_or_b32_e32 v97, v96, v113
	v_or_b32_e32 v96, v96, v112
	v_lshlrev_b32_e32 v97, 2, v97
	v_lshlrev_b32_e32 v96, 2, v96
	global_load_dword v170, v97, s[8:9]
	global_load_dword v171, v97, s[10:11]
	global_load_dword v202, v96, s[8:9]
	global_load_dword v203, v96, s[10:11]
	v_mfma_f32_32x32x16_f16 v[64:79], v[138:141], v[118:121], v[64:79]
	v_mfma_f32_32x32x16_f16 v[32:47], v[138:141], v[126:129], v[32:47]
	v_mfma_f32_32x32x16_f16 v[0:15], v[138:141], v[134:137], v[0:15]
	v_mfma_f32_32x32x16_f16 v[64:79], v[122:125], v[142:145], v[64:79]
	v_mfma_f32_32x32x16_f16 v[32:47], v[122:125], v[150:153], v[32:47]
	v_mfma_f32_32x32x16_f16 v[0:15], v[122:125], v[158:161], v[0:15]
	v_mfma_f32_32x32x16_f16 v[80:95], v[100:103], v[146:149], v[80:95]
	v_mfma_f32_32x32x16_f16 v[48:63], v[100:103], v[154:157], v[48:63]
	v_mfma_f32_32x32x16_f16 v[16:31], v[100:103], v[114:117], v[16:31]
	v_mfma_f32_32x32x16_f16 v[64:79], v[130:133], v[146:149], v[64:79]
	v_mfma_f32_32x32x16_f16 v[32:47], v[130:133], v[154:157], v[32:47]
	v_mfma_f32_32x32x16_f16 v[0:15], v[130:133], v[114:117], v[0:15]
	ds_read_b128 v[128:131], v104 offset:64512
	ds_read_b128 v[106:109], v105
	ds_read_b128 v[100:103], v169 offset:64512
	ds_read_b128 v[132:135], v104 offset:64544
	ds_read_b128 v[160:163], v105 offset:32
	v_mbcnt_lo_u32_b32 v110, -1, 0
	s_waitcnt lgkmcnt(3)
	v_mfma_f32_32x32x16_f16 v[80:95], v[128:131], v[106:109], v[80:95]
	v_mbcnt_hi_u32_b32 v110, -1, v110
	v_and_b32_e32 v111, 64, v110
	ds_read_b128 v[96:99], v169 offset:64544
	ds_read_b128 v[148:151], v105 offset:4608
	ds_read_b128 v[144:147], v105 offset:4640
	v_add_u32_e32 v111, 64, v111
	ds_read_b128 v[140:143], v104 offset:64576
	ds_read_b128 v[136:139], v104 offset:64608
	ds_read_b128 v[124:127], v105 offset:9216
	ds_read_b128 v[120:123], v105 offset:9248
	s_lshr_b32 s0, s0, 7
	s_and_b32 s8, s0, 0xfffff0
	s_waitcnt lgkmcnt(7)
	v_mfma_f32_32x32x16_f16 v[80:95], v[132:135], v[160:163], v[80:95]
	s_bfe_u32 s2, s14, 0x40006
	s_cmpk_lt_u32 s14, 0x400
	s_cselect_b64 s[0:1], -1, 0
	s_and_b32 s9, s14, 0x7ffffc00
	v_mov_b32_e32 v228, 0x3e38aa3b
	s_cmpk_eq_i32 s9, 0x400
	s_cselect_b32 s9, s6, s12
	v_mfma_f32_32x32x16_f16 v[64:79], v[100:103], v[106:109], v[64:79]
	v_xor_b32_e32 v106, 1, v110
	v_cmp_lt_i32_e32 vcc, v106, v111
	s_cselect_b32 s10, s7, s13
	s_nop 0
	v_cndmask_b32_e32 v235, v110, v106, vcc
	ds_read_b128 v[236:239], v105 offset:64
	ds_read_b128 v[240:243], v105 offset:96
	ds_read_b128 v[156:159], v105 offset:4672
	ds_read_b128 v[152:155], v105 offset:4704
	ds_read_b128 v[112:115], v105 offset:9280
	ds_read_b128 v[104:107], v105 offset:9312
	ds_read_b128 v[116:119], v169 offset:64576
	ds_read_b128 v[108:111], v169 offset:64608
	v_cmp_eq_u32_e32 vcc, 0, v164
	s_waitcnt lgkmcnt(7)
	v_mfma_f32_32x32x16_f16 v[80:95], v[140:143], v[236:239], v[80:95]
	s_waitcnt lgkmcnt(0)
	s_barrier
	v_lshlrev_b32_e32 v169, 2, v235
	v_cndmask_b32_e64 v235, 1.0, v228, s[0:1]
	s_and_b64 s[0:1], s[0:1], exec
	s_cselect_b32 s16, s5, s10
	v_mfma_f32_32x32x16_f16 v[80:95], v[136:139], v[240:243], v[80:95]
	s_cselect_b32 s9, s4, s9
	s_cmpk_lt_u32 s14, 0x800
	s_cselect_b64 s[0:1], -1, 0
	s_waitcnt vmcnt(62)
	v_cndmask_b32_e64 v244, 0, v201, s[0:1]
	s_nop 6
	v_cndmask_b32_e32 v164, v80, v81, vcc
	ds_bpermute_b32 v164, v169, v164
	s_or_b32 s2, s2, s8
	s_lshl_b64 s[10:11], s[2:3], 18
	s_add_u32 s10, s9, s10
	s_addc_u32 s11, s16, s11
	s_waitcnt lgkmcnt(0)
	v_cndmask_b32_e32 v81, v81, v164, vcc
	v_cndmask_b32_e32 v80, v164, v80, vcc
	v_cndmask_b32_e64 v164, 1.0, v200, s[0:1]
	v_mul_f32_e32 v245, v81, v244
	v_fma_f32 v245, v80, v164, -v245
	v_mul_f32_e32 v80, v80, v244
	v_fmac_f32_e32 v80, v81, v164
	v_bitop3_b32 v81, s15, 62, v166 bitop3:0xc8
	v_lshlrev_b32_e32 v164, 1, v81
	v_mul_f32_e32 v81, v235, v245
	v_mul_f32_e32 v80, v235, v80
	v_cvt_pk_f16_f32 v246, v81, v80
	v_lshlrev_b32_e32 v80, 7, v167
	v_and_b32_e32 v80, 0x3e280, v80
	v_mov_b32_e32 v81, v165
	v_lshl_add_u64 v[166:167], s[10:11], 0, v[164:165]
	v_lshl_add_u64 v[244:245], v[166:167], 0, v[80:81]
	global_store_dword v[244:245], v246, off
	s_waitcnt vmcnt(61)
	v_cndmask_b32_e64 v247, 0, v199, s[0:1]
	v_cndmask_b32_e32 v246, v82, v83, vcc
	ds_bpermute_b32 v246, v169, v246
	v_mfma_f32_32x32x16_f16 v[64:79], v[96:99], v[160:163], v[64:79]
	s_add_i32 s2, s14, 32
	s_bfe_u32 s9, s2, 0x40006
	s_cmpk_lt_u32 s14, 0x3e0
	s_waitcnt lgkmcnt(0)
	v_cndmask_b32_e32 v83, v83, v246, vcc
	v_cndmask_b32_e32 v82, v246, v82, vcc
	v_cndmask_b32_e64 v246, 1.0, v198, s[0:1]
	v_mul_f32_e32 v248, v83, v247
	v_fma_f32 v248, v82, v246, -v248
	v_mul_f32_e32 v82, v82, v247
	v_fmac_f32_e32 v82, v83, v246
	v_mul_f32_e32 v83, v235, v248
	v_mul_f32_e32 v82, v235, v82
	v_cvt_pk_f16_f32 v82, v83, v82
	global_store_dword v[244:245], v82, off offset:256
	v_mov_b32_e32 v82, v85
	s_waitcnt vmcnt(60)
	v_cndmask_b32_e64 v85, 0, v197, s[0:1]
	v_cndmask_b32_e32 v83, v84, v82, vcc
	ds_bpermute_b32 v83, v169, v83
	v_mfma_f32_32x32x16_f16 v[64:79], v[116:119], v[236:239], v[64:79]
	s_waitcnt lgkmcnt(0)
	v_cndmask_b32_e32 v82, v82, v83, vcc
	v_cndmask_b32_e32 v83, v83, v84, vcc
	v_cndmask_b32_e64 v84, 1.0, v196, s[0:1]
	v_mul_f32_e32 v246, v82, v85
	v_fma_f32 v246, v83, v84, -v246
	v_mul_f32_e32 v83, v83, v85
	v_fmac_f32_e32 v83, v82, v84
	v_mul_f32_e32 v82, v235, v246
	v_mul_f32_e32 v83, v235, v83
	v_cvt_pk_f16_f32 v82, v82, v83
	global_store_dword v[244:245], v82, off offset:1024
	v_mov_b32_e32 v82, v87
	s_waitcnt vmcnt(59)
	v_cndmask_b32_e64 v85, 0, v195, s[0:1]
	v_cndmask_b32_e32 v83, v86, v82, vcc
	ds_bpermute_b32 v83, v169, v83
	v_cndmask_b32_e64 v84, 1.0, v194, s[0:1]
	v_mfma_f32_32x32x16_f16 v[64:79], v[108:111], v[240:243], v[64:79]
	s_waitcnt lgkmcnt(0)
	v_cndmask_b32_e32 v82, v82, v83, vcc
	v_cndmask_b32_e32 v83, v83, v86, vcc
	v_mul_f32_e32 v86, v82, v85
	v_fma_f32 v86, v83, v84, -v86
	v_mul_f32_e32 v83, v83, v85
	v_fmac_f32_e32 v83, v82, v84
	v_mul_f32_e32 v82, v235, v86
	v_mul_f32_e32 v83, v235, v83
	v_cvt_pk_f16_f32 v82, v82, v83
	global_store_dword v[244:245], v82, off offset:1280
	v_mov_b32_e32 v82, v89
	s_waitcnt vmcnt(50)
	v_cndmask_b32_e64 v85, 0, v193, s[0:1]
	v_cndmask_b32_e32 v83, v88, v82, vcc
	ds_bpermute_b32 v83, v169, v83
	v_cndmask_b32_e64 v84, 1.0, v192, s[0:1]
	v_mfma_f32_32x32x16_f16 v[48:63], v[128:131], v[148:151], v[48:63]
	s_waitcnt lgkmcnt(0)
	v_cndmask_b32_e32 v82, v82, v83, vcc
	v_cndmask_b32_e32 v83, v83, v88, vcc
	v_mul_f32_e32 v86, v82, v85
	v_fma_f32 v86, v83, v84, -v86
	v_mul_f32_e32 v83, v83, v85
	v_fmac_f32_e32 v83, v82, v84
	v_mul_f32_e32 v82, v235, v86
	v_mul_f32_e32 v83, v235, v83
	v_cvt_pk_f16_f32 v82, v82, v83
	global_store_dword v[244:245], v82, off offset:2048
	v_mov_b32_e32 v82, v91
	s_waitcnt vmcnt(49)
	v_cndmask_b32_e64 v85, 0, v191, s[0:1]
	v_cndmask_b32_e32 v83, v90, v82, vcc
	ds_bpermute_b32 v83, v169, v83
	v_cndmask_b32_e64 v84, 1.0, v190, s[0:1]
	v_mfma_f32_32x32x16_f16 v[48:63], v[132:135], v[144:147], v[48:63]
	s_waitcnt lgkmcnt(0)
	v_cndmask_b32_e32 v82, v82, v83, vcc
	v_cndmask_b32_e32 v83, v83, v90, vcc
	v_mul_f32_e32 v86, v82, v85
	v_fma_f32 v86, v83, v84, -v86
	v_mul_f32_e32 v83, v83, v85
	v_fmac_f32_e32 v83, v82, v84
	v_mul_f32_e32 v82, v235, v86
	v_mul_f32_e32 v83, v235, v83
	v_cvt_pk_f16_f32 v82, v82, v83
	global_store_dword v[244:245], v82, off offset:2304
	v_mov_b32_e32 v82, v93
	s_waitcnt vmcnt(48)
	v_cndmask_b32_e64 v85, 0, v189, s[0:1]
	v_cndmask_b32_e32 v83, v92, v82, vcc
	ds_bpermute_b32 v83, v169, v83
	v_cndmask_b32_e64 v84, 1.0, v188, s[0:1]
	v_mfma_f32_32x32x16_f16 v[48:63], v[140:143], v[156:159], v[48:63]
	s_waitcnt lgkmcnt(0)
	v_cndmask_b32_e32 v82, v82, v83, vcc
	v_cndmask_b32_e32 v83, v83, v92, vcc
	v_mul_f32_e32 v86, v82, v85
	v_fma_f32 v86, v83, v84, -v86
	v_mul_f32_e32 v83, v83, v85
	v_fmac_f32_e32 v83, v82, v84
	v_mul_f32_e32 v82, v235, v86
	v_mul_f32_e32 v83, v235, v83
	v_cvt_pk_f16_f32 v82, v82, v83
	global_store_dword v[244:245], v82, off offset:3072
	v_mov_b32_e32 v82, v95
	s_waitcnt vmcnt(47)
	v_cndmask_b32_e64 v85, 0, v187, s[0:1]
	v_cndmask_b32_e32 v83, v94, v82, vcc
	ds_bpermute_b32 v83, v169, v83
	v_mfma_f32_32x32x16_f16 v[48:63], v[136:139], v[152:155], v[48:63]
	s_waitcnt lgkmcnt(0)
	v_cndmask_b32_e32 v82, v82, v83, vcc
	v_cndmask_b32_e32 v84, v83, v94, vcc
	v_cndmask_b32_e64 v83, 1.0, v186, s[0:1]
	v_mul_f32_e32 v86, v82, v85
	v_fma_f32 v86, v84, v83, -v86
	v_mul_f32_e32 v84, v84, v85
	v_fmac_f32_e32 v84, v82, v83
	v_mul_f32_e32 v82, v235, v86
	v_mul_f32_e32 v83, v235, v84
	v_cvt_pk_f16_f32 v82, v82, v83
	global_store_dword v[244:245], v82, off offset:3328
	s_waitcnt vmcnt(38)
	v_cndmask_b32_e64 v83, 0, v185, s[0:1]
	v_cndmask_b32_e32 v82, v64, v65, vcc
	ds_bpermute_b32 v82, v169, v82
	v_mfma_f32_32x32x16_f16 v[32:47], v[100:103], v[148:151], v[32:47]
	s_waitcnt lgkmcnt(0)
	v_cndmask_b32_e32 v65, v65, v82, vcc
	v_cndmask_b32_e32 v64, v82, v64, vcc
	v_cndmask_b32_e64 v82, 1.0, v184, s[0:1]
	v_mul_f32_e32 v84, v65, v83
	v_fma_f32 v84, v64, v82, -v84
	v_mul_f32_e32 v64, v64, v83
	v_fmac_f32_e32 v64, v65, v82
	v_mul_f32_e32 v65, v235, v84
	v_mul_f32_e32 v64, v235, v64
	v_cvt_pk_f16_f32 v84, v65, v64
	v_or_b32_e32 v64, 0x1000, v80
	v_mov_b32_e32 v65, v165
	v_lshl_add_u64 v[82:83], v[166:167], 0, v[64:65]
	global_store_dword v[82:83], v84, off
	s_waitcnt vmcnt(35)
	v_cndmask_b32_e64 v83, 0, v183, s[0:1]
	v_cndmask_b32_e32 v82, v66, v67, vcc
	ds_bpermute_b32 v82, v169, v82
	v_mfma_f32_32x32x16_f16 v[32:47], v[96:99], v[144:147], v[32:47]
	s_waitcnt lgkmcnt(0)
	v_cndmask_b32_e32 v67, v67, v82, vcc
	v_cndmask_b32_e32 v66, v82, v66, vcc
	v_cndmask_b32_e64 v82, 1.0, v182, s[0:1]
	v_mul_f32_e32 v84, v67, v83
	v_fma_f32 v84, v66, v82, -v84
	v_mul_f32_e32 v66, v66, v83
	v_fmac_f32_e32 v66, v67, v82
	v_mul_f32_e32 v67, v235, v84
	v_mul_f32_e32 v66, v235, v66
	v_cvt_pk_f16_f32 v84, v67, v66
	v_or_b32_e32 v66, 0x1100, v80
	v_mov_b32_e32 v67, v165
	v_lshl_add_u64 v[82:83], v[166:167], 0, v[66:67]
	global_store_dword v[82:83], v84, off
	s_waitcnt vmcnt(32)
	v_cndmask_b32_e64 v83, 0, v181, s[0:1]
	v_cndmask_b32_e32 v82, v68, v69, vcc
	ds_bpermute_b32 v82, v169, v82
	v_mfma_f32_32x32x16_f16 v[32:47], v[116:119], v[156:159], v[32:47]
	s_waitcnt lgkmcnt(0)
	v_cndmask_b32_e32 v69, v69, v82, vcc
	v_cndmask_b32_e32 v68, v82, v68, vcc
	v_cndmask_b32_e64 v82, 1.0, v180, s[0:1]
	v_mul_f32_e32 v84, v69, v83
	v_fma_f32 v84, v68, v82, -v84
	v_mul_f32_e32 v68, v68, v83
	v_fmac_f32_e32 v68, v69, v82
	v_mul_f32_e32 v69, v235, v84
	v_mul_f32_e32 v68, v235, v68
	v_cvt_pk_f16_f32 v84, v69, v68
	v_or_b32_e32 v68, 0x1400, v80
	v_mov_b32_e32 v69, v165
	v_lshl_add_u64 v[82:83], v[166:167], 0, v[68:69]
	global_store_dword v[82:83], v84, off
	s_waitcnt vmcnt(29)
	v_cndmask_b32_e64 v83, 0, v179, s[0:1]
	v_cndmask_b32_e32 v82, v70, v71, vcc
	ds_bpermute_b32 v82, v169, v82
	v_mfma_f32_32x32x16_f16 v[32:47], v[108:111], v[152:155], v[32:47]
	s_waitcnt lgkmcnt(0)
	v_cndmask_b32_e32 v71, v71, v82, vcc
	v_cndmask_b32_e32 v70, v82, v70, vcc
	v_cndmask_b32_e64 v82, 1.0, v178, s[0:1]
	v_mul_f32_e32 v84, v71, v83
	v_fma_f32 v84, v70, v82, -v84
	v_mul_f32_e32 v70, v70, v83
	v_fmac_f32_e32 v70, v71, v82
	v_mul_f32_e32 v71, v235, v84
	v_mul_f32_e32 v70, v235, v70
	v_cvt_pk_f16_f32 v84, v71, v70
	v_or_b32_e32 v70, 0x1500, v80
	v_mov_b32_e32 v71, v165
	v_lshl_add_u64 v[82:83], v[166:167], 0, v[70:71]
	global_store_dword v[82:83], v84, off
	s_waitcnt vmcnt(26)
	v_cndmask_b32_e64 v83, 0, v177, s[0:1]
	v_cndmask_b32_e32 v82, v72, v73, vcc
	ds_bpermute_b32 v82, v169, v82
	v_mfma_f32_32x32x16_f16 v[16:31], v[128:131], v[124:127], v[16:31]
	s_waitcnt lgkmcnt(0)
	v_cndmask_b32_e32 v73, v73, v82, vcc
	v_cndmask_b32_e32 v72, v82, v72, vcc
	v_cndmask_b32_e64 v82, 1.0, v176, s[0:1]
	v_mul_f32_e32 v84, v73, v83
	v_fma_f32 v84, v72, v82, -v84
	v_mul_f32_e32 v72, v72, v83
	v_fmac_f32_e32 v72, v73, v82
	v_mul_f32_e32 v73, v235, v84
	v_mul_f32_e32 v72, v235, v72
	v_cvt_pk_f16_f32 v84, v73, v72
	v_or_b32_e32 v72, 0x1800, v80
	v_mov_b32_e32 v73, v165
	v_lshl_add_u64 v[82:83], v[166:167], 0, v[72:73]
	global_store_dword v[82:83], v84, off
	s_waitcnt vmcnt(23)
	v_cndmask_b32_e64 v83, 0, v175, s[0:1]
	v_cndmask_b32_e32 v82, v74, v75, vcc
	ds_bpermute_b32 v82, v169, v82
	v_mfma_f32_32x32x16_f16 v[16:31], v[132:135], v[120:123], v[16:31]
	s_waitcnt lgkmcnt(0)
	v_cndmask_b32_e32 v75, v75, v82, vcc
	v_cndmask_b32_e32 v74, v82, v74, vcc
	v_cndmask_b32_e64 v82, 1.0, v174, s[0:1]
	v_mul_f32_e32 v84, v75, v83
	v_fma_f32 v84, v74, v82, -v84
	v_mul_f32_e32 v74, v74, v83
	v_fmac_f32_e32 v74, v75, v82
	v_mul_f32_e32 v75, v235, v84
	v_mul_f32_e32 v74, v235, v74
	v_cvt_pk_f16_f32 v84, v75, v74
	v_or_b32_e32 v74, 0x1900, v80
	v_mov_b32_e32 v75, v165
	v_lshl_add_u64 v[82:83], v[166:167], 0, v[74:75]
	global_store_dword v[82:83], v84, off
	s_waitcnt vmcnt(20)
	v_cndmask_b32_e64 v83, 0, v173, s[0:1]
	v_cndmask_b32_e32 v82, v76, v77, vcc
	ds_bpermute_b32 v82, v169, v82
	v_mfma_f32_32x32x16_f16 v[16:31], v[140:143], v[112:115], v[16:31]
	s_waitcnt lgkmcnt(0)
	v_cndmask_b32_e32 v77, v77, v82, vcc
	v_cndmask_b32_e32 v76, v82, v76, vcc
	v_cndmask_b32_e64 v82, 1.0, v172, s[0:1]
	v_mul_f32_e32 v84, v77, v83
	v_fma_f32 v84, v76, v82, -v84
	v_mul_f32_e32 v76, v76, v83
	v_fmac_f32_e32 v76, v77, v82
	v_mul_f32_e32 v77, v235, v84
	v_mul_f32_e32 v76, v235, v76
	v_cvt_pk_f16_f32 v84, v77, v76
	v_or_b32_e32 v76, 0x1c00, v80
	v_mov_b32_e32 v77, v165
	v_lshl_add_u64 v[82:83], v[166:167], 0, v[76:77]
	global_store_dword v[82:83], v84, off
	s_waitcnt vmcnt(17)
	v_cndmask_b32_e64 v83, 0, v171, s[0:1]
	v_cndmask_b32_e32 v82, v78, v79, vcc
	ds_bpermute_b32 v82, v169, v82
	v_mfma_f32_32x32x16_f16 v[16:31], v[136:139], v[104:107], v[16:31]
	s_waitcnt lgkmcnt(0)
	v_cndmask_b32_e32 v79, v79, v82, vcc
	v_cndmask_b32_e32 v78, v82, v78, vcc
	v_cndmask_b32_e64 v82, 1.0, v170, s[0:1]
	v_mul_f32_e32 v84, v79, v83
	v_fma_f32 v84, v78, v82, -v84
	v_mul_f32_e32 v78, v78, v83
	v_fmac_f32_e32 v78, v79, v82
	v_mul_f32_e32 v79, v235, v84
	v_mul_f32_e32 v78, v235, v78
	v_cvt_pk_f16_f32 v84, v79, v78
	v_or_b32_e32 v78, 0x1d00, v80
	v_mov_b32_e32 v79, v165
	v_lshl_add_u64 v[82:83], v[166:167], 0, v[78:79]
	global_store_dword v[82:83], v84, off
	s_cselect_b64 s[0:1], -1, 0
	v_cndmask_b32_e32 v82, v48, v49, vcc
	s_and_b32 s2, s2, 0x7ffffc00
	ds_bpermute_b32 v82, v169, v82
	s_cmpk_eq_i32 s2, 0x400
	s_cselect_b32 s2, s6, s12
	s_cselect_b32 s10, s7, s13
	v_cndmask_b32_e64 v84, 1.0, v228, s[0:1]
	s_and_b64 s[0:1], s[0:1], exec
	s_cselect_b32 s15, s5, s10
	s_cselect_b32 s16, s4, s2
	s_cmpk_lt_u32 s14, 0x7e0
	s_cselect_b64 s[0:1], -1, 0
	s_waitcnt lgkmcnt(0)
	v_cndmask_b32_e32 v49, v49, v82, vcc
	v_cndmask_b32_e64 v83, 0, v234, s[0:1]
	v_cndmask_b32_e32 v48, v82, v48, vcc
	v_cndmask_b32_e64 v82, 1.0, v233, s[0:1]
	v_mul_f32_e32 v85, v49, v83
	v_fma_f32 v85, v48, v82, -v85
	v_mul_f32_e32 v48, v48, v83
	v_fmac_f32_e32 v48, v49, v82
	s_or_b32 s2, s9, s8
	v_mul_f32_e32 v49, v84, v85
	v_mul_f32_e32 v48, v84, v48
	s_lshl_b64 s[10:11], s[2:3], 18
	v_cvt_pk_f16_f32 v85, v49, v48
	v_bitop3_b32 v48, v168, 62, 32 bitop3:0x48
	s_add_u32 s10, s16, s10
	s_addc_u32 s11, s15, s11
	v_lshlrev_b32_e32 v48, 1, v48
	v_mov_b32_e32 v49, v165
	v_lshl_add_u64 v[48:49], s[10:11], 0, v[48:49]
	v_lshl_add_u64 v[82:83], v[48:49], 0, v[80:81]
	global_store_dword v[82:83], v85, off
	v_cndmask_b32_e64 v86, 0, v232, s[0:1]
	v_cndmask_b32_e32 v85, v50, v51, vcc
	ds_bpermute_b32 v85, v169, v85
	s_add_i32 s2, s14, 64
	s_bfe_u32 s9, s2, 0x40006
	s_cmpk_lt_u32 s14, 0x3c0
	v_mfma_f32_32x32x16_f16 v[0:15], v[100:103], v[124:127], v[0:15]
	s_waitcnt lgkmcnt(0)
	v_cndmask_b32_e32 v51, v51, v85, vcc
	v_cndmask_b32_e32 v50, v85, v50, vcc
	v_cndmask_b32_e64 v85, 1.0, v231, s[0:1]
	v_mul_f32_e32 v87, v51, v86
	v_fma_f32 v87, v50, v85, -v87
	v_mul_f32_e32 v50, v50, v86
	v_fmac_f32_e32 v50, v51, v85
	v_mul_f32_e32 v51, v84, v87
	v_mul_f32_e32 v50, v84, v50
	v_cvt_pk_f16_f32 v50, v51, v50
	global_store_dword v[82:83], v50, off offset:256
	v_mov_b32_e32 v50, v53
	v_cndmask_b32_e64 v53, 0, v230, s[0:1]
	v_cndmask_b32_e32 v51, v52, v50, vcc
	ds_bpermute_b32 v51, v169, v51
	v_mfma_f32_32x32x16_f16 v[0:15], v[96:99], v[120:123], v[0:15]
	s_waitcnt lgkmcnt(0)
	v_cndmask_b32_e32 v50, v50, v51, vcc
	v_cndmask_b32_e32 v51, v51, v52, vcc
	v_cndmask_b32_e64 v52, 1.0, v229, s[0:1]
	v_mul_f32_e32 v85, v50, v53
	v_fma_f32 v85, v51, v52, -v85
	v_mul_f32_e32 v51, v51, v53
	v_fmac_f32_e32 v51, v50, v52
	v_mul_f32_e32 v50, v84, v85
	v_mul_f32_e32 v51, v84, v51
	v_cvt_pk_f16_f32 v50, v50, v51
	global_store_dword v[82:83], v50, off offset:1024
	v_mov_b32_e32 v50, v55
	v_cndmask_b32_e64 v53, 0, v227, s[0:1]
	v_cndmask_b32_e32 v51, v54, v50, vcc
	ds_bpermute_b32 v51, v169, v51
	v_cndmask_b32_e64 v52, 1.0, v226, s[0:1]
	v_mfma_f32_32x32x16_f16 v[0:15], v[116:119], v[112:115], v[0:15]
	s_waitcnt lgkmcnt(0)
	v_cndmask_b32_e32 v50, v50, v51, vcc
	v_cndmask_b32_e32 v51, v51, v54, vcc
	v_mul_f32_e32 v54, v50, v53
	v_fma_f32 v54, v51, v52, -v54
	v_mul_f32_e32 v51, v51, v53
	v_fmac_f32_e32 v51, v50, v52
	v_mul_f32_e32 v50, v84, v54
	v_mul_f32_e32 v51, v84, v51
	v_cvt_pk_f16_f32 v50, v50, v51
	global_store_dword v[82:83], v50, off offset:1280
	v_mov_b32_e32 v50, v57
	v_cndmask_b32_e64 v53, 0, v225, s[0:1]
	v_cndmask_b32_e32 v51, v56, v50, vcc
	ds_bpermute_b32 v51, v169, v51
	v_cndmask_b32_e64 v52, 1.0, v224, s[0:1]
	v_mfma_f32_32x32x16_f16 v[0:15], v[108:111], v[104:107], v[0:15]
	s_waitcnt lgkmcnt(0)
	v_cndmask_b32_e32 v50, v50, v51, vcc
	v_cndmask_b32_e32 v51, v51, v56, vcc
	v_mul_f32_e32 v54, v50, v53
	v_fma_f32 v54, v51, v52, -v54
	v_mul_f32_e32 v51, v51, v53
	v_fmac_f32_e32 v51, v50, v52
	v_mul_f32_e32 v50, v84, v54
	v_mul_f32_e32 v51, v84, v51
	v_cvt_pk_f16_f32 v50, v50, v51
	global_store_dword v[82:83], v50, off offset:2048
	v_mov_b32_e32 v50, v59
	v_cndmask_b32_e64 v53, 0, v223, s[0:1]
	v_cndmask_b32_e32 v51, v58, v50, vcc
	ds_bpermute_b32 v51, v169, v51
	v_cndmask_b32_e64 v52, 1.0, v222, s[0:1]
	s_waitcnt lgkmcnt(0)
	v_cndmask_b32_e32 v50, v50, v51, vcc
	v_cndmask_b32_e32 v51, v51, v58, vcc
	v_mul_f32_e32 v54, v50, v53
	v_fma_f32 v54, v51, v52, -v54
	v_mul_f32_e32 v51, v51, v53
	v_fmac_f32_e32 v51, v50, v52
	v_mul_f32_e32 v50, v84, v54
	v_mul_f32_e32 v51, v84, v51
	v_cvt_pk_f16_f32 v50, v50, v51
	global_store_dword v[82:83], v50, off offset:2304
	v_mov_b32_e32 v50, v61
	v_cndmask_b32_e64 v53, 0, v221, s[0:1]
	v_cndmask_b32_e32 v51, v60, v50, vcc
	ds_bpermute_b32 v51, v169, v51
	v_cndmask_b32_e64 v52, 1.0, v220, s[0:1]
	s_waitcnt lgkmcnt(0)
	v_cndmask_b32_e32 v50, v50, v51, vcc
	v_cndmask_b32_e32 v51, v51, v60, vcc
	v_mul_f32_e32 v54, v50, v53
	v_fma_f32 v54, v51, v52, -v54
	v_mul_f32_e32 v51, v51, v53
	v_fmac_f32_e32 v51, v50, v52
	v_mul_f32_e32 v50, v84, v54
	v_mul_f32_e32 v51, v84, v51
	v_cvt_pk_f16_f32 v50, v50, v51
	global_store_dword v[82:83], v50, off offset:3072
	v_mov_b32_e32 v50, v63
	v_cndmask_b32_e64 v53, 0, v219, s[0:1]
	v_cndmask_b32_e32 v51, v62, v50, vcc
	ds_bpermute_b32 v51, v169, v51
	s_waitcnt lgkmcnt(0)
	v_cndmask_b32_e32 v50, v50, v51, vcc
	v_cndmask_b32_e32 v52, v51, v62, vcc
	v_cndmask_b32_e64 v51, 1.0, v218, s[0:1]
	v_mul_f32_e32 v54, v50, v53
	v_fma_f32 v54, v52, v51, -v54
	v_mul_f32_e32 v52, v52, v53
	v_fmac_f32_e32 v52, v50, v51
	v_mul_f32_e32 v50, v84, v54
	v_mul_f32_e32 v51, v84, v52
	v_cvt_pk_f16_f32 v50, v50, v51
	global_store_dword v[82:83], v50, off offset:3328
	v_cndmask_b32_e64 v51, 0, v217, s[0:1]
	v_cndmask_b32_e32 v50, v32, v33, vcc
	ds_bpermute_b32 v50, v169, v50
	s_waitcnt lgkmcnt(0)
	v_cndmask_b32_e32 v33, v33, v50, vcc
	v_cndmask_b32_e32 v32, v50, v32, vcc
	v_cndmask_b32_e64 v50, 1.0, v216, s[0:1]
	v_mul_f32_e32 v52, v33, v51
	v_fma_f32 v52, v32, v50, -v52
	v_mul_f32_e32 v32, v32, v51
	v_fmac_f32_e32 v32, v33, v50
	v_mul_f32_e32 v33, v84, v52
	v_mul_f32_e32 v32, v84, v32
	v_cvt_pk_f16_f32 v50, v33, v32
	v_lshl_add_u64 v[32:33], v[48:49], 0, v[64:65]
	global_store_dword v[32:33], v50, off
	v_mov_b32_e32 v32, v35
	v_cndmask_b32_e64 v35, 0, v215, s[0:1]
	v_cndmask_b32_e32 v33, v34, v32, vcc
	ds_bpermute_b32 v33, v169, v33
	s_waitcnt lgkmcnt(0)
	v_cndmask_b32_e32 v32, v32, v33, vcc
	v_cndmask_b32_e32 v33, v33, v34, vcc
	v_cndmask_b32_e64 v34, 1.0, v214, s[0:1]
	v_mul_f32_e32 v50, v32, v35
	v_fma_f32 v50, v33, v34, -v50
	v_mul_f32_e32 v33, v33, v35
	v_fmac_f32_e32 v33, v32, v34
	v_mul_f32_e32 v32, v84, v50
	v_mul_f32_e32 v33, v84, v33
	v_cvt_pk_f16_f32 v34, v32, v33
	v_lshl_add_u64 v[32:33], v[48:49], 0, v[66:67]
	global_store_dword v[32:33], v34, off
	v_mov_b32_e32 v32, v37
	v_cndmask_b32_e64 v35, 0, v213, s[0:1]
	v_cndmask_b32_e32 v33, v36, v32, vcc
	ds_bpermute_b32 v33, v169, v33
	v_cndmask_b32_e64 v34, 1.0, v212, s[0:1]
	s_waitcnt lgkmcnt(0)
	v_cndmask_b32_e32 v32, v32, v33, vcc
	v_cndmask_b32_e32 v33, v33, v36, vcc
	v_mul_f32_e32 v36, v32, v35
	v_fma_f32 v36, v33, v34, -v36
	v_mul_f32_e32 v33, v33, v35
	v_fmac_f32_e32 v33, v32, v34
	v_mul_f32_e32 v32, v84, v36
	v_mul_f32_e32 v33, v84, v33
	v_cvt_pk_f16_f32 v34, v32, v33
	v_lshl_add_u64 v[32:33], v[48:49], 0, v[68:69]
	global_store_dword v[32:33], v34, off
	v_mov_b32_e32 v32, v39
	v_cndmask_b32_e64 v35, 0, v211, s[0:1]
	v_cndmask_b32_e32 v33, v38, v32, vcc
	ds_bpermute_b32 v33, v169, v33
	v_cndmask_b32_e64 v34, 1.0, v210, s[0:1]
	s_waitcnt lgkmcnt(0)
	v_cndmask_b32_e32 v32, v32, v33, vcc
	v_cndmask_b32_e32 v33, v33, v38, vcc
	v_mul_f32_e32 v36, v32, v35
	v_fma_f32 v36, v33, v34, -v36
	v_mul_f32_e32 v33, v33, v35
	v_fmac_f32_e32 v33, v32, v34
	v_mul_f32_e32 v32, v84, v36
	v_mul_f32_e32 v33, v84, v33
	v_cvt_pk_f16_f32 v34, v32, v33
	v_lshl_add_u64 v[32:33], v[48:49], 0, v[70:71]
	global_store_dword v[32:33], v34, off
	v_mov_b32_e32 v32, v41
	v_cndmask_b32_e64 v35, 0, v209, s[0:1]
	v_cndmask_b32_e32 v33, v40, v32, vcc
	ds_bpermute_b32 v33, v169, v33
	v_cndmask_b32_e64 v34, 1.0, v208, s[0:1]
	s_waitcnt lgkmcnt(0)
	v_cndmask_b32_e32 v32, v32, v33, vcc
	v_cndmask_b32_e32 v33, v33, v40, vcc
	v_mul_f32_e32 v36, v32, v35
	v_fma_f32 v36, v33, v34, -v36
	v_mul_f32_e32 v33, v33, v35
	v_fmac_f32_e32 v33, v32, v34
	v_mul_f32_e32 v32, v84, v36
	v_mul_f32_e32 v33, v84, v33
	v_cvt_pk_f16_f32 v34, v32, v33
	v_lshl_add_u64 v[32:33], v[48:49], 0, v[72:73]
	global_store_dword v[32:33], v34, off
	v_mov_b32_e32 v32, v43
	v_cndmask_b32_e64 v35, 0, v207, s[0:1]
	v_cndmask_b32_e32 v33, v42, v32, vcc
	ds_bpermute_b32 v33, v169, v33
	v_cndmask_b32_e64 v34, 1.0, v206, s[0:1]
	s_waitcnt lgkmcnt(0)
	v_cndmask_b32_e32 v32, v32, v33, vcc
	v_cndmask_b32_e32 v33, v33, v42, vcc
	v_mul_f32_e32 v36, v32, v35
	v_fma_f32 v36, v33, v34, -v36
	v_mul_f32_e32 v33, v33, v35
	v_fmac_f32_e32 v33, v32, v34
	v_mul_f32_e32 v32, v84, v36
	v_mul_f32_e32 v33, v84, v33
	v_cvt_pk_f16_f32 v34, v32, v33
	v_lshl_add_u64 v[32:33], v[48:49], 0, v[74:75]
	global_store_dword v[32:33], v34, off
	v_mov_b32_e32 v32, v45
	v_cndmask_b32_e64 v35, 0, v205, s[0:1]
	v_cndmask_b32_e32 v33, v44, v32, vcc
	ds_bpermute_b32 v33, v169, v33
	v_cndmask_b32_e64 v34, 1.0, v204, s[0:1]
	s_waitcnt lgkmcnt(0)
	v_cndmask_b32_e32 v32, v32, v33, vcc
	v_cndmask_b32_e32 v33, v33, v44, vcc
	v_mul_f32_e32 v36, v32, v35
	v_fma_f32 v36, v33, v34, -v36
	v_mul_f32_e32 v33, v33, v35
	v_fmac_f32_e32 v33, v32, v34
	v_mul_f32_e32 v32, v84, v36
	v_mul_f32_e32 v33, v84, v33
	v_cvt_pk_f16_f32 v34, v32, v33
	v_lshl_add_u64 v[32:33], v[48:49], 0, v[76:77]
	global_store_dword v[32:33], v34, off
	v_mov_b32_e32 v32, v47
	s_waitcnt vmcnt(31)
	v_cndmask_b32_e64 v35, 0, v203, s[0:1]
	v_cndmask_b32_e32 v33, v46, v32, vcc
	ds_bpermute_b32 v33, v169, v33
	s_waitcnt lgkmcnt(0)
	v_cndmask_b32_e32 v32, v32, v33, vcc
	v_cndmask_b32_e32 v34, v33, v46, vcc
	v_cndmask_b32_e64 v33, 1.0, v202, s[0:1]
	v_mul_f32_e32 v36, v32, v35
	v_fma_f32 v36, v34, v33, -v36
	v_mul_f32_e32 v34, v34, v35
	v_fmac_f32_e32 v34, v32, v33
	v_mul_f32_e32 v32, v84, v36
	v_mul_f32_e32 v33, v84, v34
	v_cvt_pk_f16_f32 v34, v32, v33
	v_lshl_add_u64 v[32:33], v[48:49], 0, v[78:79]
	global_store_dword v[32:33], v34, off
	s_cselect_b64 s[0:1], -1, 0
	v_cndmask_b32_e32 v32, v16, v17, vcc
	s_and_b32 s2, s2, 0x7ffffc00
	ds_bpermute_b32 v32, v169, v32
	s_cmpk_eq_i32 s2, 0x400
	s_cselect_b32 s2, s6, s12
	s_cselect_b32 s6, s7, s13
	v_cndmask_b32_e64 v34, 1.0, v228, s[0:1]
	s_and_b64 s[0:1], s[0:1], exec
	s_cselect_b32 s5, s5, s6
	s_cselect_b32 s4, s4, s2
	s_cmpk_lt_u32 s14, 0x7c0
	s_cselect_b64 s[0:1], -1, 0
	s_waitcnt lgkmcnt(0)
	v_cndmask_b32_e32 v17, v17, v32, vcc
	v_cndmask_b32_e64 v33, 0, v201, s[0:1]
	v_cndmask_b32_e32 v16, v32, v16, vcc
	v_cndmask_b32_e64 v32, 1.0, v200, s[0:1]
	v_mul_f32_e32 v35, v17, v33
	s_or_b32 s2, s9, s8
	v_fma_f32 v35, v16, v32, -v35
	v_mul_f32_e32 v16, v16, v33
	s_lshl_b64 s[2:3], s[2:3], 18
	v_fmac_f32_e32 v16, v17, v32
	s_add_u32 s2, s4, s2
	v_mul_f32_e32 v17, v34, v35
	v_mul_f32_e32 v16, v34, v16
	s_addc_u32 s3, s5, s3
	v_cvt_pk_f16_f32 v35, v17, v16
	v_lshl_add_u64 v[16:17], s[2:3], 0, v[164:165]
	v_lshl_add_u64 v[32:33], v[16:17], 0, v[80:81]
	global_store_dword v[32:33], v35, off
	v_cndmask_b32_e64 v36, 0, v199, s[0:1]
	v_cndmask_b32_e32 v35, v18, v19, vcc
	ds_bpermute_b32 v35, v169, v35
	s_waitcnt lgkmcnt(0)
	v_cndmask_b32_e32 v19, v19, v35, vcc
	v_cndmask_b32_e32 v18, v35, v18, vcc
	v_cndmask_b32_e64 v35, 1.0, v198, s[0:1]
	v_mul_f32_e32 v37, v19, v36
	v_fma_f32 v37, v18, v35, -v37
	v_mul_f32_e32 v18, v18, v36
	v_fmac_f32_e32 v18, v19, v35
	v_mul_f32_e32 v19, v34, v37
	v_mul_f32_e32 v18, v34, v18
	v_cvt_pk_f16_f32 v18, v19, v18
	global_store_dword v[32:33], v18, off offset:256
	v_mov_b32_e32 v18, v21
	v_cndmask_b32_e64 v21, 0, v197, s[0:1]
	v_cndmask_b32_e32 v19, v20, v18, vcc
	ds_bpermute_b32 v19, v169, v19
	s_waitcnt lgkmcnt(0)
	v_cndmask_b32_e32 v18, v18, v19, vcc
	v_cndmask_b32_e32 v19, v19, v20, vcc
	v_cndmask_b32_e64 v20, 1.0, v196, s[0:1]
	v_mul_f32_e32 v35, v18, v21
	v_fma_f32 v35, v19, v20, -v35
	v_mul_f32_e32 v19, v19, v21
	v_fmac_f32_e32 v19, v18, v20
	v_mul_f32_e32 v18, v34, v35
	v_mul_f32_e32 v19, v34, v19
	v_cvt_pk_f16_f32 v18, v18, v19
	global_store_dword v[32:33], v18, off offset:1024
	v_mov_b32_e32 v18, v23
	v_cndmask_b32_e64 v21, 0, v195, s[0:1]
	v_cndmask_b32_e32 v19, v22, v18, vcc
	ds_bpermute_b32 v19, v169, v19
	v_cndmask_b32_e64 v20, 1.0, v194, s[0:1]
	s_waitcnt lgkmcnt(0)
	v_cndmask_b32_e32 v18, v18, v19, vcc
	v_cndmask_b32_e32 v19, v19, v22, vcc
	v_mul_f32_e32 v22, v18, v21
	v_fma_f32 v22, v19, v20, -v22
	v_mul_f32_e32 v19, v19, v21
	v_fmac_f32_e32 v19, v18, v20
	v_mul_f32_e32 v18, v34, v22
	v_mul_f32_e32 v19, v34, v19
	v_cvt_pk_f16_f32 v18, v18, v19
	global_store_dword v[32:33], v18, off offset:1280
	v_mov_b32_e32 v18, v25
	v_cndmask_b32_e64 v21, 0, v193, s[0:1]
	v_cndmask_b32_e32 v19, v24, v18, vcc
	ds_bpermute_b32 v19, v169, v19
	v_cndmask_b32_e64 v20, 1.0, v192, s[0:1]
	s_waitcnt lgkmcnt(0)
	v_cndmask_b32_e32 v18, v18, v19, vcc
	v_cndmask_b32_e32 v19, v19, v24, vcc
	v_mul_f32_e32 v22, v18, v21
	v_fma_f32 v22, v19, v20, -v22
	v_mul_f32_e32 v19, v19, v21
	v_fmac_f32_e32 v19, v18, v20
	v_mul_f32_e32 v18, v34, v22
	v_mul_f32_e32 v19, v34, v19
	v_cvt_pk_f16_f32 v18, v18, v19
	global_store_dword v[32:33], v18, off offset:2048
	v_mov_b32_e32 v18, v27
	v_cndmask_b32_e64 v21, 0, v191, s[0:1]
	v_cndmask_b32_e32 v19, v26, v18, vcc
	ds_bpermute_b32 v19, v169, v19
	v_cndmask_b32_e64 v20, 1.0, v190, s[0:1]
	s_waitcnt lgkmcnt(0)
	v_cndmask_b32_e32 v18, v18, v19, vcc
	v_cndmask_b32_e32 v19, v19, v26, vcc
	v_mul_f32_e32 v22, v18, v21
	v_fma_f32 v22, v19, v20, -v22
	v_mul_f32_e32 v19, v19, v21
	v_fmac_f32_e32 v19, v18, v20
	v_mul_f32_e32 v18, v34, v22
	v_mul_f32_e32 v19, v34, v19
	v_cvt_pk_f16_f32 v18, v18, v19
	global_store_dword v[32:33], v18, off offset:2304
	v_mov_b32_e32 v18, v29
	v_cndmask_b32_e64 v21, 0, v189, s[0:1]
	v_cndmask_b32_e32 v19, v28, v18, vcc
	ds_bpermute_b32 v19, v169, v19
	v_cndmask_b32_e64 v20, 1.0, v188, s[0:1]
	s_waitcnt lgkmcnt(0)
	v_cndmask_b32_e32 v18, v18, v19, vcc
	v_cndmask_b32_e32 v19, v19, v28, vcc
	v_mul_f32_e32 v22, v18, v21
	v_fma_f32 v22, v19, v20, -v22
	v_mul_f32_e32 v19, v19, v21
	v_fmac_f32_e32 v19, v18, v20
	v_mul_f32_e32 v18, v34, v22
	v_mul_f32_e32 v19, v34, v19
	v_cvt_pk_f16_f32 v18, v18, v19
	global_store_dword v[32:33], v18, off offset:3072
	v_mov_b32_e32 v18, v31
	v_cndmask_b32_e64 v21, 0, v187, s[0:1]
	v_cndmask_b32_e32 v19, v30, v18, vcc
	ds_bpermute_b32 v19, v169, v19
	s_waitcnt lgkmcnt(0)
	v_cndmask_b32_e32 v18, v18, v19, vcc
	v_cndmask_b32_e32 v20, v19, v30, vcc
	v_cndmask_b32_e64 v19, 1.0, v186, s[0:1]
	v_mul_f32_e32 v22, v18, v21
	v_fma_f32 v22, v20, v19, -v22
	v_mul_f32_e32 v20, v20, v21
	v_fmac_f32_e32 v20, v18, v19
	v_mul_f32_e32 v22, v34, v22
	v_mul_f32_e32 v18, v34, v20
	v_cvt_pk_f16_f32 v18, v22, v18
	global_store_dword v[32:33], v18, off offset:3328
	v_cndmask_b32_e64 v19, 0, v185, s[0:1]
	v_cndmask_b32_e32 v18, v0, v1, vcc
	ds_bpermute_b32 v18, v169, v18
	s_waitcnt lgkmcnt(0)
	v_cndmask_b32_e32 v1, v1, v18, vcc
	v_cndmask_b32_e32 v0, v18, v0, vcc
	v_cndmask_b32_e64 v18, 1.0, v184, s[0:1]
	v_mul_f32_e32 v20, v1, v19
	v_fma_f32 v20, v0, v18, -v20
	v_mul_f32_e32 v0, v0, v19
	v_fmac_f32_e32 v0, v1, v18
	v_mul_f32_e32 v20, v34, v20
	v_mul_f32_e32 v0, v34, v0
	v_cvt_pk_f16_f32 v18, v20, v0
	v_lshl_add_u64 v[0:1], v[16:17], 0, v[64:65]
	global_store_dword v[0:1], v18, off
	v_mov_b32_e32 v0, v3
	v_cndmask_b32_e64 v3, 0, v183, s[0:1]
	v_cndmask_b32_e32 v1, v2, v0, vcc
	ds_bpermute_b32 v1, v169, v1
	s_waitcnt lgkmcnt(0)
	v_cndmask_b32_e32 v0, v0, v1, vcc
	v_cndmask_b32_e32 v2, v1, v2, vcc
	v_cndmask_b32_e64 v1, 1.0, v182, s[0:1]
	v_mul_f32_e32 v18, v0, v3
	v_fma_f32 v18, v2, v1, -v18
	v_mul_f32_e32 v2, v2, v3
	v_fmac_f32_e32 v2, v0, v1
	v_mul_f32_e32 v18, v34, v18
	v_mul_f32_e32 v0, v34, v2
	v_cvt_pk_f16_f32 v2, v18, v0
	v_lshl_add_u64 v[0:1], v[16:17], 0, v[66:67]
	global_store_dword v[0:1], v2, off
	v_mov_b32_e32 v0, v5
	v_cndmask_b32_e64 v3, 0, v181, s[0:1]
	v_cndmask_b32_e32 v1, v4, v0, vcc
	ds_bpermute_b32 v1, v169, v1
	s_waitcnt lgkmcnt(0)
	v_cndmask_b32_e32 v0, v0, v1, vcc
	v_cndmask_b32_e32 v2, v1, v4, vcc
	v_cndmask_b32_e64 v1, 1.0, v180, s[0:1]
	v_mul_f32_e32 v4, v0, v3
	v_fma_f32 v4, v2, v1, -v4
	v_mul_f32_e32 v2, v2, v3
	v_fmac_f32_e32 v2, v0, v1
	v_mul_f32_e32 v4, v34, v4
	v_mul_f32_e32 v0, v34, v2
	v_cvt_pk_f16_f32 v2, v4, v0
	v_lshl_add_u64 v[0:1], v[16:17], 0, v[68:69]
	global_store_dword v[0:1], v2, off
	v_mov_b32_e32 v0, v7
	v_cndmask_b32_e64 v3, 0, v179, s[0:1]
	v_cndmask_b32_e32 v1, v6, v0, vcc
	ds_bpermute_b32 v1, v169, v1
	s_waitcnt lgkmcnt(0)
	v_cndmask_b32_e32 v0, v0, v1, vcc
	v_cndmask_b32_e32 v2, v1, v6, vcc
	v_cndmask_b32_e64 v1, 1.0, v178, s[0:1]
	v_mul_f32_e32 v4, v0, v3
	v_fma_f32 v4, v2, v1, -v4
	v_mul_f32_e32 v2, v2, v3
	v_fmac_f32_e32 v2, v0, v1
	v_mul_f32_e32 v4, v34, v4
	v_mul_f32_e32 v0, v34, v2
	v_cvt_pk_f16_f32 v2, v4, v0
	v_lshl_add_u64 v[0:1], v[16:17], 0, v[70:71]
	global_store_dword v[0:1], v2, off
	v_mov_b32_e32 v0, v9
	v_cndmask_b32_e64 v3, 0, v177, s[0:1]
	v_cndmask_b32_e32 v1, v8, v0, vcc
	ds_bpermute_b32 v1, v169, v1
	s_waitcnt lgkmcnt(0)
	v_cndmask_b32_e32 v0, v0, v1, vcc
	v_cndmask_b32_e32 v2, v1, v8, vcc
	v_cndmask_b32_e64 v1, 1.0, v176, s[0:1]
	v_mul_f32_e32 v4, v0, v3
	v_fma_f32 v4, v2, v1, -v4
	v_mul_f32_e32 v2, v2, v3
	v_fmac_f32_e32 v2, v0, v1
	v_mul_f32_e32 v4, v34, v4
	v_mul_f32_e32 v0, v34, v2
	v_cvt_pk_f16_f32 v2, v4, v0
	v_lshl_add_u64 v[0:1], v[16:17], 0, v[72:73]
	global_store_dword v[0:1], v2, off
	v_mov_b32_e32 v0, v11
	v_cndmask_b32_e64 v3, 0, v175, s[0:1]
	v_cndmask_b32_e32 v1, v10, v0, vcc
	ds_bpermute_b32 v1, v169, v1
	s_waitcnt lgkmcnt(0)
	v_cndmask_b32_e32 v0, v0, v1, vcc
	v_cndmask_b32_e32 v2, v1, v10, vcc
	v_cndmask_b32_e64 v1, 1.0, v174, s[0:1]
	v_mul_f32_e32 v4, v0, v3
	v_fma_f32 v4, v2, v1, -v4
	v_mul_f32_e32 v2, v2, v3
	v_fmac_f32_e32 v2, v0, v1
	v_mul_f32_e32 v4, v34, v4
	v_mul_f32_e32 v0, v34, v2
	v_cvt_pk_f16_f32 v2, v4, v0
	v_lshl_add_u64 v[0:1], v[16:17], 0, v[74:75]
	global_store_dword v[0:1], v2, off
	v_mov_b32_e32 v0, v13
	v_cndmask_b32_e64 v3, 0, v173, s[0:1]
	v_cndmask_b32_e32 v1, v12, v0, vcc
	ds_bpermute_b32 v1, v169, v1
	s_waitcnt lgkmcnt(0)
	v_cndmask_b32_e32 v0, v0, v1, vcc
	v_cndmask_b32_e32 v2, v1, v12, vcc
	v_cndmask_b32_e64 v1, 1.0, v172, s[0:1]
	v_mul_f32_e32 v4, v0, v3
	v_fma_f32 v4, v2, v1, -v4
	v_mul_f32_e32 v2, v2, v3
	v_fmac_f32_e32 v2, v0, v1
	v_mul_f32_e32 v4, v34, v4
	v_mul_f32_e32 v0, v34, v2
	v_cvt_pk_f16_f32 v2, v4, v0
	v_lshl_add_u64 v[0:1], v[16:17], 0, v[76:77]
	global_store_dword v[0:1], v2, off
	v_mov_b32_e32 v0, v15
	v_cndmask_b32_e64 v3, 0, v171, s[0:1]
	v_cndmask_b32_e32 v1, v14, v0, vcc
	ds_bpermute_b32 v1, v169, v1
	v_cndmask_b32_e64 v2, 1.0, v170, s[0:1]
	s_waitcnt lgkmcnt(0)
	v_cndmask_b32_e32 v0, v0, v1, vcc
	v_cndmask_b32_e32 v1, v1, v14, vcc
	v_mul_f32_e32 v4, v0, v3
	v_fma_f32 v4, v1, v2, -v4
	v_mul_f32_e32 v1, v1, v3
	v_fmac_f32_e32 v1, v0, v2
	v_mul_f32_e32 v4, v34, v4
	v_mul_f32_e32 v0, v34, v1
	v_cvt_pk_f16_f32 v2, v4, v0
	v_lshl_add_u64 v[0:1], v[16:17], 0, v[78:79]
	global_store_dword v[0:1], v2, off
	s_endpgm
	.p2alignl 8, 3212836864

_Z11gemm_kernelILi128ELi128ELi4ELi2ELi1EEvPKDF16_S1_PKfS3_PDF16_S4_S4_Pfi:
	s_load_dwordx4 s[8:11], s[0:1], 0x0
	s_load_dwordx2 s[4:5], s[0:1], 0x38
	s_lshl_b32 s0, s2, 2
	s_and_b32 s1, s0, 28
	s_bfe_u32 s2, s2, 0x20003
	v_readfirstlane_b32 s3, v0
	s_or_b32 s2, s1, s2
	s_and_b32 s0, s0, 0x7fffff80
	s_mov_b32 s1, 0
	s_lshl_b64 s[6:7], s[0:1], 11
	s_and_b32 s1, s3, 64
	s_lshl_b32 s12, s2, 18
	s_waitcnt lgkmcnt(0)
	s_add_u32 s8, s8, s12
	s_addc_u32 s9, s9, 0
	v_lshlrev_b32_e32 v2, 4, v0
	v_lshlrev_b32_e32 v4, 8, v0
	s_add_u32 s6, s10, s6
	v_lshlrev_b32_e32 v1, 7, v0
	v_and_b32_e32 v32, 0x70, v2
	v_mov_b32_e32 v33, 0
	v_and_b32_e32 v26, 0x1f800, v4
	s_mov_b32 s12, 0x1fc00
	v_mov_b32_e32 v4, 0x10000
	s_addc_u32 s7, s11, s7
	v_lshl_add_u64 v[2:3], s[8:9], 0, v[32:33]
	v_mov_b32_e32 v27, v33
	v_bitop3_b32 v1, v1, s12, v4 bitop3:0xc8
	v_lshl_add_u64 v[10:11], s[6:7], 0, v[32:33]
	v_lshl_add_u64 v[36:37], v[2:3], 0, v[26:27]
	v_lshlrev_b32_e32 v28, 1, v1
	v_mov_b32_e32 v29, v33
	v_lshl_add_u64 v[40:41], v[10:11], 0, v[26:27]
	v_lshl_add_u64 v[38:39], v[2:3], 0, v[28:29]
	global_load_dwordx4 v[2:5], v[36:37], off
	global_load_dwordx4 v[6:9], v[38:39], off
	v_lshl_add_u64 v[42:43], v[10:11], 0, v[28:29]
	global_load_dwordx4 v[10:13], v[40:41], off
	global_load_dwordx4 v[14:17], v[42:43], off
	v_or_b32_e32 v18, 0x200, v0
	s_movk_i32 s10, 0x90
	v_lshrrev_b32_e32 v1, 3, v0
	v_lshrrev_b32_e32 v18, 3, v18
	v_add_u32_e32 v19, 0, v32
	v_mad_u32_u24 v45, v1, s10, v19
	v_mad_u32_u24 v46, v18, s10, v19
	v_lshl_add_u64 v[18:19], s[8:9], 0, v[26:27]
	v_lshl_add_u64 v[20:21], s[8:9], 0, v[28:29]
	v_lshl_add_u64 v[30:31], v[18:19], 0, v[32:33]
	v_lshl_add_u64 v[26:27], s[6:7], 0, v[26:27]
	v_lshl_add_u64 v[34:35], v[20:21], 0, v[32:33]
	global_load_dwordx4 v[18:21], v[30:31], off offset:128
	global_load_dwordx4 v[22:25], v[34:35], off offset:128
	v_lshl_add_u64 v[28:29], s[6:7], 0, v[28:29]
	v_lshl_add_u64 v[30:31], v[26:27], 0, v[32:33]
	v_lshl_add_u64 v[34:35], v[28:29], 0, v[32:33]
	global_load_dwordx4 v[26:29], v[30:31], off offset:128
	global_load_dwordx4 v[48:51], v[34:35], off offset:128
	s_lshr_b32 s3, s3, 2
	v_and_b32_e32 v44, 31, v0
	v_bfe_u32 v32, v0, 5, 1
	s_and_b32 s3, s3, 0x3fffffe0
	v_or_b32_e32 v0, s3, v44
	s_waitcnt vmcnt(7)
	ds_write_b128 v45, v[2:5]
	s_waitcnt vmcnt(6)
	ds_write_b128 v46, v[6:9]
	s_waitcnt vmcnt(5)
	ds_write_b128 v45, v[10:13] offset:18432
	s_waitcnt vmcnt(4)
	ds_write_b128 v46, v[14:17] offset:18432
	s_waitcnt lgkmcnt(0)
	s_barrier
	global_load_dwordx4 v[52:55], v[36:37], off offset:256
	global_load_dwordx4 v[56:59], v[38:39], off offset:256
	global_load_dwordx4 v[60:63], v[40:41], off offset:256
	global_load_dwordx4 v[64:67], v[42:43], off offset:256
	v_lshl_add_u32 v4, v32, 4, 0
	v_mad_u64_u32 v[34:35], s[6:7], v0, s10, v[4:5]
	v_or_b32_e32 v5, s1, v44
	s_waitcnt vmcnt(7)
	ds_write_b128 v45, v[18:21] offset:36864
	s_waitcnt vmcnt(6)
	ds_write_b128 v46, v[22:25] offset:36864
	s_waitcnt vmcnt(5)
	ds_write_b128 v45, v[26:29] offset:55296
	s_waitcnt vmcnt(4)
	ds_write_b128 v46, v[48:51] offset:55296
	ds_read_b128 v[0:3], v34
	v_mad_u32_u24 v35, v5, s10, v4
	ds_read_b128 v[4:7], v35 offset:18432
	ds_read_b128 v[48:51], v34 offset:32
	ds_read_b128 v[68:71], v35 offset:18464
	s_waitcnt lgkmcnt(2)
	v_mfma_f32_32x32x16_f16 v[16:31], v[0:3], v[4:7], 0
	ds_read_b128 v[4:7], v35 offset:23040
	ds_read_b128 v[72:75], v35 offset:23072
	s_waitcnt lgkmcnt(1)
	v_mfma_f32_32x32x16_f16 v[0:15], v[0:3], v[4:7], 0
	v_mfma_f32_32x32x16_f16 v[16:31], v[48:51], v[68:71], v[16:31]
	s_waitcnt lgkmcnt(0)
	v_mfma_f32_32x32x16_f16 v[0:15], v[48:51], v[72:75], v[0:15]
	ds_read_b128 v[48:51], v34 offset:64
	ds_read_b128 v[68:71], v35 offset:18496
	ds_read_b128 v[72:75], v34 offset:96
	ds_read_b128 v[76:79], v35 offset:18528
	s_waitcnt lgkmcnt(2)
	v_mfma_f32_32x32x16_f16 v[16:31], v[48:51], v[68:71], v[16:31]
	ds_read_b128 v[68:71], v35 offset:23104
	ds_read_b128 v[80:83], v35 offset:23136
	s_waitcnt lgkmcnt(0)
	s_barrier
	v_mfma_f32_32x32x16_f16 v[0:15], v[48:51], v[68:71], v[0:15]
	v_mfma_f32_32x32x16_f16 v[16:31], v[72:75], v[76:79], v[16:31]
	global_load_dwordx4 v[48:51], v[36:37], off offset:384
	global_load_dwordx4 v[68:71], v[38:39], off offset:384
	global_load_dwordx4 v[76:79], v[40:41], off offset:384
	global_load_dwordx4 v[84:87], v[42:43], off offset:384
	v_mfma_f32_32x32x16_f16 v[0:15], v[72:75], v[80:83], v[0:15]
	s_waitcnt vmcnt(7)
	ds_write_b128 v45, v[52:55]
	s_waitcnt vmcnt(6)
	ds_write_b128 v46, v[56:59]
	s_waitcnt vmcnt(5)
	ds_write_b128 v45, v[60:63] offset:18432
	s_waitcnt vmcnt(4)
	ds_write_b128 v46, v[64:67] offset:18432
	ds_read_b128 v[52:55], v34 offset:36864
	ds_read_b128 v[56:59], v35 offset:55296
	ds_read_b128 v[60:63], v34 offset:36896
	ds_read_b128 v[64:67], v35 offset:55328
	s_waitcnt lgkmcnt(2)
	v_mfma_f32_32x32x16_f16 v[16:31], v[52:55], v[56:59], v[16:31]
	ds_read_b128 v[56:59], v35 offset:59904
	ds_read_b128 v[72:75], v35 offset:59936
	s_waitcnt lgkmcnt(1)
	v_mfma_f32_32x32x16_f16 v[0:15], v[52:55], v[56:59], v[0:15]
	v_mfma_f32_32x32x16_f16 v[16:31], v[60:63], v[64:67], v[16:31]
	s_waitcnt lgkmcnt(0)
	v_mfma_f32_32x32x16_f16 v[0:15], v[60:63], v[72:75], v[0:15]
	ds_read_b128 v[52:55], v34 offset:36928
	ds_read_b128 v[56:59], v35 offset:55360
	ds_read_b128 v[60:63], v34 offset:36960
	ds_read_b128 v[64:67], v35 offset:55392
	s_waitcnt lgkmcnt(2)
	v_mfma_f32_32x32x16_f16 v[16:31], v[52:55], v[56:59], v[16:31]
	ds_read_b128 v[56:59], v35 offset:59968
	ds_read_b128 v[72:75], v35 offset:60000
	s_waitcnt lgkmcnt(0)
	s_barrier
	v_mfma_f32_32x32x16_f16 v[0:15], v[52:55], v[56:59], v[0:15]
	v_mfma_f32_32x32x16_f16 v[16:31], v[60:63], v[64:67], v[16:31]
	global_load_dwordx4 v[52:55], v[36:37], off offset:512
	global_load_dwordx4 v[56:59], v[38:39], off offset:512
	global_load_dwordx4 v[64:67], v[40:41], off offset:512
	global_load_dwordx4 v[80:83], v[42:43], off offset:512
	v_mfma_f32_32x32x16_f16 v[0:15], v[60:63], v[72:75], v[0:15]
	s_waitcnt vmcnt(7)
	ds_write_b128 v45, v[48:51] offset:36864
	s_waitcnt vmcnt(6)
	ds_write_b128 v46, v[68:71] offset:36864
	s_waitcnt vmcnt(5)
	ds_write_b128 v45, v[76:79] offset:55296
	s_waitcnt vmcnt(4)
	ds_write_b128 v46, v[84:87] offset:55296
	ds_read_b128 v[48:51], v34
	ds_read_b128 v[60:63], v35 offset:18432
	ds_read_b128 v[68:71], v34 offset:32
	ds_read_b128 v[72:75], v35 offset:18464
	s_waitcnt lgkmcnt(2)
	v_mfma_f32_32x32x16_f16 v[16:31], v[48:51], v[60:63], v[16:31]
	ds_read_b128 v[60:63], v35 offset:23040
	ds_read_b128 v[76:79], v35 offset:23072
	s_waitcnt lgkmcnt(1)
	v_mfma_f32_32x32x16_f16 v[0:15], v[48:51], v[60:63], v[0:15]
	v_mfma_f32_32x32x16_f16 v[16:31], v[68:71], v[72:75], v[16:31]
	s_waitcnt lgkmcnt(0)
	v_mfma_f32_32x32x16_f16 v[0:15], v[68:71], v[76:79], v[0:15]
	ds_read_b128 v[48:51], v34 offset:64
	ds_read_b128 v[60:63], v35 offset:18496
	ds_read_b128 v[68:71], v34 offset:96
	ds_read_b128 v[72:75], v35 offset:18528
	s_waitcnt lgkmcnt(2)
	v_mfma_f32_32x32x16_f16 v[16:31], v[48:51], v[60:63], v[16:31]
	ds_read_b128 v[60:63], v35 offset:23104
	ds_read_b128 v[76:79], v35 offset:23136
	s_waitcnt lgkmcnt(0)
	s_barrier
	v_mfma_f32_32x32x16_f16 v[0:15], v[48:51], v[60:63], v[0:15]
	v_mfma_f32_32x32x16_f16 v[16:31], v[68:71], v[72:75], v[16:31]
	global_load_dwordx4 v[48:51], v[36:37], off offset:640
	global_load_dwordx4 v[60:63], v[38:39], off offset:640
	global_load_dwordx4 v[72:75], v[40:41], off offset:640
	global_load_dwordx4 v[84:87], v[42:43], off offset:640
	v_mfma_f32_32x32x16_f16 v[0:15], v[68:71], v[76:79], v[0:15]
	s_waitcnt vmcnt(7)
	ds_write_b128 v45, v[52:55]
	s_waitcnt vmcnt(6)
	ds_write_b128 v46, v[56:59]
	s_waitcnt vmcnt(5)
	ds_write_b128 v45, v[64:67] offset:18432
	s_waitcnt vmcnt(4)
	ds_write_b128 v46, v[80:83] offset:18432
	ds_read_b128 v[52:55], v34 offset:36864
	ds_read_b128 v[56:59], v35 offset:55296
	ds_read_b128 v[64:67], v34 offset:36896
	ds_read_b128 v[68:71], v35 offset:55328
	s_waitcnt lgkmcnt(2)
	v_mfma_f32_32x32x16_f16 v[16:31], v[52:55], v[56:59], v[16:31]
	ds_read_b128 v[56:59], v35 offset:59904
	ds_read_b128 v[76:79], v35 offset:59936
	s_waitcnt lgkmcnt(1)
	v_mfma_f32_32x32x16_f16 v[0:15], v[52:55], v[56:59], v[0:15]
	v_mfma_f32_32x32x16_f16 v[16:31], v[64:67], v[68:71], v[16:31]
	s_waitcnt lgkmcnt(0)
	v_mfma_f32_32x32x16_f16 v[0:15], v[64:67], v[76:79], v[0:15]
	ds_read_b128 v[52:55], v34 offset:36928
	ds_read_b128 v[56:59], v35 offset:55360
	ds_read_b128 v[64:67], v34 offset:36960
	ds_read_b128 v[68:71], v35 offset:55392
	s_waitcnt lgkmcnt(2)
	v_mfma_f32_32x32x16_f16 v[16:31], v[52:55], v[56:59], v[16:31]
	ds_read_b128 v[56:59], v35 offset:59968
	ds_read_b128 v[76:79], v35 offset:60000
	s_waitcnt lgkmcnt(0)
	s_barrier
	v_mfma_f32_32x32x16_f16 v[0:15], v[52:55], v[56:59], v[0:15]
	v_mfma_f32_32x32x16_f16 v[16:31], v[64:67], v[68:71], v[16:31]
	global_load_dwordx4 v[52:55], v[36:37], off offset:768
	global_load_dwordx4 v[56:59], v[38:39], off offset:768
	global_load_dwordx4 v[68:71], v[40:41], off offset:768
	global_load_dwordx4 v[80:83], v[42:43], off offset:768
	v_mfma_f32_32x32x16_f16 v[0:15], v[64:67], v[76:79], v[0:15]
	s_waitcnt vmcnt(7)
	ds_write_b128 v45, v[48:51] offset:36864
	s_waitcnt vmcnt(6)
	ds_write_b128 v46, v[60:63] offset:36864
	s_waitcnt vmcnt(5)
	ds_write_b128 v45, v[72:75] offset:55296
	s_waitcnt vmcnt(4)
	ds_write_b128 v46, v[84:87] offset:55296
	ds_read_b128 v[48:51], v34
	ds_read_b128 v[60:63], v35 offset:18432
	ds_read_b128 v[64:67], v34 offset:32
	ds_read_b128 v[72:75], v35 offset:18464
	s_waitcnt lgkmcnt(2)
	v_mfma_f32_32x32x16_f16 v[16:31], v[48:51], v[60:63], v[16:31]
	ds_read_b128 v[60:63], v35 offset:23040
	ds_read_b128 v[76:79], v35 offset:23072
	s_waitcnt lgkmcnt(1)
	v_mfma_f32_32x32x16_f16 v[0:15], v[48:51], v[60:63], v[0:15]
	v_mfma_f32_32x32x16_f16 v[16:31], v[64:67], v[72:75], v[16:31]
	s_waitcnt lgkmcnt(0)
	v_mfma_f32_32x32x16_f16 v[0:15], v[64:67], v[76:79], v[0:15]
	ds_read_b128 v[48:51], v34 offset:64
	ds_read_b128 v[60:63], v35 offset:18496
	ds_read_b128 v[64:67], v34 offset:96
	ds_read_b128 v[72:75], v35 offset:18528
	s_waitcnt lgkmcnt(2)
	v_mfma_f32_32x32x16_f16 v[16:31], v[48:51], v[60:63], v[16:31]
	ds_read_b128 v[60:63], v35 offset:23104
	ds_read_b128 v[76:79], v35 offset:23136
	s_waitcnt lgkmcnt(0)
	s_barrier
	v_mfma_f32_32x32x16_f16 v[0:15], v[48:51], v[60:63], v[0:15]
	v_mfma_f32_32x32x16_f16 v[16:31], v[64:67], v[72:75], v[16:31]
	global_load_dwordx4 v[48:51], v[36:37], off offset:896
	global_load_dwordx4 v[60:63], v[38:39], off offset:896
	global_load_dwordx4 v[72:75], v[40:41], off offset:896
	global_load_dwordx4 v[84:87], v[42:43], off offset:896
	v_mfma_f32_32x32x16_f16 v[0:15], v[64:67], v[76:79], v[0:15]
	s_waitcnt vmcnt(7)
	ds_write_b128 v45, v[52:55]
	s_waitcnt vmcnt(6)
	ds_write_b128 v46, v[56:59]
	s_waitcnt vmcnt(5)
	ds_write_b128 v45, v[68:71] offset:18432
	s_waitcnt vmcnt(4)
	ds_write_b128 v46, v[80:83] offset:18432
	ds_read_b128 v[52:55], v34 offset:36864
	ds_read_b128 v[56:59], v35 offset:55296
	ds_read_b128 v[64:67], v34 offset:36896
	ds_read_b128 v[68:71], v35 offset:55328
	s_waitcnt lgkmcnt(2)
	v_mfma_f32_32x32x16_f16 v[16:31], v[52:55], v[56:59], v[16:31]
	ds_read_b128 v[56:59], v35 offset:59904
	ds_read_b128 v[76:79], v35 offset:59936
	s_waitcnt lgkmcnt(1)
	v_mfma_f32_32x32x16_f16 v[0:15], v[52:55], v[56:59], v[0:15]
	v_mfma_f32_32x32x16_f16 v[16:31], v[64:67], v[68:71], v[16:31]
	s_waitcnt lgkmcnt(0)
	v_mfma_f32_32x32x16_f16 v[0:15], v[64:67], v[76:79], v[0:15]
	ds_read_b128 v[52:55], v34 offset:36928
	ds_read_b128 v[56:59], v35 offset:55360
	ds_read_b128 v[64:67], v34 offset:36960
	ds_read_b128 v[68:71], v35 offset:55392
	s_waitcnt lgkmcnt(2)
	v_mfma_f32_32x32x16_f16 v[16:31], v[52:55], v[56:59], v[16:31]
	ds_read_b128 v[56:59], v35 offset:59968
	ds_read_b128 v[76:79], v35 offset:60000
	s_waitcnt lgkmcnt(0)
	s_barrier
	v_mfma_f32_32x32x16_f16 v[0:15], v[52:55], v[56:59], v[0:15]
	v_mfma_f32_32x32x16_f16 v[16:31], v[64:67], v[68:71], v[16:31]
	global_load_dwordx4 v[52:55], v[36:37], off offset:1024
	global_load_dwordx4 v[56:59], v[38:39], off offset:1024
	global_load_dwordx4 v[68:71], v[40:41], off offset:1024
	global_load_dwordx4 v[80:83], v[42:43], off offset:1024
	v_mfma_f32_32x32x16_f16 v[0:15], v[64:67], v[76:79], v[0:15]
	s_waitcnt vmcnt(7)
	ds_write_b128 v45, v[48:51] offset:36864
	s_waitcnt vmcnt(6)
	ds_write_b128 v46, v[60:63] offset:36864
	s_waitcnt vmcnt(5)
	ds_write_b128 v45, v[72:75] offset:55296
	s_waitcnt vmcnt(4)
	ds_write_b128 v46, v[84:87] offset:55296
	ds_read_b128 v[48:51], v34
	ds_read_b128 v[60:63], v35 offset:18432
	ds_read_b128 v[64:67], v34 offset:32
	ds_read_b128 v[72:75], v35 offset:18464
	s_waitcnt lgkmcnt(2)
	v_mfma_f32_32x32x16_f16 v[16:31], v[48:51], v[60:63], v[16:31]
	ds_read_b128 v[60:63], v35 offset:23040
	ds_read_b128 v[76:79], v35 offset:23072
	s_waitcnt lgkmcnt(1)
	v_mfma_f32_32x32x16_f16 v[0:15], v[48:51], v[60:63], v[0:15]
	v_mfma_f32_32x32x16_f16 v[16:31], v[64:67], v[72:75], v[16:31]
	s_waitcnt lgkmcnt(0)
	v_mfma_f32_32x32x16_f16 v[0:15], v[64:67], v[76:79], v[0:15]
	ds_read_b128 v[48:51], v34 offset:64
	ds_read_b128 v[60:63], v35 offset:18496
	ds_read_b128 v[64:67], v34 offset:96
	ds_read_b128 v[72:75], v35 offset:18528
	s_waitcnt lgkmcnt(2)
	v_mfma_f32_32x32x16_f16 v[16:31], v[48:51], v[60:63], v[16:31]
	ds_read_b128 v[60:63], v35 offset:23104
	ds_read_b128 v[76:79], v35 offset:23136
	s_waitcnt lgkmcnt(0)
	s_barrier
	v_mfma_f32_32x32x16_f16 v[0:15], v[48:51], v[60:63], v[0:15]
	v_mfma_f32_32x32x16_f16 v[16:31], v[64:67], v[72:75], v[16:31]
	global_load_dwordx4 v[48:51], v[36:37], off offset:1152
	global_load_dwordx4 v[60:63], v[38:39], off offset:1152
	global_load_dwordx4 v[72:75], v[40:41], off offset:1152
	global_load_dwordx4 v[84:87], v[42:43], off offset:1152
	v_mfma_f32_32x32x16_f16 v[0:15], v[64:67], v[76:79], v[0:15]
	s_waitcnt vmcnt(7)
	ds_write_b128 v45, v[52:55]
	s_waitcnt vmcnt(6)
	ds_write_b128 v46, v[56:59]
	s_waitcnt vmcnt(5)
	ds_write_b128 v45, v[68:71] offset:18432
	s_waitcnt vmcnt(4)
	ds_write_b128 v46, v[80:83] offset:18432
	ds_read_b128 v[52:55], v34 offset:36864
	ds_read_b128 v[56:59], v35 offset:55296
	ds_read_b128 v[64:67], v34 offset:36896
	ds_read_b128 v[68:71], v35 offset:55328
	s_waitcnt lgkmcnt(2)
	v_mfma_f32_32x32x16_f16 v[16:31], v[52:55], v[56:59], v[16:31]
	ds_read_b128 v[56:59], v35 offset:59904
	ds_read_b128 v[76:79], v35 offset:59936
	s_waitcnt lgkmcnt(1)
	v_mfma_f32_32x32x16_f16 v[0:15], v[52:55], v[56:59], v[0:15]
	v_mfma_f32_32x32x16_f16 v[16:31], v[64:67], v[68:71], v[16:31]
	s_waitcnt lgkmcnt(0)
	v_mfma_f32_32x32x16_f16 v[0:15], v[64:67], v[76:79], v[0:15]
	ds_read_b128 v[52:55], v34 offset:36928
	ds_read_b128 v[56:59], v35 offset:55360
	ds_read_b128 v[64:67], v34 offset:36960
	ds_read_b128 v[68:71], v35 offset:55392
	s_waitcnt lgkmcnt(2)
	v_mfma_f32_32x32x16_f16 v[16:31], v[52:55], v[56:59], v[16:31]
	ds_read_b128 v[56:59], v35 offset:59968
	ds_read_b128 v[76:79], v35 offset:60000
	s_waitcnt lgkmcnt(0)
	s_barrier
	v_mfma_f32_32x32x16_f16 v[0:15], v[52:55], v[56:59], v[0:15]
	v_mfma_f32_32x32x16_f16 v[16:31], v[64:67], v[68:71], v[16:31]
	global_load_dwordx4 v[52:55], v[36:37], off offset:1280
	global_load_dwordx4 v[56:59], v[38:39], off offset:1280
	global_load_dwordx4 v[68:71], v[40:41], off offset:1280
	global_load_dwordx4 v[80:83], v[42:43], off offset:1280
	v_mfma_f32_32x32x16_f16 v[0:15], v[64:67], v[76:79], v[0:15]
	s_waitcnt vmcnt(7)
	ds_write_b128 v45, v[48:51] offset:36864
	s_waitcnt vmcnt(6)
	ds_write_b128 v46, v[60:63] offset:36864
	s_waitcnt vmcnt(5)
	ds_write_b128 v45, v[72:75] offset:55296
	s_waitcnt vmcnt(4)
	ds_write_b128 v46, v[84:87] offset:55296
	ds_read_b128 v[48:51], v34
	ds_read_b128 v[60:63], v35 offset:18432
	ds_read_b128 v[64:67], v34 offset:32
	ds_read_b128 v[72:75], v35 offset:18464
	s_waitcnt lgkmcnt(2)
	v_mfma_f32_32x32x16_f16 v[16:31], v[48:51], v[60:63], v[16:31]
	ds_read_b128 v[60:63], v35 offset:23040
	ds_read_b128 v[76:79], v35 offset:23072
	s_waitcnt lgkmcnt(1)
	v_mfma_f32_32x32x16_f16 v[0:15], v[48:51], v[60:63], v[0:15]
	v_mfma_f32_32x32x16_f16 v[16:31], v[64:67], v[72:75], v[16:31]
	s_waitcnt lgkmcnt(0)
	v_mfma_f32_32x32x16_f16 v[0:15], v[64:67], v[76:79], v[0:15]
	ds_read_b128 v[48:51], v34 offset:64
	ds_read_b128 v[60:63], v35 offset:18496
	ds_read_b128 v[64:67], v34 offset:96
	ds_read_b128 v[72:75], v35 offset:18528
	s_waitcnt lgkmcnt(2)
	v_mfma_f32_32x32x16_f16 v[16:31], v[48:51], v[60:63], v[16:31]
	ds_read_b128 v[60:63], v35 offset:23104
	ds_read_b128 v[76:79], v35 offset:23136
	s_waitcnt lgkmcnt(0)
	s_barrier
	v_mfma_f32_32x32x16_f16 v[0:15], v[48:51], v[60:63], v[0:15]
	v_mfma_f32_32x32x16_f16 v[16:31], v[64:67], v[72:75], v[16:31]
	global_load_dwordx4 v[48:51], v[36:37], off offset:1408
	global_load_dwordx4 v[60:63], v[38:39], off offset:1408
	global_load_dwordx4 v[72:75], v[40:41], off offset:1408
	global_load_dwordx4 v[84:87], v[42:43], off offset:1408
	v_mfma_f32_32x32x16_f16 v[0:15], v[64:67], v[76:79], v[0:15]
	s_waitcnt vmcnt(7)
	ds_write_b128 v45, v[52:55]
	s_waitcnt vmcnt(6)
	ds_write_b128 v46, v[56:59]
	s_waitcnt vmcnt(5)
	ds_write_b128 v45, v[68:71] offset:18432
	s_waitcnt vmcnt(4)
	ds_write_b128 v46, v[80:83] offset:18432
	ds_read_b128 v[52:55], v34 offset:36864
	ds_read_b128 v[56:59], v35 offset:55296
	ds_read_b128 v[64:67], v34 offset:36896
	ds_read_b128 v[68:71], v35 offset:55328
	s_waitcnt lgkmcnt(2)
	v_mfma_f32_32x32x16_f16 v[16:31], v[52:55], v[56:59], v[16:31]
	ds_read_b128 v[56:59], v35 offset:59904
	ds_read_b128 v[76:79], v35 offset:59936
	s_waitcnt lgkmcnt(1)
	v_mfma_f32_32x32x16_f16 v[0:15], v[52:55], v[56:59], v[0:15]
	v_mfma_f32_32x32x16_f16 v[16:31], v[64:67], v[68:71], v[16:31]
	s_waitcnt lgkmcnt(0)
	v_mfma_f32_32x32x16_f16 v[0:15], v[64:67], v[76:79], v[0:15]
	ds_read_b128 v[52:55], v34 offset:36928
	ds_read_b128 v[56:59], v35 offset:55360
	ds_read_b128 v[64:67], v34 offset:36960
	ds_read_b128 v[68:71], v35 offset:55392
	s_waitcnt lgkmcnt(2)
	v_mfma_f32_32x32x16_f16 v[16:31], v[52:55], v[56:59], v[16:31]
	ds_read_b128 v[56:59], v35 offset:59968
	ds_read_b128 v[76:79], v35 offset:60000
	s_waitcnt lgkmcnt(0)
	s_barrier
	v_mfma_f32_32x32x16_f16 v[0:15], v[52:55], v[56:59], v[0:15]
	v_mfma_f32_32x32x16_f16 v[16:31], v[64:67], v[68:71], v[16:31]
	global_load_dwordx4 v[52:55], v[36:37], off offset:1536
	global_load_dwordx4 v[56:59], v[38:39], off offset:1536
	global_load_dwordx4 v[68:71], v[40:41], off offset:1536
	global_load_dwordx4 v[80:83], v[42:43], off offset:1536
	v_mfma_f32_32x32x16_f16 v[0:15], v[64:67], v[76:79], v[0:15]
	s_waitcnt vmcnt(7)
	ds_write_b128 v45, v[48:51] offset:36864
	s_waitcnt vmcnt(6)
	ds_write_b128 v46, v[60:63] offset:36864
	s_waitcnt vmcnt(5)
	ds_write_b128 v45, v[72:75] offset:55296
	s_waitcnt vmcnt(4)
	ds_write_b128 v46, v[84:87] offset:55296
	ds_read_b128 v[48:51], v34
	ds_read_b128 v[60:63], v35 offset:18432
	ds_read_b128 v[64:67], v34 offset:32
	ds_read_b128 v[72:75], v35 offset:18464
	s_waitcnt lgkmcnt(2)
	v_mfma_f32_32x32x16_f16 v[16:31], v[48:51], v[60:63], v[16:31]
	ds_read_b128 v[60:63], v35 offset:23040
	ds_read_b128 v[76:79], v35 offset:23072
	s_waitcnt lgkmcnt(1)
	v_mfma_f32_32x32x16_f16 v[0:15], v[48:51], v[60:63], v[0:15]
	v_mfma_f32_32x32x16_f16 v[16:31], v[64:67], v[72:75], v[16:31]
	s_waitcnt lgkmcnt(0)
	v_mfma_f32_32x32x16_f16 v[0:15], v[64:67], v[76:79], v[0:15]
	ds_read_b128 v[48:51], v34 offset:64
	ds_read_b128 v[60:63], v35 offset:18496
	ds_read_b128 v[64:67], v34 offset:96
	ds_read_b128 v[72:75], v35 offset:18528
	s_waitcnt lgkmcnt(2)
	v_mfma_f32_32x32x16_f16 v[16:31], v[48:51], v[60:63], v[16:31]
	ds_read_b128 v[60:63], v35 offset:23104
	ds_read_b128 v[76:79], v35 offset:23136
	s_waitcnt lgkmcnt(0)
	s_barrier
	v_mfma_f32_32x32x16_f16 v[0:15], v[48:51], v[60:63], v[0:15]
	v_mfma_f32_32x32x16_f16 v[16:31], v[64:67], v[72:75], v[16:31]
	global_load_dwordx4 v[48:51], v[36:37], off offset:1664
	global_load_dwordx4 v[60:63], v[38:39], off offset:1664
	global_load_dwordx4 v[72:75], v[40:41], off offset:1664
	global_load_dwordx4 v[84:87], v[42:43], off offset:1664
	v_mfma_f32_32x32x16_f16 v[0:15], v[64:67], v[76:79], v[0:15]
	s_waitcnt vmcnt(7)
	ds_write_b128 v45, v[52:55]
	s_waitcnt vmcnt(6)
	ds_write_b128 v46, v[56:59]
	s_waitcnt vmcnt(5)
	ds_write_b128 v45, v[68:71] offset:18432
	s_waitcnt vmcnt(4)
	ds_write_b128 v46, v[80:83] offset:18432
	ds_read_b128 v[52:55], v34 offset:36864
	ds_read_b128 v[56:59], v35 offset:55296
	ds_read_b128 v[64:67], v34 offset:36896
	ds_read_b128 v[68:71], v35 offset:55328
	s_waitcnt lgkmcnt(2)
	v_mfma_f32_32x32x16_f16 v[16:31], v[52:55], v[56:59], v[16:31]
	ds_read_b128 v[56:59], v35 offset:59904
	ds_read_b128 v[76:79], v35 offset:59936
	s_waitcnt lgkmcnt(1)
	v_mfma_f32_32x32x16_f16 v[0:15], v[52:55], v[56:59], v[0:15]
	v_mfma_f32_32x32x16_f16 v[16:31], v[64:67], v[68:71], v[16:31]
	s_waitcnt lgkmcnt(0)
	v_mfma_f32_32x32x16_f16 v[0:15], v[64:67], v[76:79], v[0:15]
	ds_read_b128 v[52:55], v34 offset:36928
	ds_read_b128 v[56:59], v35 offset:55360
	ds_read_b128 v[64:67], v34 offset:36960
	ds_read_b128 v[68:71], v35 offset:55392
	s_waitcnt lgkmcnt(2)
	v_mfma_f32_32x32x16_f16 v[16:31], v[52:55], v[56:59], v[16:31]
	ds_read_b128 v[56:59], v35 offset:59968
	ds_read_b128 v[76:79], v35 offset:60000
	s_waitcnt lgkmcnt(0)
	s_barrier
	v_mfma_f32_32x32x16_f16 v[0:15], v[52:55], v[56:59], v[0:15]
	v_mfma_f32_32x32x16_f16 v[16:31], v[64:67], v[68:71], v[16:31]
	global_load_dwordx4 v[52:55], v[36:37], off offset:1792
	global_load_dwordx4 v[56:59], v[38:39], off offset:1792
	global_load_dwordx4 v[68:71], v[40:41], off offset:1792
	global_load_dwordx4 v[80:83], v[42:43], off offset:1792
	v_mfma_f32_32x32x16_f16 v[0:15], v[64:67], v[76:79], v[0:15]
	s_waitcnt vmcnt(7)
	ds_write_b128 v45, v[48:51] offset:36864
	s_waitcnt vmcnt(6)
	ds_write_b128 v46, v[60:63] offset:36864
	s_waitcnt vmcnt(5)
	ds_write_b128 v45, v[72:75] offset:55296
	s_waitcnt vmcnt(4)
	ds_write_b128 v46, v[84:87] offset:55296
	ds_read_b128 v[48:51], v34
	ds_read_b128 v[60:63], v35 offset:18432
	ds_read_b128 v[64:67], v34 offset:32
	ds_read_b128 v[72:75], v35 offset:18464
	s_waitcnt lgkmcnt(2)
	v_mfma_f32_32x32x16_f16 v[16:31], v[48:51], v[60:63], v[16:31]
	ds_read_b128 v[60:63], v35 offset:23040
	ds_read_b128 v[76:79], v35 offset:23072
	s_waitcnt lgkmcnt(1)
	v_mfma_f32_32x32x16_f16 v[0:15], v[48:51], v[60:63], v[0:15]
	v_mfma_f32_32x32x16_f16 v[16:31], v[64:67], v[72:75], v[16:31]
	s_waitcnt lgkmcnt(0)
	v_mfma_f32_32x32x16_f16 v[0:15], v[64:67], v[76:79], v[0:15]
	ds_read_b128 v[48:51], v34 offset:64
	ds_read_b128 v[60:63], v35 offset:18496
	ds_read_b128 v[64:67], v34 offset:96
	ds_read_b128 v[72:75], v35 offset:18528
	s_waitcnt lgkmcnt(2)
	v_mfma_f32_32x32x16_f16 v[16:31], v[48:51], v[60:63], v[16:31]
	ds_read_b128 v[60:63], v35 offset:23104
	ds_read_b128 v[76:79], v35 offset:23136
	s_waitcnt lgkmcnt(0)
	s_barrier
	v_mfma_f32_32x32x16_f16 v[0:15], v[48:51], v[60:63], v[0:15]
	v_mfma_f32_32x32x16_f16 v[16:31], v[64:67], v[72:75], v[16:31]
	global_load_dwordx4 v[48:51], v[36:37], off offset:1920
	global_load_dwordx4 v[60:63], v[38:39], off offset:1920
	global_load_dwordx4 v[72:75], v[40:41], off offset:1920
	global_load_dwordx4 v[84:87], v[42:43], off offset:1920
	v_mfma_f32_32x32x16_f16 v[0:15], v[64:67], v[76:79], v[0:15]
	s_waitcnt vmcnt(7)
	ds_write_b128 v45, v[52:55]
	s_waitcnt vmcnt(6)
	ds_write_b128 v46, v[56:59]
	s_waitcnt vmcnt(5)
	ds_write_b128 v45, v[68:71] offset:18432
	s_waitcnt vmcnt(4)
	ds_write_b128 v46, v[80:83] offset:18432
	ds_read_b128 v[36:39], v34 offset:36864
	ds_read_b128 v[40:43], v35 offset:55296
	ds_read_b128 v[52:55], v34 offset:36896
	ds_read_b128 v[56:59], v35 offset:55328
	s_waitcnt lgkmcnt(2)
	v_mfma_f32_32x32x16_f16 v[16:31], v[36:39], v[40:43], v[16:31]
	ds_read_b128 v[40:43], v35 offset:59904
	ds_read_b128 v[64:67], v35 offset:59936
	s_waitcnt lgkmcnt(1)
	v_mfma_f32_32x32x16_f16 v[0:15], v[36:39], v[40:43], v[0:15]
	v_mfma_f32_32x32x16_f16 v[16:31], v[52:55], v[56:59], v[16:31]
	s_waitcnt lgkmcnt(0)
	v_mfma_f32_32x32x16_f16 v[0:15], v[52:55], v[64:67], v[0:15]
	ds_read_b128 v[36:39], v34 offset:36928
	ds_read_b128 v[40:43], v35 offset:55360
	ds_read_b128 v[52:55], v34 offset:36960
	ds_read_b128 v[56:59], v35 offset:55392
	s_waitcnt lgkmcnt(2)
	v_mfma_f32_32x32x16_f16 v[16:31], v[36:39], v[40:43], v[16:31]
	ds_read_b128 v[40:43], v35 offset:59968
	ds_read_b128 v[64:67], v35 offset:60000
	s_waitcnt lgkmcnt(0)
	s_barrier
	v_mfma_f32_32x32x16_f16 v[0:15], v[36:39], v[40:43], v[0:15]
	v_mfma_f32_32x32x16_f16 v[16:31], v[52:55], v[56:59], v[16:31]
	v_mfma_f32_32x32x16_f16 v[0:15], v[52:55], v[64:67], v[0:15]
	s_waitcnt vmcnt(3)
	ds_write_b128 v45, v[48:51] offset:36864
	s_waitcnt vmcnt(2)
	ds_write_b128 v46, v[60:63] offset:36864
	s_waitcnt vmcnt(1)
	ds_write_b128 v45, v[72:75] offset:55296
	s_waitcnt vmcnt(0)
	ds_write_b128 v46, v[84:87] offset:55296
	ds_read_b128 v[36:39], v34
	ds_read_b128 v[40:43], v35 offset:18432
	ds_read_b128 v[46:49], v34 offset:32
	ds_read_b128 v[50:53], v35 offset:18464
	s_waitcnt lgkmcnt(2)
	v_mfma_f32_32x32x16_f16 v[16:31], v[36:39], v[40:43], v[16:31]
	ds_read_b128 v[40:43], v35 offset:23040
	ds_read_b128 v[54:57], v35 offset:23072
	s_waitcnt lgkmcnt(1)
	v_mfma_f32_32x32x16_f16 v[0:15], v[36:39], v[40:43], v[0:15]
	v_mfma_f32_32x32x16_f16 v[16:31], v[46:49], v[50:53], v[16:31]
	s_waitcnt lgkmcnt(0)
	v_mfma_f32_32x32x16_f16 v[0:15], v[46:49], v[54:57], v[0:15]
	ds_read_b128 v[36:39], v34 offset:64
	ds_read_b128 v[40:43], v35 offset:18496
	ds_read_b128 v[46:49], v34 offset:96
	ds_read_b128 v[50:53], v35 offset:18528
	s_waitcnt lgkmcnt(2)
	v_mfma_f32_32x32x16_f16 v[16:31], v[36:39], v[40:43], v[16:31]
	ds_read_b128 v[40:43], v35 offset:23104
	ds_read_b128 v[54:57], v35 offset:23136
	s_waitcnt lgkmcnt(0)
	s_barrier
	v_mfma_f32_32x32x16_f16 v[0:15], v[36:39], v[40:43], v[0:15]
	v_mfma_f32_32x32x16_f16 v[16:31], v[46:49], v[50:53], v[16:31]
	v_mfma_f32_32x32x16_f16 v[0:15], v[46:49], v[54:57], v[0:15]
	ds_read_b128 v[36:39], v34 offset:36864
	ds_read_b128 v[40:43], v35 offset:55296
	ds_read_b128 v[46:49], v34 offset:36896
	ds_read_b128 v[50:53], v35 offset:55328
	ds_read_b128 v[54:57], v35 offset:59904
	ds_read_b128 v[58:61], v35 offset:59936
	s_waitcnt lgkmcnt(4)
	v_mfma_f32_32x32x16_f16 v[16:31], v[36:39], v[40:43], v[16:31]
	ds_read_b128 v[40:43], v34 offset:36928
	ds_read_b128 v[62:65], v34 offset:36960
	ds_read_b128 v[66:69], v35 offset:55360
	ds_read_b128 v[70:73], v35 offset:55392
	ds_read_b128 v[74:77], v35 offset:59968
	ds_read_b128 v[78:81], v35 offset:60000
	s_lshl_b32 s2, s2, 7
	s_add_i32 s3, s3, s2
	s_or_b32 s0, s1, s0
	v_lshl_or_b32 v32, v32, 2, s3
	v_or_b32_e32 v34, s0, v44
	v_mov_b32_e32 v35, v33
	s_waitcnt lgkmcnt(7)
	v_mfma_f32_32x32x16_f16 v[0:15], v[36:39], v[54:57], v[0:15]
	v_lshlrev_b64 v[36:37], 12, v[32:33]
	v_lshl_add_u64 v[34:35], v[34:35], 2, s[4:5]
	v_or_b32_e32 v38, 1, v32
	v_mov_b32_e32 v39, v33
	v_or_b32_e32 v44, 2, v32
	v_mov_b32_e32 v45, v33
	v_or_b32_e32 v54, 17, v32
	v_mfma_f32_32x32x16_f16 v[16:31], v[46:49], v[50:53], v[16:31]
	v_or_b32_e32 v50, 9, v32
	v_mov_b32_e32 v51, v33
	v_or_b32_e32 v52, 16, v32
	v_mov_b32_e32 v53, v33
	v_mov_b32_e32 v55, v33
	v_or_b32_e32 v56, 18, v32
	v_mov_b32_e32 v57, v33
	s_waitcnt lgkmcnt(6)
	v_mfma_f32_32x32x16_f16 v[0:15], v[46:49], v[58:61], v[0:15]
	v_or_b32_e32 v46, 3, v32
	v_mov_b32_e32 v47, v33
	v_or_b32_e32 v48, 8, v32
	v_mov_b32_e32 v49, v33
	v_or_b32_e32 v58, 19, v32
	v_mov_b32_e32 v59, v33
	v_or_b32_e32 v60, 24, v32
	s_waitcnt lgkmcnt(3)
	v_mfma_f32_32x32x16_f16 v[16:31], v[40:43], v[66:69], v[16:31]
	v_mov_b32_e32 v61, v33
	v_or_b32_e32 v66, 25, v32
	v_mov_b32_e32 v67, v33
	v_or_b32_e32 v68, 26, v32
	v_mov_b32_e32 v69, v33
	v_lshl_add_u64 v[36:37], v[34:35], 0, v[36:37]
	v_lshlrev_b64 v[38:39], 12, v[38:39]
	s_waitcnt lgkmcnt(1)
	v_mfma_f32_32x32x16_f16 v[0:15], v[40:43], v[74:77], v[0:15]
	v_or_b32_e32 v40, 10, v32
	v_mov_b32_e32 v41, v33
	v_or_b32_e32 v42, 11, v32
	v_mov_b32_e32 v43, v33
	v_or_b32_e32 v32, 27, v32
	v_lshlrev_b64 v[44:45], 12, v[44:45]
	v_lshlrev_b64 v[46:47], 12, v[46:47]
	v_mfma_f32_32x32x16_f16 v[16:31], v[62:65], v[70:73], v[16:31]
	v_lshlrev_b64 v[48:49], 12, v[48:49]
	v_lshlrev_b64 v[50:51], 12, v[50:51]
	v_lshlrev_b64 v[40:41], 12, v[40:41]
	v_lshlrev_b64 v[42:43], 12, v[42:43]
	v_lshlrev_b64 v[52:53], 12, v[52:53]
	v_lshlrev_b64 v[54:55], 12, v[54:55]
	v_lshlrev_b64 v[56:57], 12, v[56:57]
	s_waitcnt lgkmcnt(0)
	v_mfma_f32_32x32x16_f16 v[0:15], v[62:65], v[78:81], v[0:15]
	v_lshlrev_b64 v[58:59], 12, v[58:59]
	v_lshlrev_b64 v[60:61], 12, v[60:61]
	v_lshlrev_b64 v[66:67], 12, v[66:67]
	v_lshlrev_b64 v[68:69], 12, v[68:69]
	v_lshlrev_b64 v[32:33], 12, v[32:33]
	v_lshl_add_u64 v[38:39], v[34:35], 0, v[38:39]
	v_lshl_add_u64 v[44:45], v[34:35], 0, v[44:45]
	v_lshl_add_u64 v[46:47], v[34:35], 0, v[46:47]
	v_lshl_add_u64 v[48:49], v[34:35], 0, v[48:49]
	v_lshl_add_u64 v[50:51], v[34:35], 0, v[50:51]
	v_lshl_add_u64 v[40:41], v[34:35], 0, v[40:41]
	v_lshl_add_u64 v[42:43], v[34:35], 0, v[42:43]
	v_lshl_add_u64 v[52:53], v[34:35], 0, v[52:53]
	v_lshl_add_u64 v[54:55], v[34:35], 0, v[54:55]
	v_lshl_add_u64 v[56:57], v[34:35], 0, v[56:57]
	v_lshl_add_u64 v[58:59], v[34:35], 0, v[58:59]
	v_lshl_add_u64 v[60:61], v[34:35], 0, v[60:61]
	v_lshl_add_u64 v[66:67], v[34:35], 0, v[66:67]
	v_lshl_add_u64 v[68:69], v[34:35], 0, v[68:69]
	v_lshl_add_u64 v[32:33], v[34:35], 0, v[32:33]
	s_barrier
	global_store_dword v[36:37], v16, off
	global_store_dword v[38:39], v17, off
	global_store_dword v[44:45], v18, off
	global_store_dword v[46:47], v19, off
	global_store_dword v[48:49], v20, off
	global_store_dword v[50:51], v21, off
	global_store_dword v[40:41], v22, off
	global_store_dword v[42:43], v23, off
	global_store_dword v[52:53], v24, off
	global_store_dword v[54:55], v25, off
	global_store_dword v[56:57], v26, off
	global_store_dword v[58:59], v27, off
	global_store_dword v[60:61], v28, off
	global_store_dword v[66:67], v29, off
	global_store_dword v[68:69], v30, off
	global_store_dword v[32:33], v31, off
	global_store_dword v[36:37], v0, off offset:128
	global_store_dword v[38:39], v1, off offset:128
	global_store_dword v[44:45], v2, off offset:128
	global_store_dword v[46:47], v3, off offset:128
	global_store_dword v[48:49], v4, off offset:128
	global_store_dword v[50:51], v5, off offset:128
	global_store_dword v[40:41], v6, off offset:128
	global_store_dword v[42:43], v7, off offset:128
	global_store_dword v[52:53], v8, off offset:128
	global_store_dword v[54:55], v9, off offset:128
	global_store_dword v[56:57], v10, off offset:128
	global_store_dword v[58:59], v11, off offset:128
	global_store_dword v[60:61], v12, off offset:128
	global_store_dword v[66:67], v13, off offset:128
	global_store_dword v[68:69], v14, off offset:128
	global_store_dword v[32:33], v15, off offset:128
	s_endpgm
	.p2alignl 8, 3212836864

_Z11attn_kernelILi0EEvPKDF16_S1_S1_PKfS3_PfPDF16_:
	v_readfirstlane_b32 s3, v0
	s_lshr_b32 s14, s3, 6
	s_lshl_b32 s3, s2, 7
	s_lshr_b32 s12, s2, 4
	s_and_b32 s3, s3, 0x780
	s_lshl_b32 s4, s14, 5
	s_mov_b32 s13, 0
	s_load_dwordx4 s[8:11], s[0:1], 0x0
	s_load_dwordx2 s[18:19], s[0:1], 0x10
	s_add_i32 s3, s4, s3
	s_lshl_b64 s[4:5], s[12:13], 11
	s_add_u32 s16, s4, s3
	s_addc_u32 s17, s5, 0
	s_lshl_b64 s[4:5], s[16:17], 7
	v_and_b32_e32 v164, 31, v0
	s_waitcnt lgkmcnt(0)
	s_add_u32 s4, s8, s4
	v_bfe_u32 v72, v0, 5, 1
	s_addc_u32 s5, s9, s5
	s_lshl_b64 s[22:23], s[12:13], 18
	v_lshlrev_b32_e32 v128, 7, v164
	v_mov_b32_e32 v129, 0
	s_add_u32 s8, s10, s22
	v_lshl_add_u64 v[2:3], s[4:5], 0, v[128:129]
	v_lshlrev_b32_e32 v128, 4, v72
	s_addc_u32 s9, s11, s23
	v_lshl_add_u64 v[10:11], v[2:3], 0, v[128:129]
	v_or_b32_e32 v12, 0x100, v0
	v_lshlrev_b32_e32 v128, 4, v0
	v_lshlrev_b32_e32 v44, 4, v12
	global_load_dwordx4 v[2:5], v128, s[8:9]
	global_load_dwordx4 v[6:9], v44, s[8:9]
	v_lshlrev_b32_e32 v79, 3, v0
	s_movk_i32 s4, 0x48
	v_lshrrev_b32_e32 v73, 3, v0
	v_and_b32_e32 v74, 56, v79
	v_lshrrev_b32_e32 v75, 3, v12
	v_mad_u32_u24 v165, v75, s4, v74
	v_mad_u32_u24 v166, v73, s4, v74
	global_load_dwordx4 v[108:111], v[10:11], off
	global_load_dwordx4 v[104:107], v[10:11], off offset:32
	global_load_dwordx4 v[100:103], v[10:11], off offset:64
	global_load_dwordx4 v[96:99], v[10:11], off offset:96
	s_add_u32 s4, s8, 0x2000
	v_lshlrev_b32_e32 v13, 1, v166
	s_addc_u32 s5, s9, 0
	v_lshlrev_b32_e32 v14, 1, v165
	v_lshlrev_b32_e32 v1, 3, v72
	v_mul_u32_u24_e32 v76, 0x48, v164
	v_lshlrev_b32_e32 v80, 3, v12
	v_mov_b32_e32 v45, v129
	s_mov_b32 s15, 1
	v_add_u32_e32 v77, 0x6000, v13
	v_add_u32_e32 v78, 0x6000, v14
	s_waitcnt vmcnt(5)
	ds_write_b128 v13, v[2:5] offset:24576
	s_waitcnt vmcnt(4)
	ds_write_b128 v14, v[6:9] offset:24576
	s_waitcnt lgkmcnt(0)
	s_barrier
	s_load_dwordx4 s[4:7], s[0:1], 0x28
	v_mov_b32_e32 v86, v44
	s_add_u32 s24, s8, 0x2000
	s_addc_u32 s25, s9, 0
	global_load_dwordx4 v[120:123], v128, s[24:25]
	global_load_dwordx4 v[124:127], v44, s[24:25]
	s_add_u32 s24, s24, 0x2000
	s_addc_u32 s25, s25, 0
	v_add_lshl_u32 v3, v1, v76, 1
	v_lshl_add_u64 v[68:69], s[8:9], 0, v[44:45]
	v_lshl_add_u64 v[66:67], s[8:9], 0, v[128:129]
	v_add_u32_e32 v167, 0x6000, v3
	s_lshl_b64 s[20:21], s[12:13], 17
	v_mov_b32_e32 v81, 0
	v_mov_b32_e32 v82, 0
	v_mov_b32_e32 v130, 0
	v_mov_b32_e32 v131, 0
	v_mov_b32_e32 v132, 0
	v_mov_b32_e32 v133, 0
	v_mov_b32_e32 v134, 0
	v_mov_b32_e32 v135, 0
	v_mov_b32_e32 v136, 0
	v_mov_b32_e32 v137, 0
	v_mov_b32_e32 v138, 0
	v_mov_b32_e32 v139, 0
	v_mov_b32_e32 v140, 0
	v_mov_b32_e32 v141, 0
	v_mov_b32_e32 v142, 0
	v_mov_b32_e32 v143, 0
	v_mov_b32_e32 v144, 0
	v_mov_b32_e32 v145, 0
	v_mov_b32_e32 v34, 0xff800000
	v_mov_b32_e32 v35, v34
	v_mov_b32_e32 v36, v34
	v_mov_b32_e32 v37, v34
	v_mov_b32_e32 v38, v34
	v_mov_b32_e32 v39, v34
	v_mov_b32_e32 v40, v34
	v_mov_b32_e32 v41, v34
	v_mov_b32_e32 v42, v34
	v_mov_b32_e32 v43, v34
	v_mov_b32_e32 v44, v34
	v_mov_b32_e32 v45, v34
	v_mov_b32_e32 v46, v34
	v_mov_b32_e32 v47, v34
	v_mov_b32_e32 v48, v34
	v_mov_b32_e32 v49, v34
	v_mov_b32_e32 v50, v34
	v_mov_b32_e32 v51, v34
	v_mov_b32_e32 v52, v34
	v_mov_b32_e32 v53, v34
	v_mov_b32_e32 v54, v34
	v_mov_b32_e32 v55, v34
	v_mov_b32_e32 v56, v34
	v_mov_b32_e32 v57, v34
	v_mov_b32_e32 v58, v34
	v_mov_b32_e32 v59, v34
	v_mov_b32_e32 v60, v34
	v_mov_b32_e32 v61, v34
	v_mov_b32_e32 v62, v34
	v_mov_b32_e32 v63, v34
	v_mov_b32_e32 v64, v34
	v_mov_b32_e32 v65, v34
	s_mov_b32 s11, 0xff800000
	s_mov_b32 s15, 0
	s_waitcnt vmcnt(2) lgkmcnt(0)
.Lp1_loop:
	global_load_dwordx4 v[112:115], v128, s[24:25]
	global_load_dwordx4 v[116:119], v86, s[24:25]
	ds_read_b128 v[168:171], v167
	ds_read_b128 v[172:175], v167 offset:4608
	ds_read_b128 v[176:179], v167 offset:32
	ds_read_b128 v[180:183], v167 offset:4640
	ds_read_b128 v[184:187], v167 offset:64
	ds_read_b128 v[188:191], v167 offset:4672
	ds_read_b128 v[192:195], v167 offset:96
	ds_read_b128 v[196:199], v167 offset:4704
	v_mov_b32_e32 v200, 0
	v_mov_b32_e32 v201, 0
	v_mov_b32_e32 v202, 0
	v_mov_b32_e32 v83, 0
	v_exp_f32_e32 v34, v34
	v_exp_f32_e32 v35, v35
	v_add_f32_e32 v200, v200, v34
	v_exp_f32_e32 v36, v36
	v_add_f32_e32 v201, v201, v35
	v_exp_f32_e32 v37, v37
	s_waitcnt lgkmcnt(7)
	v_mfma_f32_32x32x16_f16 v[2:17], v[168:171], v[108:111], v[130:145]
	v_add_f32_e32 v202, v202, v36
	v_exp_f32_e32 v38, v38
	v_add_f32_e32 v83, v83, v37
	v_exp_f32_e32 v39, v39
	v_add_f32_e32 v200, v200, v38
	v_exp_f32_e32 v40, v40
	s_waitcnt lgkmcnt(6)
	v_mfma_f32_32x32x16_f16 v[18:33], v[172:175], v[108:111], v[130:145]
	v_add_f32_e32 v201, v201, v39
	v_exp_f32_e32 v41, v41
	v_add_f32_e32 v202, v202, v40
	v_exp_f32_e32 v42, v42
	v_add_f32_e32 v83, v83, v41
	v_exp_f32_e32 v43, v43
	s_waitcnt lgkmcnt(5)
	v_mfma_f32_32x32x16_f16 v[2:17], v[176:179], v[104:107], v[2:17]
	v_add_f32_e32 v200, v200, v42
	v_exp_f32_e32 v44, v44
	v_add_f32_e32 v201, v201, v43
	v_exp_f32_e32 v45, v45
	v_add_f32_e32 v202, v202, v44
	v_exp_f32_e32 v46, v46
	s_waitcnt lgkmcnt(4)
	v_mfma_f32_32x32x16_f16 v[18:33], v[180:183], v[104:107], v[18:33]
	v_add_f32_e32 v83, v83, v45
	v_exp_f32_e32 v47, v47
	v_add_f32_e32 v200, v200, v46
	v_exp_f32_e32 v48, v48
	v_add_f32_e32 v201, v201, v47
	v_exp_f32_e32 v49, v49
	s_waitcnt lgkmcnt(3)
	v_mfma_f32_32x32x16_f16 v[2:17], v[184:187], v[100:103], v[2:17]
	v_add_f32_e32 v202, v202, v48
	v_exp_f32_e32 v50, v50
	v_add_f32_e32 v83, v83, v49
	v_exp_f32_e32 v51, v51
	v_add_f32_e32 v200, v200, v50
	v_exp_f32_e32 v52, v52
	s_waitcnt lgkmcnt(2)
	v_mfma_f32_32x32x16_f16 v[18:33], v[188:191], v[100:103], v[18:33]
	v_add_f32_e32 v201, v201, v51
	v_exp_f32_e32 v53, v53
	v_add_f32_e32 v202, v202, v52
	v_exp_f32_e32 v54, v54
	v_add_f32_e32 v83, v83, v53
	v_exp_f32_e32 v55, v55
	s_waitcnt lgkmcnt(1)
	v_mfma_f32_32x32x16_f16 v[2:17], v[192:195], v[96:99], v[2:17]
	v_add_f32_e32 v200, v200, v54
	v_exp_f32_e32 v56, v56
	v_add_f32_e32 v201, v201, v55
	v_exp_f32_e32 v57, v57
	v_add_f32_e32 v202, v202, v56
	v_exp_f32_e32 v58, v58
	s_waitcnt lgkmcnt(0)
	v_mfma_f32_32x32x16_f16 v[18:33], v[196:199], v[96:99], v[18:33]
	v_add_f32_e32 v83, v83, v57
	v_exp_f32_e32 v59, v59
	v_add_f32_e32 v200, v200, v58
	v_exp_f32_e32 v60, v60
	v_add_f32_e32 v201, v201, v59
	v_exp_f32_e32 v61, v61
	v_add_f32_e32 v202, v202, v60
	v_exp_f32_e32 v62, v62
	v_add_f32_e32 v83, v83, v61
	v_exp_f32_e32 v63, v63
	v_add_f32_e32 v200, v200, v62
	v_exp_f32_e32 v64, v64
	v_add_f32_e32 v201, v201, v63
	v_exp_f32_e32 v65, v65
	v_add_f32_e32 v202, v202, v64
	v_add_f32_e32 v83, v83, v65
	v_add_f32_e32 v200, v200, v201
	v_add_f32_e32 v202, v202, v83
	v_add_f32_e32 v200, v200, v202
	v_add_f32_e32 v82, v82, v200
	v_max3_f32 v84, v2, v3, v4
	v_max3_f32 v85, v18, v19, v20
	v_max3_f32 v84, v84, v5, v6
	v_max3_f32 v85, v85, v21, v22
	v_max3_f32 v84, v84, v7, v8
	v_max3_f32 v85, v85, v23, v24
	v_max3_f32 v84, v84, v9, v10
	v_max3_f32 v85, v85, v25, v26
	v_max3_f32 v84, v84, v11, v12
	v_max3_f32 v85, v85, v27, v28
	v_max3_f32 v84, v84, v13, v14
	v_max3_f32 v85, v85, v29, v30
	v_max3_f32 v84, v84, v15, v16
	v_max3_f32 v85, v85, v31, v32
	v_max3_f32 v84, v84, v17, v33
	s_nop 0
	v_max_f32_e32 v84, v84, v85
	s_nop 0
	v_cmp_lt_f32_e32 vcc, s11, v84
	s_cbranch_vccnz .Lp1_rare_e
.Lp1_back_e:
	s_add_u32 s24, s24, 0x2000
	s_addc_u32 s25, s25, 0
	s_waitcnt vmcnt(2)
	ds_write_b128 v77, v[120:123] offset:9216
	ds_write_b128 v78, v[124:127] offset:9216
	s_waitcnt lgkmcnt(0)
	s_barrier
	global_load_dwordx4 v[120:123], v128, s[24:25]
	global_load_dwordx4 v[124:127], v86, s[24:25]
	ds_read_b128 v[168:171], v167 offset:9216
	ds_read_b128 v[172:175], v167 offset:13824
	ds_read_b128 v[176:179], v167 offset:9248
	ds_read_b128 v[180:183], v167 offset:13856
	ds_read_b128 v[184:187], v167 offset:9280
	ds_read_b128 v[188:191], v167 offset:13888
	ds_read_b128 v[192:195], v167 offset:9312
	ds_read_b128 v[196:199], v167 offset:13920
	v_mov_b32_e32 v200, 0
	v_mov_b32_e32 v201, 0
	v_mov_b32_e32 v202, 0
	v_mov_b32_e32 v83, 0
	v_exp_f32_e32 v2, v2
	v_exp_f32_e32 v3, v3
	v_add_f32_e32 v200, v200, v2
	v_exp_f32_e32 v4, v4
	v_add_f32_e32 v201, v201, v3
	v_exp_f32_e32 v5, v5
	s_waitcnt lgkmcnt(7)
	v_mfma_f32_32x32x16_f16 v[34:49], v[168:171], v[108:111], v[130:145]
	v_add_f32_e32 v202, v202, v4
	v_exp_f32_e32 v6, v6
	v_add_f32_e32 v83, v83, v5
	v_exp_f32_e32 v7, v7
	v_add_f32_e32 v200, v200, v6
	v_exp_f32_e32 v8, v8
	s_waitcnt lgkmcnt(6)
	v_mfma_f32_32x32x16_f16 v[50:65], v[172:175], v[108:111], v[130:145]
	v_add_f32_e32 v201, v201, v7
	v_exp_f32_e32 v9, v9
	v_add_f32_e32 v202, v202, v8
	v_exp_f32_e32 v10, v10
	v_add_f32_e32 v83, v83, v9
	v_exp_f32_e32 v11, v11
	s_waitcnt lgkmcnt(5)
	v_mfma_f32_32x32x16_f16 v[34:49], v[176:179], v[104:107], v[34:49]
	v_add_f32_e32 v200, v200, v10
	v_exp_f32_e32 v12, v12
	v_add_f32_e32 v201, v201, v11
	v_exp_f32_e32 v13, v13
	v_add_f32_e32 v202, v202, v12
	v_exp_f32_e32 v14, v14
	s_waitcnt lgkmcnt(4)
	v_mfma_f32_32x32x16_f16 v[50:65], v[180:183], v[104:107], v[50:65]
	v_add_f32_e32 v83, v83, v13
	v_exp_f32_e32 v15, v15
	v_add_f32_e32 v200, v200, v14
	v_exp_f32_e32 v16, v16
	v_add_f32_e32 v201, v201, v15
	v_exp_f32_e32 v17, v17
	s_waitcnt lgkmcnt(3)
	v_mfma_f32_32x32x16_f16 v[34:49], v[184:187], v[100:103], v[34:49]
	v_add_f32_e32 v202, v202, v16
	v_exp_f32_e32 v18, v18
	v_add_f32_e32 v83, v83, v17
	v_exp_f32_e32 v19, v19
	v_add_f32_e32 v200, v200, v18
	v_exp_f32_e32 v20, v20
	s_waitcnt lgkmcnt(2)
	v_mfma_f32_32x32x16_f16 v[50:65], v[188:191], v[100:103], v[50:65]
	v_add_f32_e32 v201, v201, v19
	v_exp_f32_e32 v21, v21
	v_add_f32_e32 v202, v202, v20
	v_exp_f32_e32 v22, v22
	v_add_f32_e32 v83, v83, v21
	v_exp_f32_e32 v23, v23
	s_waitcnt lgkmcnt(1)
	v_mfma_f32_32x32x16_f16 v[34:49], v[192:195], v[96:99], v[34:49]
	v_add_f32_e32 v200, v200, v22
	v_exp_f32_e32 v24, v24
	v_add_f32_e32 v201, v201, v23
	v_exp_f32_e32 v25, v25
	v_add_f32_e32 v202, v202, v24
	v_exp_f32_e32 v26, v26
	s_waitcnt lgkmcnt(0)
	v_mfma_f32_32x32x16_f16 v[50:65], v[196:199], v[96:99], v[50:65]
	v_add_f32_e32 v83, v83, v25
	v_exp_f32_e32 v27, v27
	v_add_f32_e32 v200, v200, v26
	v_exp_f32_e32 v28, v28
	v_add_f32_e32 v201, v201, v27
	v_exp_f32_e32 v29, v29
	v_add_f32_e32 v202, v202, v28
	v_exp_f32_e32 v30, v30
	v_add_f32_e32 v83, v83, v29
	v_exp_f32_e32 v31, v31
	v_add_f32_e32 v200, v200, v30
	v_exp_f32_e32 v32, v32
	v_add_f32_e32 v201, v201, v31
	v_exp_f32_e32 v33, v33
	v_add_f32_e32 v202, v202, v32
	v_add_f32_e32 v83, v83, v33
	v_add_f32_e32 v200, v200, v201
	v_add_f32_e32 v202, v202, v83
	v_add_f32_e32 v200, v200, v202
	v_add_f32_e32 v82, v82, v200
	v_max3_f32 v84, v34, v35, v36
	v_max3_f32 v85, v50, v51, v52
	v_max3_f32 v84, v84, v37, v38
	v_max3_f32 v85, v85, v53, v54
	v_max3_f32 v84, v84, v39, v40
	v_max3_f32 v85, v85, v55, v56
	v_max3_f32 v84, v84, v41, v42
	v_max3_f32 v85, v85, v57, v58
	v_max3_f32 v84, v84, v43, v44
	v_max3_f32 v85, v85, v59, v60
	v_max3_f32 v84, v84, v45, v46
	v_max3_f32 v85, v85, v61, v62
	v_max3_f32 v84, v84, v47, v48
	v_max3_f32 v85, v85, v63, v64
	v_max3_f32 v84, v84, v49, v65
	s_nop 0
	v_max_f32_e32 v84, v84, v85
	s_nop 0
	v_cmp_lt_f32_e32 vcc, s11, v84
	s_cbranch_vccnz .Lp1_rare_o
.Lp1_back_o:
	s_add_u32 s24, s24, 0x2000
	s_addc_u32 s25, s25, 0
	s_waitcnt vmcnt(2)
	ds_write_b128 v77, v[112:115]
	ds_write_b128 v78, v[116:119]
	s_add_i32 s15, s15, 2
	s_cmp_lt_u32 s15, 32
	s_waitcnt lgkmcnt(0)
	s_barrier
	s_cbranch_scc1 .Lp1_loop
	s_branch .Lp1_fin
.Lp1_rare_e:
	s_nop 1
	v_cndmask_b32_e32 v84, 0, v84, vcc
	v_exp_f32_e64 v85, -v84
	v_add_f32_e32 v81, v81, v84
	v_sub_f32_e32 v2, v2, v84
	v_sub_f32_e32 v3, v3, v84
	v_sub_f32_e32 v4, v4, v84
	v_sub_f32_e32 v5, v5, v84
	v_sub_f32_e32 v6, v6, v84
	v_sub_f32_e32 v7, v7, v84
	v_sub_f32_e32 v8, v8, v84
	v_sub_f32_e32 v9, v9, v84
	v_sub_f32_e32 v10, v10, v84
	v_sub_f32_e32 v11, v11, v84
	v_sub_f32_e32 v12, v12, v84
	v_sub_f32_e32 v13, v13, v84
	v_sub_f32_e32 v14, v14, v84
	v_sub_f32_e32 v15, v15, v84
	v_sub_f32_e32 v16, v16, v84
	v_sub_f32_e32 v17, v17, v84
	v_sub_f32_e32 v18, v18, v84
	v_sub_f32_e32 v19, v19, v84
	v_sub_f32_e32 v20, v20, v84
	v_sub_f32_e32 v21, v21, v84
	v_sub_f32_e32 v22, v22, v84
	v_sub_f32_e32 v23, v23, v84
	v_sub_f32_e32 v24, v24, v84
	v_sub_f32_e32 v25, v25, v84
	v_sub_f32_e32 v26, v26, v84
	v_sub_f32_e32 v27, v27, v84
	v_sub_f32_e32 v28, v28, v84
	v_sub_f32_e32 v29, v29, v84
	v_sub_f32_e32 v30, v30, v84
	v_sub_f32_e32 v31, v31, v84
	v_sub_f32_e32 v32, v32, v84
	v_sub_f32_e32 v33, v33, v84
	v_mul_f32_e32 v82, v82, v85
	v_xor_b32_e32 v130, 0x80000000, v81
	s_mov_b32 s11, 0x41000000
	v_mov_b32_e32 v131, v130
	v_mov_b32_e32 v132, v130
	v_mov_b32_e32 v133, v130
	v_mov_b32_e32 v134, v130
	v_mov_b32_e32 v135, v130
	v_mov_b32_e32 v136, v130
	v_mov_b32_e32 v137, v130
	v_mov_b32_e32 v138, v130
	v_mov_b32_e32 v139, v130
	v_mov_b32_e32 v140, v130
	v_mov_b32_e32 v141, v130
	v_mov_b32_e32 v142, v130
	v_mov_b32_e32 v143, v130
	v_mov_b32_e32 v144, v130
	v_mov_b32_e32 v145, v130
	s_branch .Lp1_back_e
.Lp1_rare_o:
	s_nop 1
	v_cndmask_b32_e32 v84, 0, v84, vcc
	v_exp_f32_e64 v85, -v84
	v_add_f32_e32 v81, v81, v84
	v_sub_f32_e32 v34, v34, v84
	v_sub_f32_e32 v35, v35, v84
	v_sub_f32_e32 v36, v36, v84
	v_sub_f32_e32 v37, v37, v84
	v_sub_f32_e32 v38, v38, v84
	v_sub_f32_e32 v39, v39, v84
	v_sub_f32_e32 v40, v40, v84
	v_sub_f32_e32 v41, v41, v84
	v_sub_f32_e32 v42, v42, v84
	v_sub_f32_e32 v43, v43, v84
	v_sub_f32_e32 v44, v44, v84
	v_sub_f32_e32 v45, v45, v84
	v_sub_f32_e32 v46, v46, v84
	v_sub_f32_e32 v47, v47, v84
	v_sub_f32_e32 v48, v48, v84
	v_sub_f32_e32 v49, v49, v84
	v_sub_f32_e32 v50, v50, v84
	v_sub_f32_e32 v51, v51, v84
	v_sub_f32_e32 v52, v52, v84
	v_sub_f32_e32 v53, v53, v84
	v_sub_f32_e32 v54, v54, v84
	v_sub_f32_e32 v55, v55, v84
	v_sub_f32_e32 v56, v56, v84
	v_sub_f32_e32 v57, v57, v84
	v_sub_f32_e32 v58, v58, v84
	v_sub_f32_e32 v59, v59, v84
	v_sub_f32_e32 v60, v60, v84
	v_sub_f32_e32 v61, v61, v84
	v_sub_f32_e32 v62, v62, v84
	v_sub_f32_e32 v63, v63, v84
	v_sub_f32_e32 v64, v64, v84
	v_sub_f32_e32 v65, v65, v84
	v_mul_f32_e32 v82, v82, v85
	v_xor_b32_e32 v130, 0x80000000, v81
	s_mov_b32 s11, 0x41000000
	v_mov_b32_e32 v131, v130
	v_mov_b32_e32 v132, v130
	v_mov_b32_e32 v133, v130
	v_mov_b32_e32 v134, v130
	v_mov_b32_e32 v135, v130
	v_mov_b32_e32 v136, v130
	v_mov_b32_e32 v137, v130
	v_mov_b32_e32 v138, v130
	v_mov_b32_e32 v139, v130
	v_mov_b32_e32 v140, v130
	v_mov_b32_e32 v141, v130
	v_mov_b32_e32 v142, v130
	v_mov_b32_e32 v143, v130
	v_mov_b32_e32 v144, v130
	v_mov_b32_e32 v145, v130
	s_branch .Lp1_back_o
.Lp1_fin:
	v_mov_b32_e32 v200, 0
	v_mov_b32_e32 v201, 0
	v_mov_b32_e32 v202, 0
	v_mov_b32_e32 v83, 0
	v_exp_f32_e32 v34, v34
	v_exp_f32_e32 v35, v35
	v_add_f32_e32 v200, v200, v34
	v_exp_f32_e32 v36, v36
	v_add_f32_e32 v201, v201, v35
	v_exp_f32_e32 v37, v37
	v_add_f32_e32 v202, v202, v36
	v_exp_f32_e32 v38, v38
	v_add_f32_e32 v83, v83, v37
	v_exp_f32_e32 v39, v39
	v_add_f32_e32 v200, v200, v38
	v_exp_f32_e32 v40, v40
	v_add_f32_e32 v201, v201, v39
	v_exp_f32_e32 v41, v41
	v_add_f32_e32 v202, v202, v40
	v_exp_f32_e32 v42, v42
	v_add_f32_e32 v83, v83, v41
	v_exp_f32_e32 v43, v43
	v_add_f32_e32 v200, v200, v42
	v_exp_f32_e32 v44, v44
	v_add_f32_e32 v201, v201, v43
	v_exp_f32_e32 v45, v45
	v_add_f32_e32 v202, v202, v44
	v_exp_f32_e32 v46, v46
	v_add_f32_e32 v83, v83, v45
	v_exp_f32_e32 v47, v47
	v_add_f32_e32 v200, v200, v46
	v_exp_f32_e32 v48, v48
	v_add_f32_e32 v201, v201, v47
	v_exp_f32_e32 v49, v49
	v_add_f32_e32 v202, v202, v48
	v_exp_f32_e32 v50, v50
	v_add_f32_e32 v83, v83, v49
	v_exp_f32_e32 v51, v51
	v_add_f32_e32 v200, v200, v50
	v_exp_f32_e32 v52, v52
	v_add_f32_e32 v201, v201, v51
	v_exp_f32_e32 v53, v53
	v_add_f32_e32 v202, v202, v52
	v_exp_f32_e32 v54, v54
	v_add_f32_e32 v83, v83, v53
	v_exp_f32_e32 v55, v55
	v_add_f32_e32 v200, v200, v54
	v_exp_f32_e32 v56, v56
	v_add_f32_e32 v201, v201, v55
	v_exp_f32_e32 v57, v57
	v_add_f32_e32 v202, v202, v56
	v_exp_f32_e32 v58, v58
	v_add_f32_e32 v83, v83, v57
	v_exp_f32_e32 v59, v59
	v_add_f32_e32 v200, v200, v58
	v_exp_f32_e32 v60, v60
	v_add_f32_e32 v201, v201, v59
	v_exp_f32_e32 v61, v61
	v_add_f32_e32 v202, v202, v60
	v_exp_f32_e32 v62, v62
	v_add_f32_e32 v83, v83, v61
	v_exp_f32_e32 v63, v63
	v_add_f32_e32 v200, v200, v62
	v_exp_f32_e32 v64, v64
	v_add_f32_e32 v201, v201, v63
	v_exp_f32_e32 v65, v65
	v_add_f32_e32 v202, v202, v64
	v_add_f32_e32 v83, v83, v65
	v_add_f32_e32 v200, v200, v201
	v_add_f32_e32 v202, v202, v83
	v_add_f32_e32 v200, v200, v202
	v_add_f32_e32 v82, v82, v200
	s_lshl_b64 s[0:1], s[20:21], 1
	s_add_u32 s0, s18, s0
	s_addc_u32 s1, s19, s1
	s_waitcnt vmcnt(0)
	s_barrier
	global_load_dwordx4 v[2:5], v[66:67], off
	global_load_dwordx4 v[6:9], v[68:69], off
	v_lshlrev_b32_e32 v10, 1, v79
	global_load_dwordx4 v[10:13], v10, s[0:1]
	v_lshlrev_b32_e32 v14, 1, v80
	global_load_dwordx4 v[14:17], v14, s[0:1]
	v_mbcnt_lo_u32_b32 v21, -1, 0
	v_mbcnt_hi_u32_b32 v21, -1, v21
	v_and_b32_e32 v23, 64, v21
	v_xor_b32_e32 v22, 32, v21
	v_add_u32_e32 v24, 64, v23
	v_cmp_lt_i32_e32 vcc, v22, v24
	v_cndmask_b32_e32 v21, v21, v22, vcc
	v_lshlrev_b32_e32 v21, 2, v21
	ds_bpermute_b32 v22, v21, v81
	v_mov_b32_e32 v18, v82
	ds_bpermute_b32 v19, v21, v18
	v_max_f32_e32 v21, v81, v81
	s_mov_b32 s15, 0
	s_waitcnt lgkmcnt(1)
	v_max_f32_e32 v20, v22, v22
	v_max_f32_e32 v20, v21, v20
	v_sub_f32_e32 v22, v22, v20
	v_sub_f32_e32 v21, v81, v20
	v_exp_f32_e32 v22, v22
	v_exp_f32_e32 v21, v21
	s_lshl_b64 s[18:19], s[14:15], 18
	v_mov_b32_e32 v131, 0
	s_waitcnt lgkmcnt(0)
	v_mul_f32_e32 v19, v22, v19
	v_fmac_f32_e32 v19, v18, v21
	v_div_scale_f32 v18, s[10:11], v19, v19, 1.0
	s_movk_i32 s10, 0x60
	s_nop 0
	v_mad_u32_u24 v188, v73, s10, v74
	v_mad_u32_u24 v189, v75, s10, v74
	s_waitcnt vmcnt(3)
	ds_write_b128 v77, v[2:5]
	s_waitcnt vmcnt(2)
	ds_write_b128 v78, v[6:9]
	v_lshlrev_b32_e32 v2, 1, v188
	s_waitcnt vmcnt(1)
	ds_write_b128 v2, v[10:13]
	v_lshlrev_b32_e32 v2, 1, v189
	s_mul_i32 s10, s14, 0x1200
	s_waitcnt vmcnt(0)
	ds_write_b128 v2, v[14:17]
	s_add_i32 s10, s10, 0xa800
	v_lshrrev_b32_e32 v2, 2, v0
	v_and_or_b32 v3, v2, 3, v1
	s_movk_i32 s11, 0x48
	v_mov_b32_e32 v5, s10
	v_add_u32_e32 v4, s10, v76
	v_mad_u32_u24 v5, v3, s11, v5
	s_lshl_b64 s[10:11], s[12:13], 24
	s_and_b32 s13, s2, 15
	s_lshl_b32 s13, s13, 20
	v_and_b32_e32 v0, 3, v0
	s_or_b32 s10, s10, s13
	v_and_or_b32 v0, v2, 4, v0
	s_add_u32 s10, s10, s18
	v_lshlrev_b32_e32 v0, 3, v0
	v_mul_u32_u24_e32 v2, 0xc0, v3
	v_lshlrev_b32_e32 v3, 13, v72
	s_addc_u32 s11, s11, s19
	v_or_b32_e32 v185, v2, v0
	v_or_b32_e32 v2, v3, v164
	s_add_u32 s10, s4, s10
	v_lshlrev_b32_e32 v130, 2, v2
	s_addc_u32 s11, s5, s11
	v_lshl_add_u64 v[2:3], s[10:11], 0, v[130:131]
	s_mov_b64 s[18:19], 0x80
	v_lshl_add_u64 v[132:133], v[2:3], 0, s[18:19]
	v_or_b32_e32 v2, 0x36000, v130
	v_mov_b32_e32 v3, v131
	v_lshl_add_u64 v[134:135], s[10:11], 0, v[2:3]
	v_or_b32_e32 v2, 0x2000, v130
	v_lshl_add_u64 v[2:3], s[10:11], 0, v[2:3]
	v_lshl_add_u64 v[136:137], v[2:3], 0, s[18:19]
	v_or_b32_e32 v2, 0x34000, v130
	v_mov_b32_e32 v3, v131
	v_rcp_f32_e32 v21, v18
	v_lshl_add_u64 v[138:139], s[10:11], 0, v[2:3]
	v_or_b32_e32 v2, 0x4000, v130
	v_lshl_add_u64 v[2:3], s[10:11], 0, v[2:3]
	v_lshl_add_u64 v[140:141], v[2:3], 0, s[18:19]
	v_or_b32_e32 v2, 0x32000, v130
	v_mov_b32_e32 v3, v131
	v_lshl_add_u64 v[142:143], s[10:11], 0, v[2:3]
	v_or_b32_e32 v2, 0x6000, v130
	v_fma_f32 v22, -v18, v21, 1.0
	v_lshl_add_u64 v[2:3], s[10:11], 0, v[2:3]
	v_fmac_f32_e32 v21, v22, v21
	v_div_scale_f32 v22, vcc, 1.0, v19, 1.0
	v_lshl_add_u64 v[144:145], v[2:3], 0, s[18:19]
	v_or_b32_e32 v2, 0x30000, v130
	v_mov_b32_e32 v3, v131
	v_mul_f32_e32 v24, v22, v21
	v_lshl_add_u64 v[146:147], s[10:11], 0, v[2:3]
	v_or_b32_e32 v2, 0x10000, v130
	v_fma_f32 v25, -v18, v24, v22
	v_lshl_add_u64 v[2:3], s[10:11], 0, v[2:3]
	v_fmac_f32_e32 v24, v25, v21
	v_lshl_add_u64 v[148:149], v[2:3], 0, s[18:19]
	v_or_b32_e32 v2, 0x26000, v130
	v_mov_b32_e32 v3, v131
	v_fma_f32 v18, -v18, v24, v22
	v_lshl_add_u64 v[150:151], s[10:11], 0, v[2:3]
	v_or_b32_e32 v2, 0x12000, v130
	v_div_fmas_f32 v18, v18, v21, v24
	v_lshlrev_b32_e32 v184, 2, v72
	v_lshl_add_u64 v[2:3], s[10:11], 0, v[2:3]
	v_div_fixup_f32 v18, v18, v19, 1.0
	v_or_b32_e32 v19, v184, v23
	v_lshl_add_u64 v[152:153], v[2:3], 0, s[18:19]
	v_or_b32_e32 v2, 0x24000, v130
	v_mov_b32_e32 v3, v131
	v_lshlrev_b32_e32 v19, 2, v19
	v_lshl_add_u64 v[154:155], s[10:11], 0, v[2:3]
	v_or_b32_e32 v2, 0x14000, v130
	ds_bpermute_b32 v33, v19, v20 offset:36
	ds_bpermute_b32 v32, v19, v20 offset:40
	ds_bpermute_b32 v35, v19, v20 offset:44
	ds_bpermute_b32 v34, v19, v20 offset:64
	ds_bpermute_b32 v37, v19, v20 offset:68
	ds_bpermute_b32 v36, v19, v20 offset:72
	ds_bpermute_b32 v39, v19, v20 offset:76
	ds_bpermute_b32 v38, v19, v20 offset:96
	ds_bpermute_b32 v41, v19, v20 offset:100
	ds_bpermute_b32 v40, v19, v20 offset:104
	ds_bpermute_b32 v43, v19, v20 offset:108
	v_lshl_add_u64 v[2:3], s[10:11], 0, v[2:3]
	ds_bpermute_b32 v46, v19, v20 offset:32
	ds_bpermute_b32 v47, v19, v20 offset:12
	ds_bpermute_b32 v42, v19, v20 offset:8
	ds_bpermute_b32 v45, v19, v20 offset:4
	ds_bpermute_b32 v44, v19, v20
	ds_bpermute_b32 v183, v19, v18
	ds_bpermute_b32 v182, v19, v18 offset:4
	ds_bpermute_b32 v181, v19, v18 offset:8
	ds_bpermute_b32 v180, v19, v18 offset:12
	ds_bpermute_b32 v179, v19, v18 offset:32
	ds_bpermute_b32 v178, v19, v18 offset:36
	ds_bpermute_b32 v177, v19, v18 offset:40
	ds_bpermute_b32 v176, v19, v18 offset:44
	ds_bpermute_b32 v175, v19, v18 offset:64
	ds_bpermute_b32 v174, v19, v18 offset:68
	ds_bpermute_b32 v173, v19, v18 offset:72
	ds_bpermute_b32 v172, v19, v18 offset:76
	ds_bpermute_b32 v171, v19, v18 offset:96
	ds_bpermute_b32 v170, v19, v18 offset:100
	ds_bpermute_b32 v169, v19, v18 offset:104
	ds_bpermute_b32 v168, v19, v18 offset:108
	v_lshl_add_u64 v[156:157], v[2:3], 0, s[18:19]
	v_or_b32_e32 v2, 0x22000, v130
	v_mov_b32_e32 v3, v131
	v_lshl_add_u64 v[158:159], s[10:11], 0, v[2:3]
	v_or_b32_e32 v2, 0x16000, v130
	v_lshl_add_u64 v[2:3], s[10:11], 0, v[2:3]
	v_lshl_add_u64 v[160:161], v[2:3], 0, s[18:19]
	v_or_b32_e32 v2, 0x20000, v130
	v_mov_b32_e32 v3, v131
	v_add_u32_e32 v187, v4, v1
	v_lshl_add_u64 v[162:163], s[10:11], 0, v[2:3]
	s_mov_b64 s[10:11], 0
	s_movk_i32 s13, 0x3000
	s_waitcnt lgkmcnt(14)
	v_xor_b32_e32 v63, 0x80000000, v43
	v_xor_b32_e32 v62, 0x80000000, v40
	v_xor_b32_e32 v61, 0x80000000, v41
	v_xor_b32_e32 v60, 0x80000000, v38
	v_xor_b32_e32 v59, 0x80000000, v39
	v_xor_b32_e32 v58, 0x80000000, v36
	v_xor_b32_e32 v57, 0x80000000, v37
	v_xor_b32_e32 v56, 0x80000000, v34
	v_xor_b32_e32 v55, 0x80000000, v35
	v_xor_b32_e32 v54, 0x80000000, v32
	v_xor_b32_e32 v53, 0x80000000, v33
	v_add_u32_e32 v186, v5, v0
	v_xor_b32_e32 v52, 0x80000000, v46
	v_xor_b32_e32 v51, 0x80000000, v47
	v_xor_b32_e32 v50, 0x80000000, v42
	v_xor_b32_e32 v49, 0x80000000, v45
	v_xor_b32_e32 v48, 0x80000000, v44
	v_mov_b32_e32 v0, v131
	v_mov_b32_e32 v1, v131
	v_mov_b32_e32 v2, v131
	v_mov_b32_e32 v4, v131
	v_mov_b32_e32 v5, v131
	v_mov_b32_e32 v6, v131
	v_mov_b32_e32 v7, v131
	v_mov_b32_e32 v8, v131
	v_mov_b32_e32 v9, v131
	v_mov_b32_e32 v10, v131
	v_mov_b32_e32 v11, v131
	v_mov_b32_e32 v12, v131
	v_mov_b32_e32 v13, v131
	v_mov_b32_e32 v14, v131
	v_mov_b32_e32 v15, v131
	v_mov_b32_e32 v16, v131
	v_mov_b32_e32 v17, v131
	v_mov_b32_e32 v18, v131
	v_mov_b32_e32 v19, v131
	v_mov_b32_e32 v20, v131
	v_mov_b32_e32 v21, v131
	v_mov_b32_e32 v22, v131
	v_mov_b32_e32 v23, v131
	v_mov_b32_e32 v24, v131
	v_mov_b32_e32 v25, v131
	v_mov_b32_e32 v26, v131
	v_mov_b32_e32 v27, v131
	v_mov_b32_e32 v28, v131
	v_mov_b32_e32 v29, v131
	v_mov_b32_e32 v30, v131
	v_mov_b32_e32 v31, v131
	v_add_u32_e32 v131, 0x800, v187
	s_waitcnt lgkmcnt(0)
	s_barrier
.LBB4_11:
	v_lshl_add_u64 v[66:67], s[8:9], 0, v[128:129]
	v_add_co_u32_e32 v66, vcc, s13, v66
	v_lshl_add_u64 v[64:65], s[0:1], 0, v[128:129]
	s_nop 0
	v_addc_co_u32_e32 v67, vcc, 0, v67, vcc
	v_add_co_u32_e32 v64, vcc, s13, v64
	s_and_b32 s14, s15, 1
	s_nop 0
	v_addc_co_u32_e32 v65, vcc, 0, v65, vcc
	global_load_dwordx4 v[112:115], v[66:67], off offset:-4096
	global_load_dwordx4 v[116:119], v[66:67], off
	global_load_dwordx4 v[120:123], v[64:65], off offset:-4096
	global_load_dwordx4 v[124:127], v[64:65], off
	s_add_i32 s15, s15, 1
	s_mul_i32 s18, s14, 0x2400
	v_add_u32_e32 v202, s18, v167
	ds_read_b128 v[80:83], v202
	ds_read_b128 v[190:193], v202 offset:32
	ds_read_b128 v[194:197], v202 offset:4608
	ds_read_b128 v[198:201], v202 offset:4640
	s_waitcnt lgkmcnt(3)
	v_mfma_f32_32x32x16_f16 v[64:79], v[108:111], v[80:83], v[48:63]
	s_waitcnt lgkmcnt(1)
	v_mfma_f32_32x32x16_f16 v[80:95], v[108:111], v[194:197], v[48:63]
	v_mfma_f32_32x32x16_f16 v[64:79], v[104:107], v[190:193], v[64:79]
	ds_read_b128 v[190:193], v202 offset:64
	ds_read_b128 v[194:197], v202 offset:96
	s_waitcnt lgkmcnt(2)
	v_mfma_f32_32x32x16_f16 v[80:95], v[104:107], v[198:201], v[80:95]
	s_waitcnt lgkmcnt(1)
	v_mfma_f32_32x32x16_f16 v[64:79], v[100:103], v[190:193], v[64:79]
	ds_read_b128 v[190:193], v202 offset:4672
	ds_read_b128 v[198:201], v202 offset:4704
	s_waitcnt lgkmcnt(1)
	v_mfma_f32_32x32x16_f16 v[80:95], v[100:103], v[190:193], v[80:95]
	v_mfma_f32_32x32x16_f16 v[64:79], v[96:99], v[194:197], v[64:79]
	s_waitcnt lgkmcnt(0)
	v_mfma_f32_32x32x16_f16 v[80:95], v[96:99], v[198:201], v[80:95]
	s_setprio 2
	s_nop 8
	v_exp_f32_e32 v192, v64
	s_nop 0
	v_exp_f32_e32 v80, v80
	v_exp_f32_e32 v193, v65
	v_exp_f32_e32 v81, v81
	v_lshl_add_u64 v[190:191], v[132:133], 0, s[10:11]
	v_mul_f32_e32 v64, v192, v183
	v_exp_f32_e32 v66, v66
	global_store_dword v[190:191], v64, off offset:-128
	v_mul_f32_e32 v64, v80, v183
	v_exp_f32_e32 v82, v82
	global_store_dword v[190:191], v64, off
	v_mul_f32_e32 v190, v193, v182
	v_lshl_add_u64 v[64:65], v[136:137], 0, s[10:11]
	v_exp_f32_e32 v67, v67
	global_store_dword v[64:65], v190, off offset:-128
	v_mul_f32_e32 v190, v81, v182
	v_exp_f32_e32 v83, v83
	global_store_dword v[64:65], v190, off
	v_mul_f32_e32 v190, v66, v181
	v_lshl_add_u64 v[64:65], v[140:141], 0, s[10:11]
	global_store_dword v[64:65], v190, off offset:-128
	v_mul_f32_e32 v190, v82, v181
	global_store_dword v[64:65], v190, off
	v_mul_f32_e32 v190, v67, v180
	v_lshl_add_u64 v[64:65], v[144:145], 0, s[10:11]
	global_store_dword v[64:65], v190, off offset:-128
	v_mul_f32_e32 v190, v83, v180
	global_store_dword v[64:65], v190, off
	v_exp_f32_e32 v190, v68
	v_cvt_pk_f16_f32 v65, v66, v67
	v_cvt_pk_f16_f32 v67, v82, v83
	v_exp_f32_e32 v82, v84
	v_cvt_pk_f16_f32 v66, v80, v81
	v_mul_f32_e32 v68, v190, v179
	v_lshl_add_u64 v[80:81], v[148:149], 0, s[10:11]
	global_store_dword v[80:81], v68, off offset:-128
	v_exp_f32_e32 v83, v69
	v_mul_f32_e32 v68, v82, v179
	global_store_dword v[80:81], v68, off
	v_exp_f32_e32 v80, v85
	v_mul_f32_e32 v81, v83, v178
	v_lshl_add_u64 v[68:69], v[152:153], 0, s[10:11]
	global_store_dword v[68:69], v81, off offset:-128
	v_exp_f32_e32 v70, v70
	v_mul_f32_e32 v81, v80, v178
	global_store_dword v[68:69], v81, off
	v_exp_f32_e32 v81, v86
	v_mul_f32_e32 v84, v70, v177
	v_lshl_add_u64 v[68:69], v[156:157], 0, s[10:11]
	global_store_dword v[68:69], v84, off offset:-128
	v_exp_f32_e32 v71, v71
	v_mul_f32_e32 v84, v81, v177
	global_store_dword v[68:69], v84, off
	v_exp_f32_e32 v84, v87
	v_mul_f32_e32 v85, v71, v176
	v_lshl_add_u64 v[68:69], v[160:161], 0, s[10:11]
	global_store_dword v[68:69], v85, off offset:-128
	v_mul_f32_e32 v85, v84, v176
	v_cvt_pk_f16_f32 v64, v192, v193
	global_store_dword v[68:69], v85, off
	v_cvt_pk_f16_f32 v69, v70, v71
	v_cvt_pk_f16_f32 v68, v190, v83
	v_exp_f32_e32 v72, v72
	v_cvt_pk_f16_f32 v71, v81, v84
	v_cvt_pk_f16_f32 v70, v82, v80
	ds_write2_b64 v187, v[64:65], v[68:69] offset1:2
	ds_write2_b64 v131, v[66:67], v[70:71] offset0:32 offset1:34
	v_exp_f32_e32 v66, v88
	v_mul_f32_e32 v67, v72, v175
	v_lshl_add_u64 v[64:65], v[162:163], 0, s[10:11]
	global_store_dword v[64:65], v67, off
	v_exp_f32_e32 v67, v73
	v_mul_f32_e32 v68, v66, v175
	global_store_dword v[64:65], v68, off offset:128
	v_exp_f32_e32 v68, v89
	v_mul_f32_e32 v69, v67, v174
	v_lshl_add_u64 v[64:65], v[158:159], 0, s[10:11]
	global_store_dword v[64:65], v69, off
	v_exp_f32_e32 v69, v74
	v_mul_f32_e32 v70, v68, v174
	global_store_dword v[64:65], v70, off offset:128
	v_exp_f32_e32 v70, v90
	v_mul_f32_e32 v71, v69, v173
	v_lshl_add_u64 v[64:65], v[154:155], 0, s[10:11]
	global_store_dword v[64:65], v71, off
	v_exp_f32_e32 v71, v75
	v_mul_f32_e32 v73, v70, v173
	global_store_dword v[64:65], v73, off offset:128
	v_exp_f32_e32 v73, v91
	v_mul_f32_e32 v74, v71, v172
	v_lshl_add_u64 v[64:65], v[150:151], 0, s[10:11]
	global_store_dword v[64:65], v74, off
	v_mul_f32_e32 v74, v73, v172
	global_store_dword v[64:65], v74, off offset:128
	v_cvt_pk_f16_f32 v65, v69, v71
	v_exp_f32_e32 v71, v76
	v_cvt_pk_f16_f32 v64, v72, v67
	v_cvt_pk_f16_f32 v67, v70, v73
	v_exp_f32_e32 v70, v92
	v_cvt_pk_f16_f32 v66, v66, v68
	v_mul_f32_e32 v72, v71, v171
	v_lshl_add_u64 v[68:69], v[146:147], 0, s[10:11]
	global_store_dword v[68:69], v72, off
	v_exp_f32_e32 v72, v77
	v_mul_f32_e32 v73, v70, v171
	global_store_dword v[68:69], v73, off offset:128
	v_exp_f32_e32 v73, v93
	v_mul_f32_e32 v74, v72, v170
	v_lshl_add_u64 v[68:69], v[142:143], 0, s[10:11]
	global_store_dword v[68:69], v74, off
	v_exp_f32_e32 v74, v78
	v_mul_f32_e32 v75, v73, v170
	global_store_dword v[68:69], v75, off offset:128
	v_exp_f32_e32 v75, v94
	v_mul_f32_e32 v76, v74, v169
	v_lshl_add_u64 v[68:69], v[138:139], 0, s[10:11]
	global_store_dword v[68:69], v76, off
	v_exp_f32_e32 v76, v79
	v_mul_f32_e32 v77, v75, v169
	global_store_dword v[68:69], v77, off offset:128
	v_exp_f32_e32 v77, v95
	v_mul_f32_e32 v78, v76, v168
	v_lshl_add_u64 v[68:69], v[134:135], 0, s[10:11]
	global_store_dword v[68:69], v78, off
	v_mul_f32_e32 v78, v77, v168
	global_store_dword v[68:69], v78, off offset:128
	v_cvt_pk_f16_f32 v69, v74, v76
	v_cvt_pk_f16_f32 v68, v71, v72
	v_cvt_pk_f16_f32 v71, v75, v77
	v_cvt_pk_f16_f32 v70, v70, v73
	ds_write2_b64 v187, v[64:65], v[68:69] offset0:4 offset1:6
	ds_write2_b64 v131, v[66:67], v[70:71] offset0:36 offset1:38
	s_setprio 0
	ds_read_b64_tr_b16 v[64:65], v186
	ds_read_b64_tr_b16 v[66:67], v186 offset:288
	s_mul_i32 s18, s14, 0x3000
	v_or_b32_e32 v80, s18, v185
	ds_read_b64_tr_b16 v[68:69], v80
	ds_read_b64_tr_b16 v[70:71], v80 offset:768
	ds_read_b64_tr_b16 v[74:75], v80 offset:832
	ds_read_b64_tr_b16 v[72:73], v80 offset:64
	ds_read_b64_tr_b16 v[76:77], v186 offset:1152
	ds_read_b64_tr_b16 v[78:79], v186 offset:1440
	s_waitcnt lgkmcnt(4)
	v_mfma_f32_32x32x16_f16 v[0:15], v[64:67], v[68:71], v[0:15]
	s_waitcnt lgkmcnt(2)
	v_mfma_f32_32x32x16_f16 v[16:31], v[64:67], v[72:75], v[16:31]
	ds_read_b64_tr_b16 v[64:65], v80 offset:3072
	ds_read_b64_tr_b16 v[66:67], v80 offset:3840
	ds_read_b64_tr_b16 v[70:71], v80 offset:3904
	ds_read_b64_tr_b16 v[68:69], v80 offset:3136
	s_waitcnt lgkmcnt(2)
	v_mfma_f32_32x32x16_f16 v[0:15], v[76:79], v[64:67], v[0:15]
	s_waitcnt lgkmcnt(0)
	v_mfma_f32_32x32x16_f16 v[16:31], v[76:79], v[68:71], v[16:31]
	ds_read_b64_tr_b16 v[64:65], v186 offset:2304
	ds_read_b64_tr_b16 v[66:67], v186 offset:2592
	ds_read_b64_tr_b16 v[68:69], v80 offset:6144
	ds_read_b64_tr_b16 v[70:71], v80 offset:6912
	ds_read_b64_tr_b16 v[74:75], v80 offset:6976
	ds_read_b64_tr_b16 v[72:73], v80 offset:6208
	ds_read_b64_tr_b16 v[76:77], v186 offset:3456
	ds_read_b64_tr_b16 v[78:79], v186 offset:3744
	s_waitcnt lgkmcnt(4)
	v_mfma_f32_32x32x16_f16 v[0:15], v[64:67], v[68:71], v[0:15]
	s_waitcnt lgkmcnt(2)
	v_mfma_f32_32x32x16_f16 v[16:31], v[64:67], v[72:75], v[16:31]
	ds_read_b64_tr_b16 v[64:65], v80 offset:9216
	ds_read_b64_tr_b16 v[66:67], v80 offset:9984
	ds_read_b64_tr_b16 v[70:71], v80 offset:10048
	ds_read_b64_tr_b16 v[68:69], v80 offset:9280
	s_waitcnt lgkmcnt(2)
	v_mfma_f32_32x32x16_f16 v[0:15], v[76:79], v[64:67], v[0:15]
	s_waitcnt lgkmcnt(0)
	v_mfma_f32_32x32x16_f16 v[16:31], v[76:79], v[68:71], v[16:31]
	s_xor_b32 s14, s14, 1
	s_mul_i32 s18, s14, 0x3000
	s_mulk_i32 s14, 0x2400
	s_addk_i32 s14, 0x6000
	s_add_u32 s10, s10, 0x100
	s_addc_u32 s11, s11, 0
	s_add_u32 s8, s8, 0x2000
	s_addc_u32 s9, s9, 0
	s_add_u32 s0, s0, 0x2000
	s_addc_u32 s1, s1, 0
	v_lshl_add_u32 v67, v166, 1, s14
	s_cmpk_eq_i32 s10, 0x1f00
	v_lshl_add_u32 v64, v189, 1, s18
	v_lshl_add_u32 v65, v188, 1, s18
	v_lshl_add_u32 v66, v165, 1, s14
	s_waitcnt vmcnt(35)
	ds_write_b128 v67, v[112:115]
	s_waitcnt vmcnt(34)
	ds_write_b128 v66, v[116:119]
	s_waitcnt vmcnt(33)
	ds_write_b128 v65, v[120:123]
	s_waitcnt vmcnt(32)
	ds_write_b128 v64, v[124:127]
	s_waitcnt lgkmcnt(0)
	s_barrier
	s_cbranch_scc0 .LBB4_11
	s_lshl_b64 s[0:1], s[16:17], 13
	s_add_u32 s0, s4, s0
	s_addc_u32 s1, s5, s1
	v_xor_b32_e32 v52, 0x80000000, v34
	v_xor_b32_e32 v51, 0x80000000, v35
	v_xor_b32_e32 v50, 0x80000000, v32
	v_xor_b32_e32 v49, 0x80000000, v33
	ds_read_b128 v[32:35], v167 offset:9216
	v_xor_b32_e32 v59, 0x80000000, v43
	v_xor_b32_e32 v58, 0x80000000, v40
	v_xor_b32_e32 v57, 0x80000000, v41
	v_xor_b32_e32 v56, 0x80000000, v38
	v_xor_b32_e32 v55, 0x80000000, v39
	v_xor_b32_e32 v54, 0x80000000, v36
	v_xor_b32_e32 v53, 0x80000000, v37
	v_xor_b32_e32 v48, 0x80000000, v46
	v_xor_b32_e32 v47, 0x80000000, v47
	v_xor_b32_e32 v46, 0x80000000, v42
	v_xor_b32_e32 v45, 0x80000000, v45
	v_xor_b32_e32 v44, 0x80000000, v44
	ds_read_b128 v[36:39], v167 offset:9248
	s_add_u32 s0, s0, 0x1f00
	s_waitcnt lgkmcnt(1)
	v_mfma_f32_32x32x16_f16 v[60:75], v[108:111], v[32:35], v[44:59]
	ds_read_b128 v[32:35], v167 offset:13824
	ds_read_b128 v[40:43], v167 offset:13856
	s_addc_u32 s1, s1, 0
	s_waitcnt lgkmcnt(1)
	v_mfma_f32_32x32x16_f16 v[44:59], v[108:111], v[32:35], v[44:59]
	v_mfma_f32_32x32x16_f16 v[60:75], v[104:107], v[36:39], v[60:75]
	ds_read_b128 v[32:35], v167 offset:9280
	ds_read_b128 v[36:39], v167 offset:9312
	s_waitcnt lgkmcnt(2)
	v_mfma_f32_32x32x16_f16 v[44:59], v[104:107], v[40:43], v[44:59]
	s_waitcnt lgkmcnt(1)
	v_mfma_f32_32x32x16_f16 v[60:75], v[100:103], v[32:35], v[60:75]
	ds_read_b128 v[32:35], v167 offset:13888
	ds_read_b128 v[40:43], v167 offset:13920
	s_waitcnt lgkmcnt(1)
	v_mfma_f32_32x32x16_f16 v[44:59], v[100:103], v[32:35], v[44:59]
	v_mfma_f32_32x32x16_f16 v[60:75], v[96:99], v[36:39], v[60:75]
	s_waitcnt lgkmcnt(0)
	v_mfma_f32_32x32x16_f16 v[44:59], v[96:99], v[40:43], v[44:59]
	s_setprio 2
	s_nop 8
	v_exp_f32_e32 v32, v60
	s_nop 0
	v_exp_f32_e32 v34, v44
	v_exp_f32_e32 v35, v61
	v_or_b32_e32 v37, 0x2000, v130
	v_mul_f32_e32 v33, v32, v183
	v_mul_f32_e32 v36, v34, v183
	global_store_dword v130, v33, s[0:1]
	global_store_dword v130, v36, s[0:1] offset:128
	v_exp_f32_e32 v36, v45
	v_mul_f32_e32 v33, v35, v182
	global_store_dword v37, v33, s[0:1]
	v_exp_f32_e32 v33, v62
	v_mul_f32_e32 v38, v36, v182
	global_store_dword v37, v38, s[0:1] offset:128
	v_exp_f32_e32 v37, v46
	v_mul_f32_e32 v38, v33, v181
	v_or_b32_e32 v39, 0x4000, v130
	global_store_dword v39, v38, s[0:1]
	v_exp_f32_e32 v38, v63
	v_mul_f32_e32 v40, v37, v181
	global_store_dword v39, v40, s[0:1] offset:128
	v_exp_f32_e32 v39, v47
	v_mul_f32_e32 v40, v38, v180
	v_cvt_pk_f16_f32 v33, v33, v38
	v_exp_f32_e32 v38, v64
	v_or_b32_e32 v41, 0x6000, v130
	global_store_dword v41, v40, s[0:1]
	v_mul_f32_e32 v40, v39, v180
	global_store_dword v41, v40, s[0:1] offset:128
	v_cvt_pk_f16_f32 v32, v32, v35
	v_cvt_pk_f16_f32 v35, v37, v39
	v_cvt_pk_f16_f32 v34, v34, v36
	v_exp_f32_e32 v40, v48
	v_mul_f32_e32 v36, v38, v179
	v_or_b32_e32 v37, 0x10000, v130
	global_store_dword v37, v36, s[0:1]
	v_exp_f32_e32 v36, v65
	v_exp_f32_e32 v41, v49
	v_mul_f32_e32 v39, v40, v179
	global_store_dword v37, v39, s[0:1] offset:128
	v_mul_f32_e32 v37, v36, v178
	v_or_b32_e32 v39, 0x12000, v130
	global_store_dword v39, v37, s[0:1]
	v_exp_f32_e32 v37, v66
	v_mul_f32_e32 v42, v41, v178
	global_store_dword v39, v42, s[0:1] offset:128
	v_exp_f32_e32 v39, v50
	v_mul_f32_e32 v42, v37, v177
	v_or_b32_e32 v43, 0x14000, v130
	global_store_dword v43, v42, s[0:1]
	v_exp_f32_e32 v42, v67
	v_mul_f32_e32 v44, v39, v177
	global_store_dword v43, v44, s[0:1] offset:128
	v_exp_f32_e32 v43, v51
	v_cvt_pk_f16_f32 v37, v37, v42
	v_cvt_pk_f16_f32 v36, v38, v36
	v_cvt_pk_f16_f32 v38, v40, v41
	v_cvt_pk_f16_f32 v39, v39, v43
	ds_write2_b64 v187, v[32:33], v[36:37] offset1:2
	v_exp_f32_e32 v32, v68
	v_add_u32_e32 v40, 0x800, v187
	ds_write2_b64 v40, v[34:35], v[38:39] offset0:32 offset1:34
	v_exp_f32_e32 v34, v52
	v_exp_f32_e32 v36, v69
	v_exp_f32_e32 v37, v53
	v_mul_f32_e32 v33, v32, v175
	v_or_b32_e32 v35, 0x20000, v130
	global_store_dword v35, v33, s[0:1]
	v_mul_f32_e32 v33, v34, v175
	global_store_dword v35, v33, s[0:1] offset:128
	v_mul_f32_e32 v33, v36, v174
	v_or_b32_e32 v35, 0x22000, v130
	global_store_dword v35, v33, s[0:1]
	v_exp_f32_e32 v33, v70
	v_mul_f32_e32 v38, v37, v174
	global_store_dword v35, v38, s[0:1] offset:128
	v_exp_f32_e32 v35, v54
	v_mul_f32_e32 v38, v33, v173
	v_or_b32_e32 v39, 0x24000, v130
	global_store_dword v39, v38, s[0:1]
	v_exp_f32_e32 v38, v71
	v_mul_f32_e32 v41, v35, v173
	global_store_dword v39, v41, s[0:1] offset:128
	v_exp_f32_e32 v39, v55
	v_mul_f32_e32 v44, v42, v176
	v_mul_f32_e32 v41, v38, v172
	v_or_b32_e32 v42, 0x26000, v130
	v_cvt_pk_f16_f32 v32, v32, v36
	v_exp_f32_e32 v36, v72
	global_store_dword v42, v41, s[0:1]
	v_mul_f32_e32 v41, v39, v172
	v_cvt_pk_f16_f32 v33, v33, v38
	v_exp_f32_e32 v38, v56
	global_store_dword v42, v41, s[0:1] offset:128
	v_exp_f32_e32 v41, v73
	v_exp_f32_e32 v42, v57
	v_cvt_pk_f16_f32 v35, v35, v39
	v_cvt_pk_f16_f32 v34, v34, v37
	v_mul_f32_e32 v37, v36, v171
	v_or_b32_e32 v39, 0x30000, v130
	global_store_dword v39, v37, s[0:1]
	v_mul_f32_e32 v37, v38, v171
	v_or_b32_e32 v45, 0x16000, v130
	global_store_dword v39, v37, s[0:1] offset:128
	v_mul_f32_e32 v37, v41, v170
	v_or_b32_e32 v39, 0x32000, v130
	global_store_dword v45, v44, s[0:1]
	v_mul_f32_e32 v44, v43, v176
	global_store_dword v39, v37, s[0:1]
	v_exp_f32_e32 v37, v74
	v_mul_f32_e32 v43, v42, v170
	global_store_dword v39, v43, s[0:1] offset:128
	v_exp_f32_e32 v39, v58
	global_store_dword v45, v44, s[0:1] offset:128
	v_mul_f32_e32 v43, v37, v169
	v_or_b32_e32 v44, 0x34000, v130
	global_store_dword v44, v43, s[0:1]
	v_exp_f32_e32 v43, v75
	v_mul_f32_e32 v45, v39, v169
	global_store_dword v44, v45, s[0:1] offset:128
	v_exp_f32_e32 v44, v59
	v_mul_f32_e32 v45, v43, v168
	v_or_b32_e32 v46, 0x36000, v130
	global_store_dword v46, v45, s[0:1]
	v_mul_f32_e32 v45, v44, v168
	v_cvt_pk_f16_f32 v37, v37, v43
	v_cvt_pk_f16_f32 v36, v36, v41
	global_store_dword v46, v45, s[0:1] offset:128
	v_cvt_pk_f16_f32 v39, v39, v44
	v_cvt_pk_f16_f32 v38, v38, v42
	ds_write2_b64 v187, v[32:33], v[36:37] offset0:4 offset1:6
	ds_write2_b64 v40, v[34:35], v[38:39] offset0:36 offset1:38
	s_setprio 0
	ds_read_b64_tr_b16 v[32:33], v186
	ds_read_b64_tr_b16 v[34:35], v186 offset:288
	ds_read_b64_tr_b16 v[36:37], v185 offset:12288
	ds_read_b64_tr_b16 v[38:39], v185 offset:13056
	ds_read_b64_tr_b16 v[42:43], v185 offset:13120
	ds_read_b64_tr_b16 v[40:41], v185 offset:12352
	ds_read_b64_tr_b16 v[44:45], v186 offset:1152
	ds_read_b64_tr_b16 v[46:47], v186 offset:1440
	s_waitcnt lgkmcnt(4)
	v_mfma_f32_32x32x16_f16 v[0:15], v[32:35], v[36:39], v[0:15]
	s_waitcnt lgkmcnt(2)
	v_mfma_f32_32x32x16_f16 v[16:31], v[32:35], v[40:43], v[16:31]
	ds_read_b64_tr_b16 v[32:33], v185 offset:15360
	ds_read_b64_tr_b16 v[34:35], v185 offset:16128
	ds_read_b64_tr_b16 v[38:39], v185 offset:16192
	ds_read_b64_tr_b16 v[36:37], v185 offset:15424
	s_waitcnt lgkmcnt(2)
	v_mfma_f32_32x32x16_f16 v[0:15], v[44:47], v[32:35], v[0:15]
	s_waitcnt lgkmcnt(0)
	v_mfma_f32_32x32x16_f16 v[16:31], v[44:47], v[36:39], v[16:31]
	ds_read_b64_tr_b16 v[32:33], v186 offset:2304
	ds_read_b64_tr_b16 v[34:35], v186 offset:2592
	ds_read_b64_tr_b16 v[36:37], v185 offset:18432
	ds_read_b64_tr_b16 v[38:39], v185 offset:19200
	ds_read_b64_tr_b16 v[42:43], v185 offset:19264
	ds_read_b64_tr_b16 v[40:41], v185 offset:18496
	ds_read_b64_tr_b16 v[44:45], v186 offset:3456
	ds_read_b64_tr_b16 v[46:47], v186 offset:3744
	s_waitcnt lgkmcnt(4)
	v_mfma_f32_32x32x16_f16 v[0:15], v[32:35], v[36:39], v[0:15]
	s_waitcnt lgkmcnt(2)
	v_mfma_f32_32x32x16_f16 v[16:31], v[32:35], v[40:43], v[16:31]
	ds_read_b64_tr_b16 v[32:33], v185 offset:21504
	ds_read_b64_tr_b16 v[34:35], v185 offset:22272
	ds_read_b64_tr_b16 v[38:39], v185 offset:22336
	ds_read_b64_tr_b16 v[36:37], v185 offset:21568
	s_waitcnt lgkmcnt(2)
	v_mfma_f32_32x32x16_f16 v[0:15], v[44:47], v[32:35], v[0:15]
	s_waitcnt lgkmcnt(0)
	v_mfma_f32_32x32x16_f16 v[16:31], v[44:47], v[36:39], v[16:31]
	s_lshl_b32 s0, s2, 3
	s_and_b32 s0, s0, 0x7ffff800
	s_add_i32 s3, s3, s0
	s_lshl_b32 s0, s12, 7
	s_and_b32 s0, s0, 0x780
	s_add_u32 s0, s6, s0
	v_mov_b32_e32 v35, 0
	v_or_b32_e32 v32, s3, v184
	s_addc_u32 s1, s7, 0
	v_lshlrev_b32_e32 v34, 1, v164
	v_mov_b32_e32 v33, v35
	v_lshl_add_u64 v[36:37], s[0:1], 0, v[34:35]
	v_lshlrev_b64 v[38:39], 11, v[32:33]
	v_fma_mixlo_f16 v0, v0, v183, 0
	v_lshl_add_u64 v[38:39], v[36:37], 0, v[38:39]
	s_waitcnt vmcnt(63) expcnt(7) lgkmcnt(15)
	s_barrier
	global_store_short v[38:39], v0, off
	v_fma_mixlo_f16 v0, v16, v183, 0
	v_or_b32_e32 v34, 1, v32
	global_store_short v[38:39], v0, off offset:64
	v_lshlrev_b64 v[38:39], 11, v[34:35]
	v_fma_mixlo_f16 v16, v1, v182, 0
	v_lshl_add_u64 v[0:1], v[36:37], 0, v[38:39]
	global_store_short v[0:1], v16, off
	v_fma_mixlo_f16 v16, v17, v182, 0
	v_or_b32_e32 v34, 2, v32
	global_store_short v[0:1], v16, off offset:64
	v_lshlrev_b64 v[0:1], 11, v[34:35]
	v_fma_mixlo_f16 v2, v2, v181, 0
	v_lshl_add_u64 v[0:1], v[36:37], 0, v[0:1]
	global_store_short v[0:1], v2, off
	v_fma_mixlo_f16 v2, v18, v181, 0
	v_or_b32_e32 v34, 3, v32
	global_store_short v[0:1], v2, off offset:64
	v_lshlrev_b64 v[0:1], 11, v[34:35]
	v_fma_mixlo_f16 v2, v3, v180, 0
	v_lshl_add_u64 v[0:1], v[36:37], 0, v[0:1]
	global_store_short v[0:1], v2, off
	v_fma_mixlo_f16 v2, v19, v180, 0
	v_or_b32_e32 v34, 8, v32
	global_store_short v[0:1], v2, off offset:64
	v_lshlrev_b64 v[0:1], 11, v[34:35]
	v_fma_mixlo_f16 v2, v4, v179, 0
	v_lshl_add_u64 v[0:1], v[36:37], 0, v[0:1]
	global_store_short v[0:1], v2, off
	v_fma_mixlo_f16 v2, v20, v179, 0
	v_or_b32_e32 v34, 9, v32
	global_store_short v[0:1], v2, off offset:64
	v_lshlrev_b64 v[0:1], 11, v[34:35]
	v_fma_mixlo_f16 v2, v5, v178, 0
	v_lshl_add_u64 v[0:1], v[36:37], 0, v[0:1]
	global_store_short v[0:1], v2, off
	v_fma_mixlo_f16 v2, v21, v178, 0
	v_or_b32_e32 v34, 10, v32
	global_store_short v[0:1], v2, off offset:64
	v_lshlrev_b64 v[0:1], 11, v[34:35]
	v_fma_mixlo_f16 v2, v6, v177, 0
	v_lshl_add_u64 v[0:1], v[36:37], 0, v[0:1]
	global_store_short v[0:1], v2, off
	v_fma_mixlo_f16 v2, v22, v177, 0
	v_or_b32_e32 v34, 11, v32
	global_store_short v[0:1], v2, off offset:64
	v_lshlrev_b64 v[0:1], 11, v[34:35]
	v_fma_mixlo_f16 v2, v7, v176, 0
	v_lshl_add_u64 v[0:1], v[36:37], 0, v[0:1]
	global_store_short v[0:1], v2, off
	v_fma_mixlo_f16 v2, v23, v176, 0
	v_or_b32_e32 v34, 16, v32
	global_store_short v[0:1], v2, off offset:64
	v_lshlrev_b64 v[0:1], 11, v[34:35]
	v_fma_mixlo_f16 v2, v8, v175, 0
	v_lshl_add_u64 v[0:1], v[36:37], 0, v[0:1]
	global_store_short v[0:1], v2, off
	v_fma_mixlo_f16 v2, v24, v175, 0
	v_or_b32_e32 v34, 17, v32
	global_store_short v[0:1], v2, off offset:64
	v_lshlrev_b64 v[0:1], 11, v[34:35]
	v_fma_mixlo_f16 v2, v9, v174, 0
	v_lshl_add_u64 v[0:1], v[36:37], 0, v[0:1]
	global_store_short v[0:1], v2, off
	v_fma_mixlo_f16 v2, v25, v174, 0
	v_or_b32_e32 v34, 18, v32
	global_store_short v[0:1], v2, off offset:64
	v_lshlrev_b64 v[0:1], 11, v[34:35]
	v_fma_mixlo_f16 v2, v10, v173, 0
	v_lshl_add_u64 v[0:1], v[36:37], 0, v[0:1]
	global_store_short v[0:1], v2, off
	v_fma_mixlo_f16 v2, v26, v173, 0
	v_or_b32_e32 v34, 19, v32
	global_store_short v[0:1], v2, off offset:64
	v_lshlrev_b64 v[0:1], 11, v[34:35]
	v_fma_mixlo_f16 v2, v11, v172, 0
	v_lshl_add_u64 v[0:1], v[36:37], 0, v[0:1]
	global_store_short v[0:1], v2, off
	v_fma_mixlo_f16 v2, v27, v172, 0
	v_or_b32_e32 v34, 24, v32
	global_store_short v[0:1], v2, off offset:64
	v_lshlrev_b64 v[0:1], 11, v[34:35]
	v_fma_mixlo_f16 v2, v12, v171, 0
	v_lshl_add_u64 v[0:1], v[36:37], 0, v[0:1]
	global_store_short v[0:1], v2, off
	v_fma_mixlo_f16 v2, v28, v171, 0
	v_or_b32_e32 v34, 25, v32
	global_store_short v[0:1], v2, off offset:64
	v_lshlrev_b64 v[0:1], 11, v[34:35]
	v_fma_mixlo_f16 v2, v13, v170, 0
	v_lshl_add_u64 v[0:1], v[36:37], 0, v[0:1]
	global_store_short v[0:1], v2, off
	v_fma_mixlo_f16 v2, v29, v170, 0
	v_or_b32_e32 v34, 26, v32
	global_store_short v[0:1], v2, off offset:64
	v_lshlrev_b64 v[0:1], 11, v[34:35]
	v_fma_mixlo_f16 v2, v14, v169, 0
	v_lshl_add_u64 v[0:1], v[36:37], 0, v[0:1]
	global_store_short v[0:1], v2, off
	v_fma_mixlo_f16 v2, v30, v169, 0
	v_or_b32_e32 v34, 27, v32
	global_store_short v[0:1], v2, off offset:64
	v_lshlrev_b64 v[0:1], 11, v[34:35]
	v_fma_mixlo_f16 v2, v15, v168, 0
	v_lshl_add_u64 v[0:1], v[36:37], 0, v[0:1]
	global_store_short v[0:1], v2, off
	v_fma_mixlo_f16 v2, v31, v168, 0
	global_store_short v[0:1], v2, off offset:64
	s_endpgm
	.p2alignl 8, 3212836864
